# speedup vs baseline: 1.0103x; 1.0103x over previous
_Z10qkv_kernelPKfPK15HIP_vector_typeIjLj4EEPDv8_DF16_S6_S6_:
	s_load_dwordx8 s[4:11], s[0:1], 0x0
	s_ashr_i32 s3, s2, 2
	s_and_b32 s3, s3, -8
	s_and_b32 s12, s2, 7
	s_bfe_u32 s2, s2, 0x20003
	s_or_b32 s12, s3, s12
	s_mul_i32 s3, s2, 0x36000
	s_waitcnt lgkmcnt(0)
	s_add_u32 s6, s6, s3
	v_mov_b32_e32 v211, 0
	s_addc_u32 s7, s7, 0
	s_mov_b64 s[22:23], s[6:7]
	v_lshlrev_b32_e32 v208, 4, v0
	v_mov_b32_e32 v209, v211
	v_lshl_add_u64 v[2:3], s[6:7], 0, v[208:209]
	s_movk_i32 s3, 0x2000
	v_add_co_u32_e32 v4, vcc, s3, v2
	v_lshrrev_b32_e32 v214, 6, v0
	s_nop 0
	v_addc_co_u32_e32 v5, vcc, 0, v3, vcc
	s_movk_i32 s3, 0x4000
	v_add_co_u32_e32 v6, vcc, s3, v2
	v_lshlrev_b32_e32 v1, 5, v214
	global_load_dwordx4 v[16:19], v208, s[6:7]
	v_addc_co_u32_e32 v7, vcc, 0, v3, vcc
	global_load_dwordx4 v[20:23], v[4:5], off
	global_load_dwordx4 v[24:27], v[6:7], off
	s_add_u32 s20, s6, 0x6000
	s_addc_u32 s21, s7, 0
	v_add_u32_e32 v172, 0x2000, v208
	v_add_u32_e32 v173, 0x4000, v208
	global_load_dwordx4 v[160:163], v208, s[20:21]
	global_load_dwordx4 v[164:167], v172, s[20:21]
	global_load_dwordx4 v[168:171], v173, s[20:21]
	v_lshl_or_b32 v1, s12, 8, v1
	s_movk_i32 s6, 0x600
	v_mov_b64_e32 v[4:5], s[4:5]
	v_mad_i64_i32 v[72:73], s[4:5], v1, s6, v[4:5]
	v_bfe_u32 v1, v0, 4, 2
	v_and_b32_e32 v80, 15, v0
	v_lshlrev_b32_e32 v210, 4, v80
	v_mul_u32_u24_e32 v4, 0x180, v1
	v_lshl_add_u64 v[40:41], v[72:73], 0, v[210:211]
	v_lshlrev_b32_e32 v48, 2, v4
	v_mov_b32_e32 v49, v211
	v_lshl_add_u64 v[12:13], v[40:41], 0, v[48:49]
	s_movk_i32 s4, 0x1000
	v_add_co_u32_e32 v14, vcc, s4, v12
	s_movk_i32 s4, 0x3000
	s_nop 0
	v_addc_co_u32_e32 v15, vcc, 0, v13, vcc
	v_add_co_u32_e32 v32, vcc, s4, v12
	global_load_dwordx4 v[4:7], v[12:13], off nt
	global_load_dwordx4 v[8:11], v[14:15], off offset:2048 nt
	v_addc_co_u32_e32 v33, vcc, 0, v13, vcc
	v_add_co_u32_e32 v34, vcc, s3, v12
	v_or_b32_e32 v64, 0x6000, v48
	v_mov_b32_e32 v65, v211
	v_addc_co_u32_e32 v35, vcc, 0, v13, vcc
	global_load_dwordx4 v[12:15], v[32:33], off nt
	global_load_dwordx4 v[28:31], v[34:35], off offset:2048 nt
	v_lshl_add_u64 v[42:43], v[40:41], 0, v[64:65]
	v_add_u32_e32 v66, 0x7800, v48
	v_mov_b32_e32 v67, v211
	v_add_u32_e32 v74, 0x9000, v48
	v_mov_b32_e32 v75, v211
	v_lshl_add_u64 v[44:45], v[40:41], 0, v[66:67]
	global_load_dwordx4 v[32:35], v[42:43], off nt
	global_load_dwordx4 v[36:39], v[44:45], off nt
	v_lshl_add_u64 v[50:51], v[40:41], 0, v[74:75]
	v_add_u32_e32 v76, 0xa800, v48
	v_mov_b32_e32 v77, v211
	v_lshl_add_u64 v[52:53], v[40:41], 0, v[76:77]
	global_load_dwordx4 v[40:43], v[50:51], off nt
	global_load_dwordx4 v[44:47], v[52:53], off nt
	v_lshl_add_u64 v[48:49], v[72:73], 0, v[48:49]
	v_lshl_add_u64 v[140:141], v[48:49], 0, v[210:211]
	s_mov_b64 s[4:5], 0x1800
	v_lshl_add_u64 v[142:143], v[140:141], 0, s[4:5]
	s_mov_b64 s[4:5], 0x3000
	v_lshl_add_u64 v[64:65], v[72:73], 0, v[64:65]
	v_lshl_add_u64 v[74:75], v[72:73], 0, v[74:75]
	v_lshl_add_u64 v[144:145], v[140:141], 0, s[4:5]
	s_mov_b64 s[4:5], 0x4800
	v_lshl_add_u64 v[148:149], v[64:65], 0, v[210:211]
	v_lshl_add_u64 v[64:65], v[72:73], 0, v[66:67]
	v_lshl_add_u64 v[152:153], v[74:75], 0, v[210:211]
	v_lshl_add_u64 v[72:73], v[72:73], 0, v[76:77]
	global_load_dwordx4 v[48:51], v[140:141], off offset:256 nt
	global_load_dwordx4 v[52:55], v[142:143], off offset:256 nt
	v_lshl_add_u64 v[146:147], v[140:141], 0, s[4:5]
	global_load_dwordx4 v[56:59], v[144:145], off offset:256 nt
	global_load_dwordx4 v[60:63], v[146:147], off offset:256 nt
	v_lshl_add_u64 v[150:151], v[64:65], 0, v[210:211]
	global_load_dwordx4 v[64:67], v[148:149], off offset:256 nt
	global_load_dwordx4 v[68:71], v[150:151], off offset:256 nt
	v_lshl_add_u64 v[154:155], v[72:73], 0, v[210:211]
	global_load_dwordx4 v[72:75], v[152:153], off offset:256 nt
	global_load_dwordx4 v[76:79], v[154:155], off offset:256 nt
	v_mul_u32_u24_e32 v82, 0x1200, v214
	v_lshl_or_b32 v80, v80, 3, v82
	s_movk_i32 s3, 0x90
	v_mad_u32_u24 v1, v1, s3, v80
	v_add_u32_e32 v157, 0xc000, v1
	v_and_b32_e32 v81, 31, v0
	v_lshrrev_b32_e32 v83, 1, v0
	v_add_u32_e32 v1, 0xc800, v1
	v_mul_u32_u24_e32 v81, 0x90, v81
	v_and_b32_e32 v83, 16, v83
	v_add3_u32 v156, v82, v81, v83
	s_load_dwordx2 s[0:1], s[0:1], 0x20
	s_mov_b32 s3, 0
	v_and_b32_e32 v0, 63, v0
	s_waitcnt vmcnt(15)
	v_cvt_pk_f16_f32 v7, v6, v7
	v_cvt_pk_f16_f32 v6, v4, v5
	s_waitcnt vmcnt(14)
	v_cvt_pk_f16_f32 v5, v10, v11
	v_cvt_pk_f16_f32 v4, v8, v9
	ds_write2_b64 v157, v[6:7], v[4:5] offset1:72
	s_waitcnt vmcnt(13)
	v_cvt_pk_f16_f32 v5, v14, v15
	v_cvt_pk_f16_f32 v4, v12, v13
	s_waitcnt vmcnt(12)
	v_cvt_pk_f16_f32 v7, v30, v31
	v_cvt_pk_f16_f32 v6, v28, v29
	ds_write2_b64 v157, v[4:5], v[6:7] offset0:144 offset1:216
	s_waitcnt vmcnt(11)
	v_cvt_pk_f16_f32 v5, v34, v35
	v_cvt_pk_f16_f32 v4, v32, v33
	s_waitcnt vmcnt(10)
	v_cvt_pk_f16_f32 v7, v38, v39
	v_cvt_pk_f16_f32 v6, v36, v37
	ds_write2_b64 v1, v[4:5], v[6:7] offset0:32 offset1:104
	s_waitcnt vmcnt(9)
	v_cvt_pk_f16_f32 v5, v42, v43
	v_cvt_pk_f16_f32 v4, v40, v41
	s_waitcnt vmcnt(8)
	v_cvt_pk_f16_f32 v7, v46, v47
	v_cvt_pk_f16_f32 v6, v44, v45
	ds_write2_b64 v1, v[4:5], v[6:7] offset0:176 offset1:248
	ds_read_b128 v[28:31], v156 offset:49152
	ds_read_b128 v[32:35], v156 offset:49184
	ds_read_b128 v[36:39], v156 offset:49216
	ds_read_b128 v[40:43], v156 offset:49248
	global_load_dwordx4 v[4:7], v[140:141], off offset:512 nt
	global_load_dwordx4 v[8:11], v[142:143], off offset:512 nt
	global_load_dwordx4 v[12:15], v[144:145], off offset:512 nt
	global_load_dwordx4 v[80:83], v[146:147], off offset:512 nt
	global_load_dwordx4 v[84:87], v[148:149], off offset:512 nt
	global_load_dwordx4 v[88:91], v[150:151], off offset:512 nt
	global_load_dwordx4 v[92:95], v[152:153], off offset:512 nt
	global_load_dwordx4 v[96:99], v[154:155], off offset:512 nt
	s_waitcnt vmcnt(15)
	v_cvt_pk_f16_f32 v45, v50, v51
	v_cvt_pk_f16_f32 v44, v48, v49
	s_waitcnt vmcnt(14)
	v_cvt_pk_f16_f32 v47, v54, v55
	v_cvt_pk_f16_f32 v46, v52, v53
	ds_write2_b64 v157, v[44:45], v[46:47] offset1:72
	s_waitcnt vmcnt(13)
	v_cvt_pk_f16_f32 v45, v58, v59
	v_cvt_pk_f16_f32 v44, v56, v57
	s_waitcnt vmcnt(12)
	v_cvt_pk_f16_f32 v47, v62, v63
	v_cvt_pk_f16_f32 v46, v60, v61
	ds_write2_b64 v157, v[44:45], v[46:47] offset0:144 offset1:216
	s_waitcnt vmcnt(11)
	v_cvt_pk_f16_f32 v45, v66, v67
	v_cvt_pk_f16_f32 v44, v64, v65
	s_waitcnt vmcnt(10)
	v_cvt_pk_f16_f32 v47, v70, v71
	v_cvt_pk_f16_f32 v46, v68, v69
	ds_write2_b64 v1, v[44:45], v[46:47] offset0:32 offset1:104
	s_waitcnt vmcnt(9)
	v_cvt_pk_f16_f32 v45, v74, v75
	v_cvt_pk_f16_f32 v44, v72, v73
	s_waitcnt vmcnt(8)
	v_cvt_pk_f16_f32 v47, v78, v79
	v_cvt_pk_f16_f32 v46, v76, v77
	ds_write2_b64 v1, v[44:45], v[46:47] offset0:176 offset1:248
	ds_read_b128 v[44:47], v156 offset:49152
	ds_read_b128 v[48:51], v156 offset:49184
	ds_read_b128 v[52:55], v156 offset:49216
	ds_read_b128 v[56:59], v156 offset:49248
	global_load_dwordx4 v[76:79], v[140:141], off offset:768 nt
	global_load_dwordx4 v[100:103], v[142:143], off offset:768 nt
	global_load_dwordx4 v[104:107], v[144:145], off offset:768 nt
	global_load_dwordx4 v[108:111], v[146:147], off offset:768 nt
	global_load_dwordx4 v[112:115], v[148:149], off offset:768 nt
	global_load_dwordx4 v[116:119], v[150:151], off offset:768 nt
	global_load_dwordx4 v[120:123], v[152:153], off offset:768 nt
	global_load_dwordx4 v[124:127], v[154:155], off offset:768 nt
	s_waitcnt vmcnt(15)
	v_cvt_pk_f16_f32 v7, v6, v7
	v_cvt_pk_f16_f32 v6, v4, v5
	s_waitcnt vmcnt(14)
	v_cvt_pk_f16_f32 v5, v10, v11
	v_cvt_pk_f16_f32 v4, v8, v9
	ds_write2_b64 v157, v[6:7], v[4:5] offset1:72
	s_waitcnt vmcnt(13)
	v_cvt_pk_f16_f32 v5, v14, v15
	v_cvt_pk_f16_f32 v4, v12, v13
	s_waitcnt vmcnt(12)
	v_cvt_pk_f16_f32 v7, v82, v83
	v_cvt_pk_f16_f32 v6, v80, v81
	ds_write2_b64 v157, v[4:5], v[6:7] offset0:144 offset1:216
	s_waitcnt vmcnt(11)
	v_cvt_pk_f16_f32 v5, v86, v87
	v_cvt_pk_f16_f32 v4, v84, v85
	s_waitcnt vmcnt(10)
	v_cvt_pk_f16_f32 v7, v90, v91
	v_cvt_pk_f16_f32 v6, v88, v89
	ds_write2_b64 v1, v[4:5], v[6:7] offset0:32 offset1:104
	s_waitcnt vmcnt(9)
	v_cvt_pk_f16_f32 v5, v94, v95
	v_cvt_pk_f16_f32 v4, v92, v93
	s_waitcnt vmcnt(8)
	v_cvt_pk_f16_f32 v7, v98, v99
	v_cvt_pk_f16_f32 v6, v96, v97
	ds_write2_b64 v1, v[4:5], v[6:7] offset0:176 offset1:248
	ds_read_b128 v[60:63], v156 offset:49152
	ds_read_b128 v[64:67], v156 offset:49184
	ds_read_b128 v[68:71], v156 offset:49216
	ds_read_b128 v[72:75], v156 offset:49248
	global_load_dwordx4 v[4:7], v[140:141], off offset:1024 nt
	global_load_dwordx4 v[8:11], v[142:143], off offset:1024 nt
	global_load_dwordx4 v[12:15], v[144:145], off offset:1024 nt
	global_load_dwordx4 v[92:95], v[146:147], off offset:1024 nt
	global_load_dwordx4 v[96:99], v[148:149], off offset:1024 nt
	global_load_dwordx4 v[128:131], v[150:151], off offset:1024 nt
	global_load_dwordx4 v[132:135], v[152:153], off offset:1024 nt
	global_load_dwordx4 v[136:139], v[154:155], off offset:1024 nt
	s_waitcnt vmcnt(15)
	v_cvt_pk_f16_f32 v79, v78, v79
	v_cvt_pk_f16_f32 v78, v76, v77
	s_waitcnt vmcnt(14)
	v_cvt_pk_f16_f32 v77, v102, v103
	v_cvt_pk_f16_f32 v76, v100, v101
	ds_write2_b64 v157, v[78:79], v[76:77] offset1:72
	s_waitcnt vmcnt(13)
	v_cvt_pk_f16_f32 v77, v106, v107
	v_cvt_pk_f16_f32 v76, v104, v105
	s_waitcnt vmcnt(12)
	v_cvt_pk_f16_f32 v79, v110, v111
	v_cvt_pk_f16_f32 v78, v108, v109
	ds_write2_b64 v157, v[76:77], v[78:79] offset0:144 offset1:216
	s_waitcnt vmcnt(11)
	v_cvt_pk_f16_f32 v77, v114, v115
	v_cvt_pk_f16_f32 v76, v112, v113
	s_waitcnt vmcnt(10)
	v_cvt_pk_f16_f32 v79, v118, v119
	v_cvt_pk_f16_f32 v78, v116, v117
	ds_write2_b64 v1, v[76:77], v[78:79] offset0:32 offset1:104
	s_waitcnt vmcnt(9)
	v_cvt_pk_f16_f32 v77, v122, v123
	v_cvt_pk_f16_f32 v76, v120, v121
	s_waitcnt vmcnt(8)
	v_cvt_pk_f16_f32 v79, v126, v127
	v_cvt_pk_f16_f32 v78, v124, v125
	ds_write2_b64 v1, v[76:77], v[78:79] offset0:176 offset1:248
	ds_read_b128 v[76:79], v156 offset:49152
	ds_read_b128 v[80:83], v156 offset:49184
	ds_read_b128 v[84:87], v156 offset:49216
	ds_read_b128 v[88:91], v156 offset:49248
	global_load_dwordx4 v[108:111], v[140:141], off offset:1280 nt
	global_load_dwordx4 v[112:115], v[142:143], off offset:1280 nt
	global_load_dwordx4 v[116:119], v[144:145], off offset:1280 nt
	global_load_dwordx4 v[120:123], v[146:147], off offset:1280 nt
	global_load_dwordx4 v[124:127], v[148:149], off offset:1280 nt
	s_nop 0
	global_load_dwordx4 v[140:143], v[150:151], off offset:1280 nt
	global_load_dwordx4 v[144:147], v[152:153], off offset:1280 nt
	s_nop 0
	global_load_dwordx4 v[148:151], v[154:155], off offset:1280 nt
	s_waitcnt vmcnt(15)
	v_cvt_pk_f16_f32 v7, v6, v7
	v_cvt_pk_f16_f32 v6, v4, v5
	s_waitcnt vmcnt(14)
	v_cvt_pk_f16_f32 v5, v10, v11
	v_cvt_pk_f16_f32 v4, v8, v9
	ds_write2_b64 v157, v[6:7], v[4:5] offset1:72
	s_waitcnt vmcnt(13)
	v_cvt_pk_f16_f32 v5, v14, v15
	v_cvt_pk_f16_f32 v4, v12, v13
	s_waitcnt vmcnt(12)
	v_cvt_pk_f16_f32 v7, v94, v95
	v_cvt_pk_f16_f32 v6, v92, v93
	ds_write2_b64 v157, v[4:5], v[6:7] offset0:144 offset1:216
	s_waitcnt vmcnt(11)
	v_cvt_pk_f16_f32 v5, v98, v99
	v_cvt_pk_f16_f32 v4, v96, v97
	s_waitcnt vmcnt(10)
	v_cvt_pk_f16_f32 v7, v130, v131
	v_cvt_pk_f16_f32 v6, v128, v129
	ds_write2_b64 v1, v[4:5], v[6:7] offset0:32 offset1:104
	s_waitcnt vmcnt(9)
	v_cvt_pk_f16_f32 v5, v134, v135
	v_cvt_pk_f16_f32 v4, v132, v133
	s_waitcnt vmcnt(8)
	v_cvt_pk_f16_f32 v7, v138, v139
	v_cvt_pk_f16_f32 v6, v136, v137
	ds_write2_b64 v1, v[4:5], v[6:7] offset0:176 offset1:248
	ds_read_b128 v[92:95], v156 offset:49152
	ds_read_b128 v[96:99], v156 offset:49184
	ds_read_b128 v[100:103], v156 offset:49216
	ds_read_b128 v[104:107], v156 offset:49248
	s_waitcnt vmcnt(7)
	v_cvt_pk_f16_f32 v5, v110, v111
	v_cvt_pk_f16_f32 v4, v108, v109
	s_waitcnt vmcnt(6)
	v_cvt_pk_f16_f32 v7, v114, v115
	v_cvt_pk_f16_f32 v6, v112, v113
	ds_write2_b64 v157, v[4:5], v[6:7] offset1:72
	s_waitcnt vmcnt(5)
	v_cvt_pk_f16_f32 v5, v118, v119
	v_cvt_pk_f16_f32 v4, v116, v117
	s_waitcnt vmcnt(4)
	v_cvt_pk_f16_f32 v7, v122, v123
	v_cvt_pk_f16_f32 v6, v120, v121
	ds_write2_b64 v157, v[4:5], v[6:7] offset0:144 offset1:216
	s_waitcnt vmcnt(3)
	v_cvt_pk_f16_f32 v5, v126, v127
	v_cvt_pk_f16_f32 v4, v124, v125
	s_waitcnt vmcnt(2)
	v_cvt_pk_f16_f32 v7, v142, v143
	v_cvt_pk_f16_f32 v6, v140, v141
	ds_write2_b64 v1, v[4:5], v[6:7] offset0:32 offset1:104
	s_waitcnt vmcnt(1)
	v_cvt_pk_f16_f32 v5, v146, v147
	v_cvt_pk_f16_f32 v4, v144, v145
	s_waitcnt vmcnt(0)
	v_cvt_pk_f16_f32 v7, v150, v151
	v_cvt_pk_f16_f32 v6, v148, v149
	ds_write2_b64 v1, v[4:5], v[6:7] offset0:176 offset1:248
	ds_read_b128 v[108:111], v156 offset:49152
	ds_read_b128 v[112:115], v156 offset:49184
	ds_read_b128 v[116:119], v156 offset:49216
	ds_read_b128 v[120:123], v156 offset:49248
	s_mul_i32 s14, s2, 9
	s_mul_i32 s15, s12, 6
	v_mov_b32_e32 v236, v208
	v_mov_b32_e32 v237, v172
	v_mov_b32_e32 v238, v173
	v_lshlrev_b32_e32 v239, 4, v0
	v_add_u32_e32 v240, 0xc000, v239
	v_lshlrev_b32_e32 v241, 12, v214
	v_or_b32_e32 v241, v241, v239
	s_waitcnt vmcnt(0) lgkmcnt(0)
	ds_write_b128 v236, v[16:19]
	ds_write_b128 v237, v[20:23]
	ds_write_b128 v238, v[24:27]
	ds_write_b128 v236, v[160:163] offset:24576
	ds_write_b128 v237, v[164:167] offset:24576
	ds_write_b128 v238, v[168:171] offset:24576
	s_waitcnt lgkmcnt(0)
	s_barrier
	s_cmp_lt_u32 s2, 2
	s_cbranch_scc1 .Lqkv_bodyS
	s_cmp_eq_u32 s2, 3
	s_cbranch_scc1 .Lqkv_bodyN
.Lqkv_bodyM:
	ds_read_b128 v[124:127], v239 offset:0
	ds_read_b128 v[128:131], v239 offset:1024
	ds_read_b128 v[132:135], v239 offset:2048
	ds_read_b128 v[136:139], v239 offset:3072
	ds_read_b128 v[140:143], v239 offset:4096
	ds_read_b128 v[144:147], v239 offset:5120
	ds_read_b128 v[148:151], v239 offset:6144
	ds_read_b128 v[152:155], v239 offset:7168
	ds_read_b128 v[156:159], v239 offset:8192
	ds_read_b128 v[160:163], v239 offset:9216
	ds_read_b128 v[164:167], v239 offset:10240
	ds_read_b128 v[168:171], v239 offset:11264
	ds_read_b128 v[172:175], v239 offset:12288
	ds_read_b128 v[176:179], v239 offset:13312
	ds_read_b128 v[180:183], v239 offset:14336
	ds_read_b128 v[184:187], v239 offset:15360
	ds_read_b128 v[188:191], v239 offset:16384
	ds_read_b128 v[192:195], v239 offset:17408
	ds_read_b128 v[196:199], v239 offset:18432
	ds_read_b128 v[200:203], v239 offset:19456
	ds_read_b128 v[204:207], v239 offset:20480
	ds_read_b128 v[208:211], v239 offset:21504
	ds_read_b128 v[212:215], v239 offset:22528
	ds_read_b128 v[216:219], v239 offset:23552
	s_add_u32 s24, s22, 49152
	s_addc_u32 s25, s23, 0
	s_waitcnt lgkmcnt(14)
	v_mfma_f32_32x32x16_f16 v[0:15], v[124:127], v[28:31], 0
	ds_read_b128 v[124:127], v239 offset:24576
	global_load_dwordx4 v[16:19], v236, s[24:25]
	global_load_dwordx4 v[20:23], v237, s[24:25]
	global_load_dwordx4 v[24:27], v238, s[24:25]
	s_waitcnt lgkmcnt(14)
	v_mfma_f32_32x32x16_f16 v[0:15], v[128:131], v[32:35], v[0:15]
	ds_read_b128 v[128:131], v239 offset:25600
	s_waitcnt lgkmcnt(14)
	v_mfma_f32_32x32x16_f16 v[0:15], v[132:135], v[36:39], v[0:15]
	ds_read_b128 v[132:135], v239 offset:26624
	s_waitcnt lgkmcnt(14)
	v_mfma_f32_32x32x16_f16 v[0:15], v[136:139], v[40:43], v[0:15]
	ds_read_b128 v[136:139], v239 offset:27648
	s_waitcnt lgkmcnt(14)
	v_mfma_f32_32x32x16_f16 v[0:15], v[140:143], v[44:47], v[0:15]
	ds_read_b128 v[140:143], v239 offset:28672
	s_waitcnt lgkmcnt(14)
	v_mfma_f32_32x32x16_f16 v[0:15], v[144:147], v[48:51], v[0:15]
	ds_read_b128 v[144:147], v239 offset:29696
	s_waitcnt lgkmcnt(14)
	v_mfma_f32_32x32x16_f16 v[0:15], v[148:151], v[52:55], v[0:15]
	ds_read_b128 v[148:151], v239 offset:30720
	s_waitcnt lgkmcnt(14)
	v_mfma_f32_32x32x16_f16 v[0:15], v[152:155], v[56:59], v[0:15]
	ds_read_b128 v[152:155], v239 offset:31744
	s_waitcnt lgkmcnt(14)
	v_mfma_f32_32x32x16_f16 v[0:15], v[156:159], v[60:63], v[0:15]
	ds_read_b128 v[156:159], v239 offset:32768
	s_waitcnt lgkmcnt(14)
	v_mfma_f32_32x32x16_f16 v[0:15], v[160:163], v[64:67], v[0:15]
	ds_read_b128 v[160:163], v239 offset:33792
	s_waitcnt lgkmcnt(14)
	v_mfma_f32_32x32x16_f16 v[0:15], v[164:167], v[68:71], v[0:15]
	ds_read_b128 v[164:167], v239 offset:34816
	s_waitcnt lgkmcnt(14)
	v_mfma_f32_32x32x16_f16 v[0:15], v[168:171], v[72:75], v[0:15]
	ds_read_b128 v[168:171], v239 offset:35840
	s_waitcnt lgkmcnt(14)
	v_mfma_f32_32x32x16_f16 v[0:15], v[172:175], v[76:79], v[0:15]
	ds_read_b128 v[172:175], v239 offset:36864
	s_waitcnt lgkmcnt(14)
	v_mfma_f32_32x32x16_f16 v[0:15], v[176:179], v[80:83], v[0:15]
	ds_read_b128 v[176:179], v239 offset:37888
	s_waitcnt lgkmcnt(14)
	v_mfma_f32_32x32x16_f16 v[0:15], v[180:183], v[84:87], v[0:15]
	ds_read_b128 v[180:183], v239 offset:38912
	s_waitcnt lgkmcnt(14)
	v_mfma_f32_32x32x16_f16 v[0:15], v[184:187], v[88:91], v[0:15]
	ds_read_b128 v[184:187], v239 offset:39936
	s_waitcnt lgkmcnt(14)
	v_mfma_f32_32x32x16_f16 v[0:15], v[188:191], v[92:95], v[0:15]
	ds_read_b128 v[188:191], v239 offset:40960
	s_waitcnt lgkmcnt(14)
	v_mfma_f32_32x32x16_f16 v[0:15], v[192:195], v[96:99], v[0:15]
	ds_read_b128 v[192:195], v239 offset:41984
	s_waitcnt lgkmcnt(14)
	v_mfma_f32_32x32x16_f16 v[0:15], v[196:199], v[100:103], v[0:15]
	ds_read_b128 v[196:199], v239 offset:43008
	s_waitcnt vmcnt(0)
	ds_write_b128 v236, v[16:19] offset:49152
	ds_write_b128 v237, v[20:23] offset:49152
	ds_write_b128 v238, v[24:27] offset:49152
	s_waitcnt lgkmcnt(14)
	v_mfma_f32_32x32x16_f16 v[0:15], v[200:203], v[104:107], v[0:15]
	ds_read_b128 v[200:203], v239 offset:44032
	s_waitcnt lgkmcnt(14)
	v_mfma_f32_32x32x16_f16 v[0:15], v[204:207], v[108:111], v[0:15]
	ds_read_b128 v[204:207], v239 offset:45056
	s_waitcnt lgkmcnt(14)
	v_mfma_f32_32x32x16_f16 v[0:15], v[208:211], v[112:115], v[0:15]
	ds_read_b128 v[208:211], v239 offset:46080
	s_waitcnt lgkmcnt(14)
	v_mfma_f32_32x32x16_f16 v[0:15], v[212:215], v[116:119], v[0:15]
	ds_read_b128 v[212:215], v239 offset:47104
	s_waitcnt lgkmcnt(14)
	v_mfma_f32_32x32x16_f16 v[0:15], v[216:219], v[120:123], v[0:15]
	ds_read_b128 v[216:219], v239 offset:48128
	s_waitcnt lgkmcnt(5)
	s_barrier
	s_add_u32 s24, s22, 73728
	s_addc_u32 s25, s23, 0
	s_waitcnt lgkmcnt(14)
	v_mfma_f32_32x32x16_f16 v[220:235], v[124:127], v[28:31], 0
	ds_read_b128 v[124:127], v240 offset:0
	global_load_dwordx4 v[16:19], v236, s[24:25]
	global_load_dwordx4 v[20:23], v237, s[24:25]
	global_load_dwordx4 v[24:27], v238, s[24:25]
	s_waitcnt lgkmcnt(14)
	v_mfma_f32_32x32x16_f16 v[220:235], v[128:131], v[32:35], v[220:235]
	ds_read_b128 v[128:131], v240 offset:1024
	s_add_i32 s20, s14, 0
	s_cmp_lt_u32 s20, 12
	s_cselect_b32 s26, s8, s10
	s_cselect_b32 s27, s9, s11
	s_waitcnt lgkmcnt(14)
	v_mfma_f32_32x32x16_f16 v[220:235], v[132:135], v[36:39], v[220:235]
	ds_read_b128 v[132:135], v240 offset:2048
	s_cselect_b32 s21, 0, 12
	s_cmp_lt_u32 s20, 24
	s_cselect_b32 s26, s26, s0
	s_cselect_b32 s27, s27, s1
	s_waitcnt lgkmcnt(14)
	v_mfma_f32_32x32x16_f16 v[220:235], v[136:139], v[40:43], v[220:235]
	ds_read_b128 v[136:139], v240 offset:3072
	s_cselect_b32 s21, s21, 24
	s_sub_i32 s20, s20, s21
	s_lshr_b32 s21, s20, 1
	s_and_b32 s20, s20, 1
	s_waitcnt lgkmcnt(14)
	v_mfma_f32_32x32x16_f16 v[220:235], v[140:143], v[44:47], v[220:235]
	ds_read_b128 v[140:143], v240 offset:4096
	s_add_i32 s21, s21, s15
	s_lshl_b32 s21, s21, 15
	s_lshl_b32 s20, s20, 11
	s_add_i32 s21, s21, s20
	s_waitcnt lgkmcnt(14)
	v_mfma_f32_32x32x16_f16 v[220:235], v[144:147], v[48:51], v[220:235]
	ds_read_b128 v[144:147], v240 offset:5120
	s_add_u32 s26, s26, s21
	s_addc_u32 s27, s27, 0
	s_waitcnt lgkmcnt(14)
	v_mfma_f32_32x32x16_f16 v[220:235], v[148:151], v[52:55], v[220:235]
	ds_read_b128 v[148:151], v240 offset:6144
	v_cvt_pk_f16_f32 v244, v0, v1
	v_cvt_pk_f16_f32 v245, v2, v3
	s_waitcnt lgkmcnt(14)
	v_mfma_f32_32x32x16_f16 v[220:235], v[152:155], v[56:59], v[220:235]
	ds_read_b128 v[152:155], v240 offset:7168
	v_cvt_pk_f16_f32 v246, v4, v5
	v_cvt_pk_f16_f32 v247, v6, v7
	s_waitcnt lgkmcnt(14)
	v_mfma_f32_32x32x16_f16 v[220:235], v[156:159], v[60:63], v[220:235]
	ds_read_b128 v[156:159], v240 offset:8192
	v_cvt_pk_f16_f32 v248, v8, v9
	v_cvt_pk_f16_f32 v249, v10, v11
	s_waitcnt lgkmcnt(14)
	v_mfma_f32_32x32x16_f16 v[220:235], v[160:163], v[64:67], v[220:235]
	ds_read_b128 v[160:163], v240 offset:9216
	v_cvt_pk_f16_f32 v250, v12, v13
	v_cvt_pk_f16_f32 v251, v14, v15
	s_waitcnt lgkmcnt(14)
	v_mfma_f32_32x32x16_f16 v[220:235], v[164:167], v[68:71], v[220:235]
	ds_read_b128 v[164:167], v240 offset:10240
	global_store_dwordx4 v241, v[244:247], s[26:27] nt
	s_waitcnt lgkmcnt(14)
	v_mfma_f32_32x32x16_f16 v[220:235], v[168:171], v[72:75], v[220:235]
	ds_read_b128 v[168:171], v240 offset:11264
	global_store_dwordx4 v241, v[248:251], s[26:27] offset:1024 nt
	s_waitcnt lgkmcnt(14)
	v_mfma_f32_32x32x16_f16 v[220:235], v[172:175], v[76:79], v[220:235]
	ds_read_b128 v[172:175], v240 offset:12288
	s_waitcnt lgkmcnt(14)
	v_mfma_f32_32x32x16_f16 v[220:235], v[176:179], v[80:83], v[220:235]
	ds_read_b128 v[176:179], v240 offset:13312
	s_waitcnt lgkmcnt(14)
	v_mfma_f32_32x32x16_f16 v[220:235], v[180:183], v[84:87], v[220:235]
	ds_read_b128 v[180:183], v240 offset:14336
	s_waitcnt lgkmcnt(14)
	v_mfma_f32_32x32x16_f16 v[220:235], v[184:187], v[88:91], v[220:235]
	ds_read_b128 v[184:187], v240 offset:15360
	s_waitcnt lgkmcnt(14)
	v_mfma_f32_32x32x16_f16 v[220:235], v[188:191], v[92:95], v[220:235]
	ds_read_b128 v[188:191], v240 offset:16384
	s_waitcnt lgkmcnt(14)
	v_mfma_f32_32x32x16_f16 v[220:235], v[192:195], v[96:99], v[220:235]
	ds_read_b128 v[192:195], v240 offset:17408
	s_waitcnt lgkmcnt(14)
	v_mfma_f32_32x32x16_f16 v[220:235], v[196:199], v[100:103], v[220:235]
	ds_read_b128 v[196:199], v240 offset:18432
	s_waitcnt vmcnt(2)
	ds_write_b128 v236, v[16:19] offset:0
	ds_write_b128 v237, v[20:23] offset:0
	ds_write_b128 v238, v[24:27] offset:0
	s_waitcnt lgkmcnt(14)
	v_mfma_f32_32x32x16_f16 v[220:235], v[200:203], v[104:107], v[220:235]
	ds_read_b128 v[200:203], v240 offset:19456
	s_waitcnt lgkmcnt(14)
	v_mfma_f32_32x32x16_f16 v[220:235], v[204:207], v[108:111], v[220:235]
	ds_read_b128 v[204:207], v240 offset:20480
	s_waitcnt lgkmcnt(14)
	v_mfma_f32_32x32x16_f16 v[220:235], v[208:211], v[112:115], v[220:235]
	ds_read_b128 v[208:211], v240 offset:21504
	s_waitcnt lgkmcnt(14)
	v_mfma_f32_32x32x16_f16 v[220:235], v[212:215], v[116:119], v[220:235]
	ds_read_b128 v[212:215], v240 offset:22528
	s_waitcnt lgkmcnt(14)
	v_mfma_f32_32x32x16_f16 v[220:235], v[216:219], v[120:123], v[220:235]
	ds_read_b128 v[216:219], v240 offset:23552
	s_waitcnt lgkmcnt(5)
	s_barrier
	s_add_u32 s24, s22, 98304
	s_addc_u32 s25, s23, 0
	s_waitcnt lgkmcnt(14)
	v_mfma_f32_32x32x16_f16 v[0:15], v[124:127], v[28:31], 0
	ds_read_b128 v[124:127], v239 offset:0
	global_load_dwordx4 v[16:19], v236, s[24:25]
	global_load_dwordx4 v[20:23], v237, s[24:25]
	global_load_dwordx4 v[24:27], v238, s[24:25]
	s_waitcnt lgkmcnt(14)
	v_mfma_f32_32x32x16_f16 v[0:15], v[128:131], v[32:35], v[0:15]
	ds_read_b128 v[128:131], v239 offset:1024
	s_add_i32 s20, s14, 1
	s_cmp_lt_u32 s20, 12
	s_cselect_b32 s26, s8, s10
	s_cselect_b32 s27, s9, s11
	s_waitcnt lgkmcnt(14)
	v_mfma_f32_32x32x16_f16 v[0:15], v[132:135], v[36:39], v[0:15]
	ds_read_b128 v[132:135], v239 offset:2048
	s_cselect_b32 s21, 0, 12
	s_cmp_lt_u32 s20, 24
	s_cselect_b32 s26, s26, s0
	s_cselect_b32 s27, s27, s1
	s_waitcnt lgkmcnt(14)
	v_mfma_f32_32x32x16_f16 v[0:15], v[136:139], v[40:43], v[0:15]
	ds_read_b128 v[136:139], v239 offset:3072
	s_cselect_b32 s21, s21, 24
	s_sub_i32 s20, s20, s21
	s_lshr_b32 s21, s20, 1
	s_and_b32 s20, s20, 1
	s_waitcnt lgkmcnt(14)
	v_mfma_f32_32x32x16_f16 v[0:15], v[140:143], v[44:47], v[0:15]
	ds_read_b128 v[140:143], v239 offset:4096
	s_add_i32 s21, s21, s15
	s_lshl_b32 s21, s21, 15
	s_lshl_b32 s20, s20, 11
	s_add_i32 s21, s21, s20
	s_waitcnt lgkmcnt(14)
	v_mfma_f32_32x32x16_f16 v[0:15], v[144:147], v[48:51], v[0:15]
	ds_read_b128 v[144:147], v239 offset:5120
	s_add_u32 s26, s26, s21
	s_addc_u32 s27, s27, 0
	s_waitcnt lgkmcnt(14)
	v_mfma_f32_32x32x16_f16 v[0:15], v[148:151], v[52:55], v[0:15]
	ds_read_b128 v[148:151], v239 offset:6144
	v_cvt_pk_f16_f32 v244, v220, v221
	v_cvt_pk_f16_f32 v245, v222, v223
	s_waitcnt lgkmcnt(14)
	v_mfma_f32_32x32x16_f16 v[0:15], v[152:155], v[56:59], v[0:15]
	ds_read_b128 v[152:155], v239 offset:7168
	v_cvt_pk_f16_f32 v246, v224, v225
	v_cvt_pk_f16_f32 v247, v226, v227
	s_waitcnt lgkmcnt(14)
	v_mfma_f32_32x32x16_f16 v[0:15], v[156:159], v[60:63], v[0:15]
	ds_read_b128 v[156:159], v239 offset:8192
	v_cvt_pk_f16_f32 v248, v228, v229
	v_cvt_pk_f16_f32 v249, v230, v231
	s_waitcnt lgkmcnt(14)
	v_mfma_f32_32x32x16_f16 v[0:15], v[160:163], v[64:67], v[0:15]
	ds_read_b128 v[160:163], v239 offset:9216
	v_cvt_pk_f16_f32 v250, v232, v233
	v_cvt_pk_f16_f32 v251, v234, v235
	s_waitcnt lgkmcnt(14)
	v_mfma_f32_32x32x16_f16 v[0:15], v[164:167], v[68:71], v[0:15]
	ds_read_b128 v[164:167], v239 offset:10240
	global_store_dwordx4 v241, v[244:247], s[26:27] nt
	s_waitcnt lgkmcnt(14)
	v_mfma_f32_32x32x16_f16 v[0:15], v[168:171], v[72:75], v[0:15]
	ds_read_b128 v[168:171], v239 offset:11264
	global_store_dwordx4 v241, v[248:251], s[26:27] offset:1024 nt
	s_waitcnt lgkmcnt(14)
	v_mfma_f32_32x32x16_f16 v[0:15], v[172:175], v[76:79], v[0:15]
	ds_read_b128 v[172:175], v239 offset:12288
	s_waitcnt lgkmcnt(14)
	v_mfma_f32_32x32x16_f16 v[0:15], v[176:179], v[80:83], v[0:15]
	ds_read_b128 v[176:179], v239 offset:13312
	s_waitcnt lgkmcnt(14)
	v_mfma_f32_32x32x16_f16 v[0:15], v[180:183], v[84:87], v[0:15]
	ds_read_b128 v[180:183], v239 offset:14336
	s_waitcnt lgkmcnt(14)
	v_mfma_f32_32x32x16_f16 v[0:15], v[184:187], v[88:91], v[0:15]
	ds_read_b128 v[184:187], v239 offset:15360
	s_waitcnt lgkmcnt(14)
	v_mfma_f32_32x32x16_f16 v[0:15], v[188:191], v[92:95], v[0:15]
	ds_read_b128 v[188:191], v239 offset:16384
	s_waitcnt lgkmcnt(14)
	v_mfma_f32_32x32x16_f16 v[0:15], v[192:195], v[96:99], v[0:15]
	ds_read_b128 v[192:195], v239 offset:17408
	s_waitcnt lgkmcnt(14)
	v_mfma_f32_32x32x16_f16 v[0:15], v[196:199], v[100:103], v[0:15]
	ds_read_b128 v[196:199], v239 offset:18432
	s_waitcnt vmcnt(2)
	ds_write_b128 v236, v[16:19] offset:24576
	ds_write_b128 v237, v[20:23] offset:24576
	ds_write_b128 v238, v[24:27] offset:24576
	s_waitcnt lgkmcnt(14)
	v_mfma_f32_32x32x16_f16 v[0:15], v[200:203], v[104:107], v[0:15]
	ds_read_b128 v[200:203], v239 offset:19456
	s_waitcnt lgkmcnt(14)
	v_mfma_f32_32x32x16_f16 v[0:15], v[204:207], v[108:111], v[0:15]
	ds_read_b128 v[204:207], v239 offset:20480
	s_waitcnt lgkmcnt(14)
	v_mfma_f32_32x32x16_f16 v[0:15], v[208:211], v[112:115], v[0:15]
	ds_read_b128 v[208:211], v239 offset:21504
	s_waitcnt lgkmcnt(14)
	v_mfma_f32_32x32x16_f16 v[0:15], v[212:215], v[116:119], v[0:15]
	ds_read_b128 v[212:215], v239 offset:22528
	s_waitcnt lgkmcnt(14)
	v_mfma_f32_32x32x16_f16 v[0:15], v[216:219], v[120:123], v[0:15]
	ds_read_b128 v[216:219], v239 offset:23552
	s_waitcnt lgkmcnt(5)
	s_barrier
	s_add_u32 s24, s22, 122880
	s_addc_u32 s25, s23, 0
	s_waitcnt lgkmcnt(14)
	v_mfma_f32_32x32x16_f16 v[220:235], v[124:127], v[28:31], 0
	ds_read_b128 v[124:127], v239 offset:24576
	global_load_dwordx4 v[16:19], v236, s[24:25]
	global_load_dwordx4 v[20:23], v237, s[24:25]
	global_load_dwordx4 v[24:27], v238, s[24:25]
	s_waitcnt lgkmcnt(14)
	v_mfma_f32_32x32x16_f16 v[220:235], v[128:131], v[32:35], v[220:235]
	ds_read_b128 v[128:131], v239 offset:25600
	s_add_i32 s20, s14, 2
	s_cmp_lt_u32 s20, 12
	s_cselect_b32 s26, s8, s10
	s_cselect_b32 s27, s9, s11
	s_waitcnt lgkmcnt(14)
	v_mfma_f32_32x32x16_f16 v[220:235], v[132:135], v[36:39], v[220:235]
	ds_read_b128 v[132:135], v239 offset:26624
	s_cselect_b32 s21, 0, 12
	s_cmp_lt_u32 s20, 24
	s_cselect_b32 s26, s26, s0
	s_cselect_b32 s27, s27, s1
	s_waitcnt lgkmcnt(14)
	v_mfma_f32_32x32x16_f16 v[220:235], v[136:139], v[40:43], v[220:235]
	ds_read_b128 v[136:139], v239 offset:27648
	s_cselect_b32 s21, s21, 24
	s_sub_i32 s20, s20, s21
	s_lshr_b32 s21, s20, 1
	s_and_b32 s20, s20, 1
	s_waitcnt lgkmcnt(14)
	v_mfma_f32_32x32x16_f16 v[220:235], v[140:143], v[44:47], v[220:235]
	ds_read_b128 v[140:143], v239 offset:28672
	s_add_i32 s21, s21, s15
	s_lshl_b32 s21, s21, 15
	s_lshl_b32 s20, s20, 11
	s_add_i32 s21, s21, s20
	s_waitcnt lgkmcnt(14)
	v_mfma_f32_32x32x16_f16 v[220:235], v[144:147], v[48:51], v[220:235]
	ds_read_b128 v[144:147], v239 offset:29696
	s_add_u32 s26, s26, s21
	s_addc_u32 s27, s27, 0
	s_waitcnt lgkmcnt(14)
	v_mfma_f32_32x32x16_f16 v[220:235], v[148:151], v[52:55], v[220:235]
	ds_read_b128 v[148:151], v239 offset:30720
	v_cvt_pk_f16_f32 v244, v0, v1
	v_cvt_pk_f16_f32 v245, v2, v3
	s_waitcnt lgkmcnt(14)
	v_mfma_f32_32x32x16_f16 v[220:235], v[152:155], v[56:59], v[220:235]
	ds_read_b128 v[152:155], v239 offset:31744
	v_cvt_pk_f16_f32 v246, v4, v5
	v_cvt_pk_f16_f32 v247, v6, v7
	s_waitcnt lgkmcnt(14)
	v_mfma_f32_32x32x16_f16 v[220:235], v[156:159], v[60:63], v[220:235]
	ds_read_b128 v[156:159], v239 offset:32768
	v_cvt_pk_f16_f32 v248, v8, v9
	v_cvt_pk_f16_f32 v249, v10, v11
	s_waitcnt lgkmcnt(14)
	v_mfma_f32_32x32x16_f16 v[220:235], v[160:163], v[64:67], v[220:235]
	ds_read_b128 v[160:163], v239 offset:33792
	v_cvt_pk_f16_f32 v250, v12, v13
	v_cvt_pk_f16_f32 v251, v14, v15
	s_waitcnt lgkmcnt(14)
	v_mfma_f32_32x32x16_f16 v[220:235], v[164:167], v[68:71], v[220:235]
	ds_read_b128 v[164:167], v239 offset:34816
	global_store_dwordx4 v241, v[244:247], s[26:27] nt
	s_waitcnt lgkmcnt(14)
	v_mfma_f32_32x32x16_f16 v[220:235], v[168:171], v[72:75], v[220:235]
	ds_read_b128 v[168:171], v239 offset:35840
	global_store_dwordx4 v241, v[248:251], s[26:27] offset:1024 nt
	s_waitcnt lgkmcnt(14)
	v_mfma_f32_32x32x16_f16 v[220:235], v[172:175], v[76:79], v[220:235]
	ds_read_b128 v[172:175], v239 offset:36864
	s_waitcnt lgkmcnt(14)
	v_mfma_f32_32x32x16_f16 v[220:235], v[176:179], v[80:83], v[220:235]
	ds_read_b128 v[176:179], v239 offset:37888
	s_waitcnt lgkmcnt(14)
	v_mfma_f32_32x32x16_f16 v[220:235], v[180:183], v[84:87], v[220:235]
	ds_read_b128 v[180:183], v239 offset:38912
	s_waitcnt lgkmcnt(14)
	v_mfma_f32_32x32x16_f16 v[220:235], v[184:187], v[88:91], v[220:235]
	ds_read_b128 v[184:187], v239 offset:39936
	s_waitcnt lgkmcnt(14)
	v_mfma_f32_32x32x16_f16 v[220:235], v[188:191], v[92:95], v[220:235]
	ds_read_b128 v[188:191], v239 offset:40960
	s_waitcnt lgkmcnt(14)
	v_mfma_f32_32x32x16_f16 v[220:235], v[192:195], v[96:99], v[220:235]
	ds_read_b128 v[192:195], v239 offset:41984
	s_waitcnt lgkmcnt(14)
	v_mfma_f32_32x32x16_f16 v[220:235], v[196:199], v[100:103], v[220:235]
	ds_read_b128 v[196:199], v239 offset:43008
	s_waitcnt vmcnt(2)
	ds_write_b128 v236, v[16:19] offset:49152
	ds_write_b128 v237, v[20:23] offset:49152
	ds_write_b128 v238, v[24:27] offset:49152
	s_waitcnt lgkmcnt(14)
	v_mfma_f32_32x32x16_f16 v[220:235], v[200:203], v[104:107], v[220:235]
	ds_read_b128 v[200:203], v239 offset:44032
	s_waitcnt lgkmcnt(14)
	v_mfma_f32_32x32x16_f16 v[220:235], v[204:207], v[108:111], v[220:235]
	ds_read_b128 v[204:207], v239 offset:45056
	s_waitcnt lgkmcnt(14)
	v_mfma_f32_32x32x16_f16 v[220:235], v[208:211], v[112:115], v[220:235]
	ds_read_b128 v[208:211], v239 offset:46080
	s_waitcnt lgkmcnt(14)
	v_mfma_f32_32x32x16_f16 v[220:235], v[212:215], v[116:119], v[220:235]
	ds_read_b128 v[212:215], v239 offset:47104
	s_waitcnt lgkmcnt(14)
	v_mfma_f32_32x32x16_f16 v[220:235], v[216:219], v[120:123], v[220:235]
	ds_read_b128 v[216:219], v239 offset:48128
	s_waitcnt lgkmcnt(5)
	s_barrier
	s_add_u32 s24, s22, 147456
	s_addc_u32 s25, s23, 0
	s_waitcnt lgkmcnt(14)
	v_mfma_f32_32x32x16_f16 v[0:15], v[124:127], v[28:31], 0
	ds_read_b128 v[124:127], v240 offset:0
	global_load_dwordx4 v[16:19], v236, s[24:25]
	global_load_dwordx4 v[20:23], v237, s[24:25]
	global_load_dwordx4 v[24:27], v238, s[24:25]
	s_waitcnt lgkmcnt(14)
	v_mfma_f32_32x32x16_f16 v[0:15], v[128:131], v[32:35], v[0:15]
	ds_read_b128 v[128:131], v240 offset:1024
	s_add_i32 s20, s14, 3
	s_cmp_lt_u32 s20, 12
	s_cselect_b32 s26, s8, s10
	s_cselect_b32 s27, s9, s11
	s_waitcnt lgkmcnt(14)
	v_mfma_f32_32x32x16_f16 v[0:15], v[132:135], v[36:39], v[0:15]
	ds_read_b128 v[132:135], v240 offset:2048
	s_cselect_b32 s21, 0, 12
	s_cmp_lt_u32 s20, 24
	s_cselect_b32 s26, s26, s0
	s_cselect_b32 s27, s27, s1
	s_waitcnt lgkmcnt(14)
	v_mfma_f32_32x32x16_f16 v[0:15], v[136:139], v[40:43], v[0:15]
	ds_read_b128 v[136:139], v240 offset:3072
	s_cselect_b32 s21, s21, 24
	s_sub_i32 s20, s20, s21
	s_lshr_b32 s21, s20, 1
	s_and_b32 s20, s20, 1
	s_waitcnt lgkmcnt(14)
	v_mfma_f32_32x32x16_f16 v[0:15], v[140:143], v[44:47], v[0:15]
	ds_read_b128 v[140:143], v240 offset:4096
	s_add_i32 s21, s21, s15
	s_lshl_b32 s21, s21, 15
	s_lshl_b32 s20, s20, 11
	s_add_i32 s21, s21, s20
	s_waitcnt lgkmcnt(14)
	v_mfma_f32_32x32x16_f16 v[0:15], v[144:147], v[48:51], v[0:15]
	ds_read_b128 v[144:147], v240 offset:5120
	s_add_u32 s26, s26, s21
	s_addc_u32 s27, s27, 0
	s_waitcnt lgkmcnt(14)
	v_mfma_f32_32x32x16_f16 v[0:15], v[148:151], v[52:55], v[0:15]
	ds_read_b128 v[148:151], v240 offset:6144
	v_cvt_pk_f16_f32 v244, v220, v221
	v_cvt_pk_f16_f32 v245, v222, v223
	s_waitcnt lgkmcnt(14)
	v_mfma_f32_32x32x16_f16 v[0:15], v[152:155], v[56:59], v[0:15]
	ds_read_b128 v[152:155], v240 offset:7168
	v_cvt_pk_f16_f32 v246, v224, v225
	v_cvt_pk_f16_f32 v247, v226, v227
	s_waitcnt lgkmcnt(14)
	v_mfma_f32_32x32x16_f16 v[0:15], v[156:159], v[60:63], v[0:15]
	ds_read_b128 v[156:159], v240 offset:8192
	v_cvt_pk_f16_f32 v248, v228, v229
	v_cvt_pk_f16_f32 v249, v230, v231
	s_waitcnt lgkmcnt(14)
	v_mfma_f32_32x32x16_f16 v[0:15], v[160:163], v[64:67], v[0:15]
	ds_read_b128 v[160:163], v240 offset:9216
	v_cvt_pk_f16_f32 v250, v232, v233
	v_cvt_pk_f16_f32 v251, v234, v235
	s_waitcnt lgkmcnt(14)
	v_mfma_f32_32x32x16_f16 v[0:15], v[164:167], v[68:71], v[0:15]
	ds_read_b128 v[164:167], v240 offset:10240
	global_store_dwordx4 v241, v[244:247], s[26:27] nt
	s_waitcnt lgkmcnt(14)
	v_mfma_f32_32x32x16_f16 v[0:15], v[168:171], v[72:75], v[0:15]
	ds_read_b128 v[168:171], v240 offset:11264
	global_store_dwordx4 v241, v[248:251], s[26:27] offset:1024 nt
	s_waitcnt lgkmcnt(14)
	v_mfma_f32_32x32x16_f16 v[0:15], v[172:175], v[76:79], v[0:15]
	ds_read_b128 v[172:175], v240 offset:12288
	s_waitcnt lgkmcnt(14)
	v_mfma_f32_32x32x16_f16 v[0:15], v[176:179], v[80:83], v[0:15]
	ds_read_b128 v[176:179], v240 offset:13312
	s_waitcnt lgkmcnt(14)
	v_mfma_f32_32x32x16_f16 v[0:15], v[180:183], v[84:87], v[0:15]
	ds_read_b128 v[180:183], v240 offset:14336
	s_waitcnt lgkmcnt(14)
	v_mfma_f32_32x32x16_f16 v[0:15], v[184:187], v[88:91], v[0:15]
	ds_read_b128 v[184:187], v240 offset:15360
	s_waitcnt lgkmcnt(14)
	v_mfma_f32_32x32x16_f16 v[0:15], v[188:191], v[92:95], v[0:15]
	ds_read_b128 v[188:191], v240 offset:16384
	s_waitcnt lgkmcnt(14)
	v_mfma_f32_32x32x16_f16 v[0:15], v[192:195], v[96:99], v[0:15]
	ds_read_b128 v[192:195], v240 offset:17408
	s_waitcnt lgkmcnt(14)
	v_mfma_f32_32x32x16_f16 v[0:15], v[196:199], v[100:103], v[0:15]
	ds_read_b128 v[196:199], v240 offset:18432
	s_waitcnt vmcnt(2)
	ds_write_b128 v236, v[16:19] offset:0
	ds_write_b128 v237, v[20:23] offset:0
	ds_write_b128 v238, v[24:27] offset:0
	s_waitcnt lgkmcnt(14)
	v_mfma_f32_32x32x16_f16 v[0:15], v[200:203], v[104:107], v[0:15]
	ds_read_b128 v[200:203], v240 offset:19456
	s_waitcnt lgkmcnt(14)
	v_mfma_f32_32x32x16_f16 v[0:15], v[204:207], v[108:111], v[0:15]
	ds_read_b128 v[204:207], v240 offset:20480
	s_waitcnt lgkmcnt(14)
	v_mfma_f32_32x32x16_f16 v[0:15], v[208:211], v[112:115], v[0:15]
	ds_read_b128 v[208:211], v240 offset:21504
	s_waitcnt lgkmcnt(14)
	v_mfma_f32_32x32x16_f16 v[0:15], v[212:215], v[116:119], v[0:15]
	ds_read_b128 v[212:215], v240 offset:22528
	s_waitcnt lgkmcnt(14)
	v_mfma_f32_32x32x16_f16 v[0:15], v[216:219], v[120:123], v[0:15]
	ds_read_b128 v[216:219], v240 offset:23552
	s_waitcnt lgkmcnt(5)
	s_barrier
	s_add_u32 s24, s22, 172032
	s_addc_u32 s25, s23, 0
	s_waitcnt lgkmcnt(14)
	v_mfma_f32_32x32x16_f16 v[220:235], v[124:127], v[28:31], 0
	ds_read_b128 v[124:127], v239 offset:0
	global_load_dwordx4 v[16:19], v236, s[24:25]
	global_load_dwordx4 v[20:23], v237, s[24:25]
	global_load_dwordx4 v[24:27], v238, s[24:25]
	s_waitcnt lgkmcnt(14)
	v_mfma_f32_32x32x16_f16 v[220:235], v[128:131], v[32:35], v[220:235]
	ds_read_b128 v[128:131], v239 offset:1024
	s_add_i32 s20, s14, 4
	s_cmp_lt_u32 s20, 12
	s_cselect_b32 s26, s8, s10
	s_cselect_b32 s27, s9, s11
	s_waitcnt lgkmcnt(14)
	v_mfma_f32_32x32x16_f16 v[220:235], v[132:135], v[36:39], v[220:235]
	ds_read_b128 v[132:135], v239 offset:2048
	s_cselect_b32 s21, 0, 12
	s_cmp_lt_u32 s20, 24
	s_cselect_b32 s26, s26, s0
	s_cselect_b32 s27, s27, s1
	s_waitcnt lgkmcnt(14)
	v_mfma_f32_32x32x16_f16 v[220:235], v[136:139], v[40:43], v[220:235]
	ds_read_b128 v[136:139], v239 offset:3072
	s_cselect_b32 s21, s21, 24
	s_sub_i32 s20, s20, s21
	s_lshr_b32 s21, s20, 1
	s_and_b32 s20, s20, 1
	s_waitcnt lgkmcnt(14)
	v_mfma_f32_32x32x16_f16 v[220:235], v[140:143], v[44:47], v[220:235]
	ds_read_b128 v[140:143], v239 offset:4096
	s_add_i32 s21, s21, s15
	s_lshl_b32 s21, s21, 15
	s_lshl_b32 s20, s20, 11
	s_add_i32 s21, s21, s20
	s_waitcnt lgkmcnt(14)
	v_mfma_f32_32x32x16_f16 v[220:235], v[144:147], v[48:51], v[220:235]
	ds_read_b128 v[144:147], v239 offset:5120
	s_add_u32 s26, s26, s21
	s_addc_u32 s27, s27, 0
	s_waitcnt lgkmcnt(14)
	v_mfma_f32_32x32x16_f16 v[220:235], v[148:151], v[52:55], v[220:235]
	ds_read_b128 v[148:151], v239 offset:6144
	v_cvt_pk_f16_f32 v244, v0, v1
	v_cvt_pk_f16_f32 v245, v2, v3
	s_waitcnt lgkmcnt(14)
	v_mfma_f32_32x32x16_f16 v[220:235], v[152:155], v[56:59], v[220:235]
	ds_read_b128 v[152:155], v239 offset:7168
	v_cvt_pk_f16_f32 v246, v4, v5
	v_cvt_pk_f16_f32 v247, v6, v7
	s_waitcnt lgkmcnt(14)
	v_mfma_f32_32x32x16_f16 v[220:235], v[156:159], v[60:63], v[220:235]
	ds_read_b128 v[156:159], v239 offset:8192
	v_cvt_pk_f16_f32 v248, v8, v9
	v_cvt_pk_f16_f32 v249, v10, v11
	s_waitcnt lgkmcnt(14)
	v_mfma_f32_32x32x16_f16 v[220:235], v[160:163], v[64:67], v[220:235]
	ds_read_b128 v[160:163], v239 offset:9216
	v_cvt_pk_f16_f32 v250, v12, v13
	v_cvt_pk_f16_f32 v251, v14, v15
	s_waitcnt lgkmcnt(14)
	v_mfma_f32_32x32x16_f16 v[220:235], v[164:167], v[68:71], v[220:235]
	ds_read_b128 v[164:167], v239 offset:10240
	global_store_dwordx4 v241, v[244:247], s[26:27] nt
	s_waitcnt lgkmcnt(14)
	v_mfma_f32_32x32x16_f16 v[220:235], v[168:171], v[72:75], v[220:235]
	ds_read_b128 v[168:171], v239 offset:11264
	global_store_dwordx4 v241, v[248:251], s[26:27] offset:1024 nt
	s_waitcnt lgkmcnt(14)
	v_mfma_f32_32x32x16_f16 v[220:235], v[172:175], v[76:79], v[220:235]
	ds_read_b128 v[172:175], v239 offset:12288
	s_waitcnt lgkmcnt(14)
	v_mfma_f32_32x32x16_f16 v[220:235], v[176:179], v[80:83], v[220:235]
	ds_read_b128 v[176:179], v239 offset:13312
	s_waitcnt lgkmcnt(14)
	v_mfma_f32_32x32x16_f16 v[220:235], v[180:183], v[84:87], v[220:235]
	ds_read_b128 v[180:183], v239 offset:14336
	s_waitcnt lgkmcnt(14)
	v_mfma_f32_32x32x16_f16 v[220:235], v[184:187], v[88:91], v[220:235]
	ds_read_b128 v[184:187], v239 offset:15360
	s_waitcnt lgkmcnt(14)
	v_mfma_f32_32x32x16_f16 v[220:235], v[188:191], v[92:95], v[220:235]
	ds_read_b128 v[188:191], v239 offset:16384
	s_waitcnt lgkmcnt(14)
	v_mfma_f32_32x32x16_f16 v[220:235], v[192:195], v[96:99], v[220:235]
	ds_read_b128 v[192:195], v239 offset:17408
	s_waitcnt lgkmcnt(14)
	v_mfma_f32_32x32x16_f16 v[220:235], v[196:199], v[100:103], v[220:235]
	ds_read_b128 v[196:199], v239 offset:18432
	s_waitcnt vmcnt(2)
	ds_write_b128 v236, v[16:19] offset:24576
	ds_write_b128 v237, v[20:23] offset:24576
	ds_write_b128 v238, v[24:27] offset:24576
	s_waitcnt lgkmcnt(14)
	v_mfma_f32_32x32x16_f16 v[220:235], v[200:203], v[104:107], v[220:235]
	ds_read_b128 v[200:203], v239 offset:19456
	s_waitcnt lgkmcnt(14)
	v_mfma_f32_32x32x16_f16 v[220:235], v[204:207], v[108:111], v[220:235]
	ds_read_b128 v[204:207], v239 offset:20480
	s_waitcnt lgkmcnt(14)
	v_mfma_f32_32x32x16_f16 v[220:235], v[208:211], v[112:115], v[220:235]
	ds_read_b128 v[208:211], v239 offset:21504
	s_waitcnt lgkmcnt(14)
	v_mfma_f32_32x32x16_f16 v[220:235], v[212:215], v[116:119], v[220:235]
	ds_read_b128 v[212:215], v239 offset:22528
	s_waitcnt lgkmcnt(14)
	v_mfma_f32_32x32x16_f16 v[220:235], v[216:219], v[120:123], v[220:235]
	ds_read_b128 v[216:219], v239 offset:23552
	s_waitcnt lgkmcnt(5)
	s_barrier
	s_add_u32 s24, s22, 196608
	s_addc_u32 s25, s23, 0
	s_waitcnt lgkmcnt(14)
	v_mfma_f32_32x32x16_f16 v[0:15], v[28:31], v[124:127], 0
	ds_read_b128 v[124:127], v239 offset:24576
	global_load_dwordx4 v[16:19], v236, s[24:25]
	global_load_dwordx4 v[20:23], v237, s[24:25]
	global_load_dwordx4 v[24:27], v238, s[24:25]
	s_waitcnt lgkmcnt(14)
	v_mfma_f32_32x32x16_f16 v[0:15], v[32:35], v[128:131], v[0:15]
	ds_read_b128 v[128:131], v239 offset:25600
	s_add_i32 s20, s14, 5
	s_cmp_lt_u32 s20, 12
	s_cselect_b32 s26, s8, s10
	s_cselect_b32 s27, s9, s11
	s_waitcnt lgkmcnt(14)
	v_mfma_f32_32x32x16_f16 v[0:15], v[36:39], v[132:135], v[0:15]
	ds_read_b128 v[132:135], v239 offset:26624
	s_cselect_b32 s21, 0, 12
	s_cmp_lt_u32 s20, 24
	s_cselect_b32 s26, s26, s0
	s_cselect_b32 s27, s27, s1
	s_waitcnt lgkmcnt(14)
	v_mfma_f32_32x32x16_f16 v[0:15], v[40:43], v[136:139], v[0:15]
	ds_read_b128 v[136:139], v239 offset:27648
	s_cselect_b32 s21, s21, 24
	s_sub_i32 s20, s20, s21
	s_lshr_b32 s21, s20, 1
	s_and_b32 s20, s20, 1
	s_waitcnt lgkmcnt(14)
	v_mfma_f32_32x32x16_f16 v[0:15], v[44:47], v[140:143], v[0:15]
	ds_read_b128 v[140:143], v239 offset:28672
	s_add_i32 s21, s21, s15
	s_lshl_b32 s21, s21, 15
	s_lshl_b32 s20, s20, 11
	s_add_i32 s21, s21, s20
	s_waitcnt lgkmcnt(14)
	v_mfma_f32_32x32x16_f16 v[0:15], v[48:51], v[144:147], v[0:15]
	ds_read_b128 v[144:147], v239 offset:29696
	s_add_u32 s26, s26, s21
	s_addc_u32 s27, s27, 0
	s_waitcnt lgkmcnt(14)
	v_mfma_f32_32x32x16_f16 v[0:15], v[52:55], v[148:151], v[0:15]
	ds_read_b128 v[148:151], v239 offset:30720
	v_cvt_pk_f16_f32 v244, v220, v221
	v_cvt_pk_f16_f32 v245, v222, v223
	s_waitcnt lgkmcnt(14)
	v_mfma_f32_32x32x16_f16 v[0:15], v[56:59], v[152:155], v[0:15]
	ds_read_b128 v[152:155], v239 offset:31744
	v_cvt_pk_f16_f32 v246, v224, v225
	v_cvt_pk_f16_f32 v247, v226, v227
	s_waitcnt lgkmcnt(14)
	v_mfma_f32_32x32x16_f16 v[0:15], v[60:63], v[156:159], v[0:15]
	ds_read_b128 v[156:159], v239 offset:32768
	v_cvt_pk_f16_f32 v248, v228, v229
	v_cvt_pk_f16_f32 v249, v230, v231
	s_waitcnt lgkmcnt(14)
	v_mfma_f32_32x32x16_f16 v[0:15], v[64:67], v[160:163], v[0:15]
	ds_read_b128 v[160:163], v239 offset:33792
	v_cvt_pk_f16_f32 v250, v232, v233
	v_cvt_pk_f16_f32 v251, v234, v235
	s_waitcnt lgkmcnt(14)
	v_mfma_f32_32x32x16_f16 v[0:15], v[68:71], v[164:167], v[0:15]
	ds_read_b128 v[164:167], v239 offset:34816
	global_store_dwordx4 v241, v[244:247], s[26:27] nt
	s_waitcnt lgkmcnt(14)
	v_mfma_f32_32x32x16_f16 v[0:15], v[72:75], v[168:171], v[0:15]
	ds_read_b128 v[168:171], v239 offset:35840
	global_store_dwordx4 v241, v[248:251], s[26:27] offset:1024 nt
	s_waitcnt lgkmcnt(14)
	v_mfma_f32_32x32x16_f16 v[0:15], v[76:79], v[172:175], v[0:15]
	ds_read_b128 v[172:175], v239 offset:36864
	s_waitcnt lgkmcnt(14)
	v_mfma_f32_32x32x16_f16 v[0:15], v[80:83], v[176:179], v[0:15]
	ds_read_b128 v[176:179], v239 offset:37888
	s_waitcnt lgkmcnt(14)
	v_mfma_f32_32x32x16_f16 v[0:15], v[84:87], v[180:183], v[0:15]
	ds_read_b128 v[180:183], v239 offset:38912
	s_waitcnt lgkmcnt(14)
	v_mfma_f32_32x32x16_f16 v[0:15], v[88:91], v[184:187], v[0:15]
	ds_read_b128 v[184:187], v239 offset:39936
	s_waitcnt lgkmcnt(14)
	v_mfma_f32_32x32x16_f16 v[0:15], v[92:95], v[188:191], v[0:15]
	ds_read_b128 v[188:191], v239 offset:40960
	s_waitcnt lgkmcnt(14)
	v_mfma_f32_32x32x16_f16 v[0:15], v[96:99], v[192:195], v[0:15]
	ds_read_b128 v[192:195], v239 offset:41984
	s_waitcnt lgkmcnt(14)
	v_mfma_f32_32x32x16_f16 v[0:15], v[100:103], v[196:199], v[0:15]
	ds_read_b128 v[196:199], v239 offset:43008
	s_waitcnt vmcnt(2)
	ds_write_b128 v236, v[16:19] offset:49152
	ds_write_b128 v237, v[20:23] offset:49152
	ds_write_b128 v238, v[24:27] offset:49152
	s_waitcnt lgkmcnt(14)
	v_mfma_f32_32x32x16_f16 v[0:15], v[104:107], v[200:203], v[0:15]
	ds_read_b128 v[200:203], v239 offset:44032
	s_waitcnt lgkmcnt(14)
	v_mfma_f32_32x32x16_f16 v[0:15], v[108:111], v[204:207], v[0:15]
	ds_read_b128 v[204:207], v239 offset:45056
	s_waitcnt lgkmcnt(14)
	v_mfma_f32_32x32x16_f16 v[0:15], v[112:115], v[208:211], v[0:15]
	ds_read_b128 v[208:211], v239 offset:46080
	s_waitcnt lgkmcnt(14)
	v_mfma_f32_32x32x16_f16 v[0:15], v[116:119], v[212:215], v[0:15]
	ds_read_b128 v[212:215], v239 offset:47104
	s_waitcnt lgkmcnt(14)
	v_mfma_f32_32x32x16_f16 v[0:15], v[120:123], v[216:219], v[0:15]
	ds_read_b128 v[216:219], v239 offset:48128
	s_waitcnt lgkmcnt(5)
	s_barrier
	s_waitcnt lgkmcnt(14)
	v_mfma_f32_32x32x16_f16 v[220:235], v[28:31], v[124:127], 0
	ds_read_b128 v[124:127], v240 offset:0
	s_waitcnt lgkmcnt(14)
	v_mfma_f32_32x32x16_f16 v[220:235], v[32:35], v[128:131], v[220:235]
	ds_read_b128 v[128:131], v240 offset:1024
	s_add_i32 s20, s14, 6
	s_cmp_lt_u32 s20, 12
	s_cselect_b32 s26, s8, s10
	s_cselect_b32 s27, s9, s11
	s_waitcnt lgkmcnt(14)
	v_mfma_f32_32x32x16_f16 v[220:235], v[36:39], v[132:135], v[220:235]
	ds_read_b128 v[132:135], v240 offset:2048
	s_cselect_b32 s21, 0, 12
	s_cmp_lt_u32 s20, 24
	s_cselect_b32 s26, s26, s0
	s_cselect_b32 s27, s27, s1
	s_waitcnt lgkmcnt(14)
	v_mfma_f32_32x32x16_f16 v[220:235], v[40:43], v[136:139], v[220:235]
	ds_read_b128 v[136:139], v240 offset:3072
	s_cselect_b32 s21, s21, 24
	s_sub_i32 s20, s20, s21
	s_lshr_b32 s21, s20, 1
	s_and_b32 s20, s20, 1
	s_waitcnt lgkmcnt(14)
	v_mfma_f32_32x32x16_f16 v[220:235], v[44:47], v[140:143], v[220:235]
	ds_read_b128 v[140:143], v240 offset:4096
	s_add_i32 s21, s21, s15
	s_lshl_b32 s21, s21, 15
	s_lshl_b32 s20, s20, 11
	s_add_i32 s21, s21, s20
	s_waitcnt lgkmcnt(14)
	v_mfma_f32_32x32x16_f16 v[220:235], v[48:51], v[144:147], v[220:235]
	ds_read_b128 v[144:147], v240 offset:5120
	s_add_u32 s26, s26, s21
	s_addc_u32 s27, s27, 0
	s_waitcnt lgkmcnt(14)
	v_mfma_f32_32x32x16_f16 v[220:235], v[52:55], v[148:151], v[220:235]
	ds_read_b128 v[148:151], v240 offset:6144
	v_cvt_pk_f16_f32 v244, v0, v1
	v_cvt_pk_f16_f32 v245, v2, v3
	s_waitcnt lgkmcnt(14)
	v_mfma_f32_32x32x16_f16 v[220:235], v[56:59], v[152:155], v[220:235]
	ds_read_b128 v[152:155], v240 offset:7168
	v_cvt_pk_f16_f32 v246, v4, v5
	v_cvt_pk_f16_f32 v247, v6, v7
	s_waitcnt lgkmcnt(14)
	v_mfma_f32_32x32x16_f16 v[220:235], v[60:63], v[156:159], v[220:235]
	ds_read_b128 v[156:159], v240 offset:8192
	v_cvt_pk_f16_f32 v248, v8, v9
	v_cvt_pk_f16_f32 v249, v10, v11
	s_waitcnt lgkmcnt(14)
	v_mfma_f32_32x32x16_f16 v[220:235], v[64:67], v[160:163], v[220:235]
	ds_read_b128 v[160:163], v240 offset:9216
	v_cvt_pk_f16_f32 v250, v12, v13
	v_cvt_pk_f16_f32 v251, v14, v15
	s_waitcnt lgkmcnt(14)
	v_mfma_f32_32x32x16_f16 v[220:235], v[68:71], v[164:167], v[220:235]
	ds_read_b128 v[164:167], v240 offset:10240
	global_store_dwordx4 v241, v[244:247], s[26:27] nt
	s_waitcnt lgkmcnt(14)
	v_mfma_f32_32x32x16_f16 v[220:235], v[72:75], v[168:171], v[220:235]
	ds_read_b128 v[168:171], v240 offset:11264
	global_store_dwordx4 v241, v[248:251], s[26:27] offset:1024 nt
	s_waitcnt lgkmcnt(14)
	v_mfma_f32_32x32x16_f16 v[220:235], v[76:79], v[172:175], v[220:235]
	ds_read_b128 v[172:175], v240 offset:12288
	s_waitcnt lgkmcnt(14)
	v_mfma_f32_32x32x16_f16 v[220:235], v[80:83], v[176:179], v[220:235]
	ds_read_b128 v[176:179], v240 offset:13312
	s_waitcnt lgkmcnt(14)
	v_mfma_f32_32x32x16_f16 v[220:235], v[84:87], v[180:183], v[220:235]
	ds_read_b128 v[180:183], v240 offset:14336
	s_waitcnt lgkmcnt(14)
	v_mfma_f32_32x32x16_f16 v[220:235], v[88:91], v[184:187], v[220:235]
	ds_read_b128 v[184:187], v240 offset:15360
	s_waitcnt lgkmcnt(14)
	v_mfma_f32_32x32x16_f16 v[220:235], v[92:95], v[188:191], v[220:235]
	ds_read_b128 v[188:191], v240 offset:16384
	s_waitcnt lgkmcnt(14)
	v_mfma_f32_32x32x16_f16 v[220:235], v[96:99], v[192:195], v[220:235]
	ds_read_b128 v[192:195], v240 offset:17408
	s_waitcnt lgkmcnt(14)
	v_mfma_f32_32x32x16_f16 v[220:235], v[100:103], v[196:199], v[220:235]
	ds_read_b128 v[196:199], v240 offset:18432
	s_waitcnt lgkmcnt(14)
	v_mfma_f32_32x32x16_f16 v[220:235], v[104:107], v[200:203], v[220:235]
	ds_read_b128 v[200:203], v240 offset:19456
	s_waitcnt lgkmcnt(14)
	v_mfma_f32_32x32x16_f16 v[220:235], v[108:111], v[204:207], v[220:235]
	ds_read_b128 v[204:207], v240 offset:20480
	s_waitcnt lgkmcnt(14)
	v_mfma_f32_32x32x16_f16 v[220:235], v[112:115], v[208:211], v[220:235]
	ds_read_b128 v[208:211], v240 offset:21504
	s_waitcnt lgkmcnt(14)
	v_mfma_f32_32x32x16_f16 v[220:235], v[116:119], v[212:215], v[220:235]
	ds_read_b128 v[212:215], v240 offset:22528
	s_waitcnt lgkmcnt(14)
	v_mfma_f32_32x32x16_f16 v[220:235], v[120:123], v[216:219], v[220:235]
	ds_read_b128 v[216:219], v240 offset:23552
	s_waitcnt lgkmcnt(14)
	v_mfma_f32_32x32x16_f16 v[0:15], v[28:31], v[124:127], 0
	s_waitcnt lgkmcnt(14)
	v_mfma_f32_32x32x16_f16 v[0:15], v[32:35], v[128:131], v[0:15]
	s_add_i32 s20, s14, 7
	s_cmp_lt_u32 s20, 12
	s_cselect_b32 s26, s8, s10
	s_cselect_b32 s27, s9, s11
	s_waitcnt lgkmcnt(14)
	v_mfma_f32_32x32x16_f16 v[0:15], v[36:39], v[132:135], v[0:15]
	s_cselect_b32 s21, 0, 12
	s_cmp_lt_u32 s20, 24
	s_cselect_b32 s26, s26, s0
	s_cselect_b32 s27, s27, s1
	s_waitcnt lgkmcnt(14)
	v_mfma_f32_32x32x16_f16 v[0:15], v[40:43], v[136:139], v[0:15]
	s_cselect_b32 s21, s21, 24
	s_sub_i32 s20, s20, s21
	s_lshr_b32 s21, s20, 1
	s_and_b32 s20, s20, 1
	s_waitcnt lgkmcnt(14)
	v_mfma_f32_32x32x16_f16 v[0:15], v[44:47], v[140:143], v[0:15]
	s_add_i32 s21, s21, s15
	s_lshl_b32 s21, s21, 15
	s_lshl_b32 s20, s20, 11
	s_add_i32 s21, s21, s20
	s_waitcnt lgkmcnt(14)
	v_mfma_f32_32x32x16_f16 v[0:15], v[48:51], v[144:147], v[0:15]
	s_add_u32 s26, s26, s21
	s_addc_u32 s27, s27, 0
	s_waitcnt lgkmcnt(14)
	v_mfma_f32_32x32x16_f16 v[0:15], v[52:55], v[148:151], v[0:15]
	v_cvt_pk_f16_f32 v244, v220, v221
	v_cvt_pk_f16_f32 v245, v222, v223
	s_waitcnt lgkmcnt(14)
	v_mfma_f32_32x32x16_f16 v[0:15], v[56:59], v[152:155], v[0:15]
	v_cvt_pk_f16_f32 v246, v224, v225
	v_cvt_pk_f16_f32 v247, v226, v227
	s_waitcnt lgkmcnt(14)
	v_mfma_f32_32x32x16_f16 v[0:15], v[60:63], v[156:159], v[0:15]
	v_cvt_pk_f16_f32 v248, v228, v229
	v_cvt_pk_f16_f32 v249, v230, v231
	s_waitcnt lgkmcnt(14)
	v_mfma_f32_32x32x16_f16 v[0:15], v[64:67], v[160:163], v[0:15]
	v_cvt_pk_f16_f32 v250, v232, v233
	v_cvt_pk_f16_f32 v251, v234, v235
	s_waitcnt lgkmcnt(13)
	v_mfma_f32_32x32x16_f16 v[0:15], v[68:71], v[164:167], v[0:15]
	global_store_dwordx4 v241, v[244:247], s[26:27] nt
	s_waitcnt lgkmcnt(12)
	v_mfma_f32_32x32x16_f16 v[0:15], v[72:75], v[168:171], v[0:15]
	global_store_dwordx4 v241, v[248:251], s[26:27] offset:1024 nt
	s_waitcnt lgkmcnt(11)
	v_mfma_f32_32x32x16_f16 v[0:15], v[76:79], v[172:175], v[0:15]
	s_waitcnt lgkmcnt(10)
	v_mfma_f32_32x32x16_f16 v[0:15], v[80:83], v[176:179], v[0:15]
	s_waitcnt lgkmcnt(9)
	v_mfma_f32_32x32x16_f16 v[0:15], v[84:87], v[180:183], v[0:15]
	s_waitcnt lgkmcnt(8)
	v_mfma_f32_32x32x16_f16 v[0:15], v[88:91], v[184:187], v[0:15]
	s_waitcnt lgkmcnt(7)
	v_mfma_f32_32x32x16_f16 v[0:15], v[92:95], v[188:191], v[0:15]
	s_waitcnt lgkmcnt(6)
	v_mfma_f32_32x32x16_f16 v[0:15], v[96:99], v[192:195], v[0:15]
	s_waitcnt lgkmcnt(5)
	v_mfma_f32_32x32x16_f16 v[0:15], v[100:103], v[196:199], v[0:15]
	s_waitcnt lgkmcnt(4)
	v_mfma_f32_32x32x16_f16 v[0:15], v[104:107], v[200:203], v[0:15]
	s_waitcnt lgkmcnt(3)
	v_mfma_f32_32x32x16_f16 v[0:15], v[108:111], v[204:207], v[0:15]
	s_waitcnt lgkmcnt(2)
	v_mfma_f32_32x32x16_f16 v[0:15], v[112:115], v[208:211], v[0:15]
	s_waitcnt lgkmcnt(1)
	v_mfma_f32_32x32x16_f16 v[0:15], v[116:119], v[212:215], v[0:15]
	s_waitcnt lgkmcnt(0)
	v_mfma_f32_32x32x16_f16 v[0:15], v[120:123], v[216:219], v[0:15]
	s_add_i32 s20, s14, 8
	s_cmp_lt_u32 s20, 12
	s_cselect_b32 s26, s8, s10
	s_cselect_b32 s27, s9, s11
	s_cselect_b32 s21, 0, 12
	s_cmp_lt_u32 s20, 24
	s_cselect_b32 s26, s26, s0
	s_cselect_b32 s27, s27, s1
	s_cselect_b32 s21, s21, 24
	s_sub_i32 s20, s20, s21
	s_lshr_b32 s21, s20, 1
	s_and_b32 s20, s20, 1
	s_add_i32 s21, s21, s15
	s_lshl_b32 s21, s21, 15
	s_lshl_b32 s20, s20, 11
	s_add_i32 s21, s21, s20
	s_add_u32 s26, s26, s21
	s_addc_u32 s27, s27, 0
	s_nop 7
	v_cvt_pk_f16_f32 v244, v0, v1
	v_cvt_pk_f16_f32 v245, v2, v3
	v_cvt_pk_f16_f32 v246, v4, v5
	v_cvt_pk_f16_f32 v247, v6, v7
	v_cvt_pk_f16_f32 v248, v8, v9
	v_cvt_pk_f16_f32 v249, v10, v11
	v_cvt_pk_f16_f32 v250, v12, v13
	v_cvt_pk_f16_f32 v251, v14, v15
	global_store_dwordx4 v241, v[244:247], s[26:27] nt
	global_store_dwordx4 v241, v[248:251], s[26:27] offset:1024 nt
	s_endpgm
.Lqkv_bodyS:
	ds_read_b128 v[124:127], v239 offset:0
	ds_read_b128 v[128:131], v239 offset:1024
	ds_read_b128 v[132:135], v239 offset:2048
	ds_read_b128 v[136:139], v239 offset:3072
	ds_read_b128 v[140:143], v239 offset:4096
	ds_read_b128 v[144:147], v239 offset:5120
	ds_read_b128 v[148:151], v239 offset:6144
	ds_read_b128 v[152:155], v239 offset:7168
	ds_read_b128 v[156:159], v239 offset:8192
	ds_read_b128 v[160:163], v239 offset:9216
	ds_read_b128 v[164:167], v239 offset:10240
	ds_read_b128 v[168:171], v239 offset:11264
	ds_read_b128 v[172:175], v239 offset:12288
	ds_read_b128 v[176:179], v239 offset:13312
	ds_read_b128 v[180:183], v239 offset:14336
	ds_read_b128 v[184:187], v239 offset:15360
	ds_read_b128 v[188:191], v239 offset:16384
	ds_read_b128 v[192:195], v239 offset:17408
	ds_read_b128 v[196:199], v239 offset:18432
	ds_read_b128 v[200:203], v239 offset:19456
	ds_read_b128 v[204:207], v239 offset:20480
	ds_read_b128 v[208:211], v239 offset:21504
	ds_read_b128 v[212:215], v239 offset:22528
	ds_read_b128 v[216:219], v239 offset:23552
	s_add_u32 s24, s22, 49152
	s_addc_u32 s25, s23, 0
	s_waitcnt lgkmcnt(14)
	v_mfma_f32_32x32x16_f16 v[0:15], v[124:127], v[28:31], 0
	ds_read_b128 v[124:127], v239 offset:24576
	global_load_dwordx4 v[16:19], v236, s[24:25]
	global_load_dwordx4 v[20:23], v237, s[24:25]
	global_load_dwordx4 v[24:27], v238, s[24:25]
	s_waitcnt lgkmcnt(14)
	v_mfma_f32_32x32x16_f16 v[0:15], v[128:131], v[32:35], v[0:15]
	ds_read_b128 v[128:131], v239 offset:25600
	s_waitcnt lgkmcnt(14)
	v_mfma_f32_32x32x16_f16 v[0:15], v[132:135], v[36:39], v[0:15]
	ds_read_b128 v[132:135], v239 offset:26624
	s_waitcnt lgkmcnt(14)
	v_mfma_f32_32x32x16_f16 v[0:15], v[136:139], v[40:43], v[0:15]
	ds_read_b128 v[136:139], v239 offset:27648
	s_waitcnt lgkmcnt(14)
	v_mfma_f32_32x32x16_f16 v[0:15], v[140:143], v[44:47], v[0:15]
	ds_read_b128 v[140:143], v239 offset:28672
	s_waitcnt lgkmcnt(14)
	v_mfma_f32_32x32x16_f16 v[0:15], v[144:147], v[48:51], v[0:15]
	ds_read_b128 v[144:147], v239 offset:29696
	s_waitcnt lgkmcnt(14)
	v_mfma_f32_32x32x16_f16 v[0:15], v[148:151], v[52:55], v[0:15]
	ds_read_b128 v[148:151], v239 offset:30720
	s_waitcnt lgkmcnt(14)
	v_mfma_f32_32x32x16_f16 v[0:15], v[152:155], v[56:59], v[0:15]
	ds_read_b128 v[152:155], v239 offset:31744
	s_waitcnt lgkmcnt(14)
	v_mfma_f32_32x32x16_f16 v[0:15], v[156:159], v[60:63], v[0:15]
	ds_read_b128 v[156:159], v239 offset:32768
	s_waitcnt lgkmcnt(14)
	v_mfma_f32_32x32x16_f16 v[0:15], v[160:163], v[64:67], v[0:15]
	ds_read_b128 v[160:163], v239 offset:33792
	s_waitcnt lgkmcnt(14)
	v_mfma_f32_32x32x16_f16 v[0:15], v[164:167], v[68:71], v[0:15]
	ds_read_b128 v[164:167], v239 offset:34816
	s_waitcnt lgkmcnt(14)
	v_mfma_f32_32x32x16_f16 v[0:15], v[168:171], v[72:75], v[0:15]
	ds_read_b128 v[168:171], v239 offset:35840
	s_waitcnt lgkmcnt(14)
	v_mfma_f32_32x32x16_f16 v[0:15], v[172:175], v[76:79], v[0:15]
	ds_read_b128 v[172:175], v239 offset:36864
	s_waitcnt lgkmcnt(14)
	v_mfma_f32_32x32x16_f16 v[0:15], v[176:179], v[80:83], v[0:15]
	ds_read_b128 v[176:179], v239 offset:37888
	s_waitcnt lgkmcnt(14)
	v_mfma_f32_32x32x16_f16 v[0:15], v[180:183], v[84:87], v[0:15]
	ds_read_b128 v[180:183], v239 offset:38912
	s_waitcnt lgkmcnt(14)
	v_mfma_f32_32x32x16_f16 v[0:15], v[184:187], v[88:91], v[0:15]
	ds_read_b128 v[184:187], v239 offset:39936
	s_waitcnt lgkmcnt(14)
	v_mfma_f32_32x32x16_f16 v[0:15], v[188:191], v[92:95], v[0:15]
	ds_read_b128 v[188:191], v239 offset:40960
	s_waitcnt lgkmcnt(14)
	v_mfma_f32_32x32x16_f16 v[0:15], v[192:195], v[96:99], v[0:15]
	ds_read_b128 v[192:195], v239 offset:41984
	s_waitcnt lgkmcnt(14)
	v_mfma_f32_32x32x16_f16 v[0:15], v[196:199], v[100:103], v[0:15]
	ds_read_b128 v[196:199], v239 offset:43008
	s_waitcnt vmcnt(0)
	ds_write_b128 v236, v[16:19] offset:49152
	ds_write_b128 v237, v[20:23] offset:49152
	ds_write_b128 v238, v[24:27] offset:49152
	s_waitcnt lgkmcnt(14)
	v_mfma_f32_32x32x16_f16 v[0:15], v[200:203], v[104:107], v[0:15]
	ds_read_b128 v[200:203], v239 offset:44032
	s_waitcnt lgkmcnt(14)
	v_mfma_f32_32x32x16_f16 v[0:15], v[204:207], v[108:111], v[0:15]
	ds_read_b128 v[204:207], v239 offset:45056
	s_waitcnt lgkmcnt(14)
	v_mfma_f32_32x32x16_f16 v[0:15], v[208:211], v[112:115], v[0:15]
	ds_read_b128 v[208:211], v239 offset:46080
	s_waitcnt lgkmcnt(14)
	v_mfma_f32_32x32x16_f16 v[0:15], v[212:215], v[116:119], v[0:15]
	ds_read_b128 v[212:215], v239 offset:47104
	s_waitcnt lgkmcnt(14)
	v_mfma_f32_32x32x16_f16 v[0:15], v[216:219], v[120:123], v[0:15]
	ds_read_b128 v[216:219], v239 offset:48128
	s_waitcnt lgkmcnt(5)
	s_barrier
	s_add_u32 s24, s22, 73728
	s_addc_u32 s25, s23, 0
	s_waitcnt lgkmcnt(14)
	v_mfma_f32_32x32x16_f16 v[220:235], v[124:127], v[28:31], 0
	ds_read_b128 v[124:127], v240 offset:0
	global_load_dwordx4 v[16:19], v236, s[24:25]
	global_load_dwordx4 v[20:23], v237, s[24:25]
	global_load_dwordx4 v[24:27], v238, s[24:25]
	s_waitcnt lgkmcnt(14)
	v_mfma_f32_32x32x16_f16 v[220:235], v[128:131], v[32:35], v[220:235]
	ds_read_b128 v[128:131], v240 offset:1024
	s_add_i32 s20, s14, 0
	s_cmp_lt_u32 s20, 12
	s_cselect_b32 s26, s8, s10
	s_cselect_b32 s27, s9, s11
	s_waitcnt lgkmcnt(14)
	v_mfma_f32_32x32x16_f16 v[220:235], v[132:135], v[36:39], v[220:235]
	ds_read_b128 v[132:135], v240 offset:2048
	s_cselect_b32 s21, 0, 12
	s_cmp_lt_u32 s20, 24
	s_cselect_b32 s26, s26, s0
	s_cselect_b32 s27, s27, s1
	s_waitcnt lgkmcnt(14)
	v_mfma_f32_32x32x16_f16 v[220:235], v[136:139], v[40:43], v[220:235]
	ds_read_b128 v[136:139], v240 offset:3072
	s_cselect_b32 s21, s21, 24
	s_sub_i32 s20, s20, s21
	s_lshr_b32 s21, s20, 1
	s_and_b32 s20, s20, 1
	s_waitcnt lgkmcnt(14)
	v_mfma_f32_32x32x16_f16 v[220:235], v[140:143], v[44:47], v[220:235]
	ds_read_b128 v[140:143], v240 offset:4096
	s_add_i32 s21, s21, s15
	s_lshl_b32 s21, s21, 15
	s_lshl_b32 s20, s20, 11
	s_add_i32 s21, s21, s20
	s_waitcnt lgkmcnt(14)
	v_mfma_f32_32x32x16_f16 v[220:235], v[144:147], v[48:51], v[220:235]
	ds_read_b128 v[144:147], v240 offset:5120
	s_add_u32 s26, s26, s21
	s_addc_u32 s27, s27, 0
	s_waitcnt lgkmcnt(14)
	v_mfma_f32_32x32x16_f16 v[220:235], v[148:151], v[52:55], v[220:235]
	ds_read_b128 v[148:151], v240 offset:6144
	v_cvt_pk_f16_f32 v244, v0, v1
	v_cvt_pk_f16_f32 v245, v2, v3
	s_waitcnt lgkmcnt(14)
	v_mfma_f32_32x32x16_f16 v[220:235], v[152:155], v[56:59], v[220:235]
	ds_read_b128 v[152:155], v240 offset:7168
	v_cvt_pk_f16_f32 v246, v4, v5
	v_cvt_pk_f16_f32 v247, v6, v7
	s_waitcnt lgkmcnt(14)
	v_mfma_f32_32x32x16_f16 v[220:235], v[156:159], v[60:63], v[220:235]
	ds_read_b128 v[156:159], v240 offset:8192
	v_cvt_pk_f16_f32 v248, v8, v9
	v_cvt_pk_f16_f32 v249, v10, v11
	s_waitcnt lgkmcnt(14)
	v_mfma_f32_32x32x16_f16 v[220:235], v[160:163], v[64:67], v[220:235]
	ds_read_b128 v[160:163], v240 offset:9216
	v_cvt_pk_f16_f32 v250, v12, v13
	v_cvt_pk_f16_f32 v251, v14, v15
	s_waitcnt lgkmcnt(14)
	v_mfma_f32_32x32x16_f16 v[220:235], v[164:167], v[68:71], v[220:235]
	ds_read_b128 v[164:167], v240 offset:10240
	global_store_dwordx4 v241, v[244:247], s[26:27] nt
	s_waitcnt lgkmcnt(14)
	v_mfma_f32_32x32x16_f16 v[220:235], v[168:171], v[72:75], v[220:235]
	ds_read_b128 v[168:171], v240 offset:11264
	global_store_dwordx4 v241, v[248:251], s[26:27] offset:1024 nt
	s_waitcnt lgkmcnt(14)
	v_mfma_f32_32x32x16_f16 v[220:235], v[172:175], v[76:79], v[220:235]
	ds_read_b128 v[172:175], v240 offset:12288
	s_waitcnt lgkmcnt(14)
	v_mfma_f32_32x32x16_f16 v[220:235], v[176:179], v[80:83], v[220:235]
	ds_read_b128 v[176:179], v240 offset:13312
	s_waitcnt lgkmcnt(14)
	v_mfma_f32_32x32x16_f16 v[220:235], v[180:183], v[84:87], v[220:235]
	ds_read_b128 v[180:183], v240 offset:14336
	s_waitcnt lgkmcnt(14)
	v_mfma_f32_32x32x16_f16 v[220:235], v[184:187], v[88:91], v[220:235]
	ds_read_b128 v[184:187], v240 offset:15360
	s_waitcnt lgkmcnt(14)
	v_mfma_f32_32x32x16_f16 v[220:235], v[188:191], v[92:95], v[220:235]
	ds_read_b128 v[188:191], v240 offset:16384
	s_waitcnt lgkmcnt(14)
	v_mfma_f32_32x32x16_f16 v[220:235], v[192:195], v[96:99], v[220:235]
	ds_read_b128 v[192:195], v240 offset:17408
	s_waitcnt lgkmcnt(14)
	v_mfma_f32_32x32x16_f16 v[220:235], v[196:199], v[100:103], v[220:235]
	ds_read_b128 v[196:199], v240 offset:18432
	s_waitcnt vmcnt(2)
	ds_write_b128 v236, v[16:19] offset:0
	ds_write_b128 v237, v[20:23] offset:0
	ds_write_b128 v238, v[24:27] offset:0
	s_waitcnt lgkmcnt(14)
	v_mfma_f32_32x32x16_f16 v[220:235], v[200:203], v[104:107], v[220:235]
	ds_read_b128 v[200:203], v240 offset:19456
	s_waitcnt lgkmcnt(14)
	v_mfma_f32_32x32x16_f16 v[220:235], v[204:207], v[108:111], v[220:235]
	ds_read_b128 v[204:207], v240 offset:20480
	s_waitcnt lgkmcnt(14)
	v_mfma_f32_32x32x16_f16 v[220:235], v[208:211], v[112:115], v[220:235]
	ds_read_b128 v[208:211], v240 offset:21504
	s_waitcnt lgkmcnt(14)
	v_mfma_f32_32x32x16_f16 v[220:235], v[212:215], v[116:119], v[220:235]
	ds_read_b128 v[212:215], v240 offset:22528
	s_waitcnt lgkmcnt(14)
	v_mfma_f32_32x32x16_f16 v[220:235], v[216:219], v[120:123], v[220:235]
	ds_read_b128 v[216:219], v240 offset:23552
	s_waitcnt lgkmcnt(5)
	s_barrier
	s_add_u32 s24, s22, 98304
	s_addc_u32 s25, s23, 0
	s_waitcnt lgkmcnt(14)
	v_mfma_f32_32x32x16_f16 v[0:15], v[124:127], v[28:31], 0
	ds_read_b128 v[124:127], v239 offset:0
	global_load_dwordx4 v[16:19], v236, s[24:25]
	global_load_dwordx4 v[20:23], v237, s[24:25]
	global_load_dwordx4 v[24:27], v238, s[24:25]
	s_waitcnt lgkmcnt(14)
	v_mfma_f32_32x32x16_f16 v[0:15], v[128:131], v[32:35], v[0:15]
	ds_read_b128 v[128:131], v239 offset:1024
	s_add_i32 s20, s14, 1
	s_cmp_lt_u32 s20, 12
	s_cselect_b32 s26, s8, s10
	s_cselect_b32 s27, s9, s11
	s_waitcnt lgkmcnt(14)
	v_mfma_f32_32x32x16_f16 v[0:15], v[132:135], v[36:39], v[0:15]
	ds_read_b128 v[132:135], v239 offset:2048
	s_cselect_b32 s21, 0, 12
	s_cmp_lt_u32 s20, 24
	s_cselect_b32 s26, s26, s0
	s_cselect_b32 s27, s27, s1
	s_waitcnt lgkmcnt(14)
	v_mfma_f32_32x32x16_f16 v[0:15], v[136:139], v[40:43], v[0:15]
	ds_read_b128 v[136:139], v239 offset:3072
	s_cselect_b32 s21, s21, 24
	s_sub_i32 s20, s20, s21
	s_lshr_b32 s21, s20, 1
	s_and_b32 s20, s20, 1
	s_waitcnt lgkmcnt(14)
	v_mfma_f32_32x32x16_f16 v[0:15], v[140:143], v[44:47], v[0:15]
	ds_read_b128 v[140:143], v239 offset:4096
	s_add_i32 s21, s21, s15
	s_lshl_b32 s21, s21, 15
	s_lshl_b32 s20, s20, 11
	s_add_i32 s21, s21, s20
	s_waitcnt lgkmcnt(14)
	v_mfma_f32_32x32x16_f16 v[0:15], v[144:147], v[48:51], v[0:15]
	ds_read_b128 v[144:147], v239 offset:5120
	s_add_u32 s26, s26, s21
	s_addc_u32 s27, s27, 0
	s_waitcnt lgkmcnt(14)
	v_mfma_f32_32x32x16_f16 v[0:15], v[148:151], v[52:55], v[0:15]
	ds_read_b128 v[148:151], v239 offset:6144
	v_cvt_pk_f16_f32 v244, v220, v221
	v_cvt_pk_f16_f32 v245, v222, v223
	s_waitcnt lgkmcnt(14)
	v_mfma_f32_32x32x16_f16 v[0:15], v[152:155], v[56:59], v[0:15]
	ds_read_b128 v[152:155], v239 offset:7168
	v_cvt_pk_f16_f32 v246, v224, v225
	v_cvt_pk_f16_f32 v247, v226, v227
	s_waitcnt lgkmcnt(14)
	v_mfma_f32_32x32x16_f16 v[0:15], v[156:159], v[60:63], v[0:15]
	ds_read_b128 v[156:159], v239 offset:8192
	v_cvt_pk_f16_f32 v248, v228, v229
	v_cvt_pk_f16_f32 v249, v230, v231
	s_waitcnt lgkmcnt(14)
	v_mfma_f32_32x32x16_f16 v[0:15], v[160:163], v[64:67], v[0:15]
	ds_read_b128 v[160:163], v239 offset:9216
	v_cvt_pk_f16_f32 v250, v232, v233
	v_cvt_pk_f16_f32 v251, v234, v235
	s_waitcnt lgkmcnt(14)
	v_mfma_f32_32x32x16_f16 v[0:15], v[164:167], v[68:71], v[0:15]
	ds_read_b128 v[164:167], v239 offset:10240
	global_store_dwordx4 v241, v[244:247], s[26:27] nt
	s_waitcnt lgkmcnt(14)
	v_mfma_f32_32x32x16_f16 v[0:15], v[168:171], v[72:75], v[0:15]
	ds_read_b128 v[168:171], v239 offset:11264
	global_store_dwordx4 v241, v[248:251], s[26:27] offset:1024 nt
	s_waitcnt lgkmcnt(14)
	v_mfma_f32_32x32x16_f16 v[0:15], v[172:175], v[76:79], v[0:15]
	ds_read_b128 v[172:175], v239 offset:12288
	s_waitcnt lgkmcnt(14)
	v_mfma_f32_32x32x16_f16 v[0:15], v[176:179], v[80:83], v[0:15]
	ds_read_b128 v[176:179], v239 offset:13312
	s_waitcnt lgkmcnt(14)
	v_mfma_f32_32x32x16_f16 v[0:15], v[180:183], v[84:87], v[0:15]
	ds_read_b128 v[180:183], v239 offset:14336
	s_waitcnt lgkmcnt(14)
	v_mfma_f32_32x32x16_f16 v[0:15], v[184:187], v[88:91], v[0:15]
	ds_read_b128 v[184:187], v239 offset:15360
	s_waitcnt lgkmcnt(14)
	v_mfma_f32_32x32x16_f16 v[0:15], v[188:191], v[92:95], v[0:15]
	ds_read_b128 v[188:191], v239 offset:16384
	s_waitcnt lgkmcnt(14)
	v_mfma_f32_32x32x16_f16 v[0:15], v[192:195], v[96:99], v[0:15]
	ds_read_b128 v[192:195], v239 offset:17408
	s_waitcnt lgkmcnt(14)
	v_mfma_f32_32x32x16_f16 v[0:15], v[196:199], v[100:103], v[0:15]
	ds_read_b128 v[196:199], v239 offset:18432
	s_waitcnt vmcnt(2)
	ds_write_b128 v236, v[16:19] offset:24576
	ds_write_b128 v237, v[20:23] offset:24576
	ds_write_b128 v238, v[24:27] offset:24576
	s_waitcnt lgkmcnt(14)
	v_mfma_f32_32x32x16_f16 v[0:15], v[200:203], v[104:107], v[0:15]
	ds_read_b128 v[200:203], v239 offset:19456
	s_waitcnt lgkmcnt(14)
	v_mfma_f32_32x32x16_f16 v[0:15], v[204:207], v[108:111], v[0:15]
	ds_read_b128 v[204:207], v239 offset:20480
	s_waitcnt lgkmcnt(14)
	v_mfma_f32_32x32x16_f16 v[0:15], v[208:211], v[112:115], v[0:15]
	ds_read_b128 v[208:211], v239 offset:21504
	s_waitcnt lgkmcnt(14)
	v_mfma_f32_32x32x16_f16 v[0:15], v[212:215], v[116:119], v[0:15]
	ds_read_b128 v[212:215], v239 offset:22528
	s_waitcnt lgkmcnt(14)
	v_mfma_f32_32x32x16_f16 v[0:15], v[216:219], v[120:123], v[0:15]
	ds_read_b128 v[216:219], v239 offset:23552
	s_waitcnt lgkmcnt(5)
	s_barrier
	s_add_u32 s24, s22, 122880
	s_addc_u32 s25, s23, 0
	s_waitcnt lgkmcnt(14)
	v_mfma_f32_32x32x16_f16 v[220:235], v[124:127], v[28:31], 0
	ds_read_b128 v[124:127], v239 offset:24576
	global_load_dwordx4 v[16:19], v236, s[24:25]
	global_load_dwordx4 v[20:23], v237, s[24:25]
	global_load_dwordx4 v[24:27], v238, s[24:25]
	s_waitcnt lgkmcnt(14)
	v_mfma_f32_32x32x16_f16 v[220:235], v[128:131], v[32:35], v[220:235]
	ds_read_b128 v[128:131], v239 offset:25600
	s_add_i32 s20, s14, 2
	s_cmp_lt_u32 s20, 12
	s_cselect_b32 s26, s8, s10
	s_cselect_b32 s27, s9, s11
	s_waitcnt lgkmcnt(14)
	v_mfma_f32_32x32x16_f16 v[220:235], v[132:135], v[36:39], v[220:235]
	ds_read_b128 v[132:135], v239 offset:26624
	s_cselect_b32 s21, 0, 12
	s_cmp_lt_u32 s20, 24
	s_cselect_b32 s26, s26, s0
	s_cselect_b32 s27, s27, s1
	s_waitcnt lgkmcnt(14)
	v_mfma_f32_32x32x16_f16 v[220:235], v[136:139], v[40:43], v[220:235]
	ds_read_b128 v[136:139], v239 offset:27648
	s_cselect_b32 s21, s21, 24
	s_sub_i32 s20, s20, s21
	s_lshr_b32 s21, s20, 1
	s_and_b32 s20, s20, 1
	s_waitcnt lgkmcnt(14)
	v_mfma_f32_32x32x16_f16 v[220:235], v[140:143], v[44:47], v[220:235]
	ds_read_b128 v[140:143], v239 offset:28672
	s_add_i32 s21, s21, s15
	s_lshl_b32 s21, s21, 15
	s_lshl_b32 s20, s20, 11
	s_add_i32 s21, s21, s20
	s_waitcnt lgkmcnt(14)
	v_mfma_f32_32x32x16_f16 v[220:235], v[144:147], v[48:51], v[220:235]
	ds_read_b128 v[144:147], v239 offset:29696
	s_add_u32 s26, s26, s21
	s_addc_u32 s27, s27, 0
	s_waitcnt lgkmcnt(14)
	v_mfma_f32_32x32x16_f16 v[220:235], v[148:151], v[52:55], v[220:235]
	ds_read_b128 v[148:151], v239 offset:30720
	v_cvt_pk_f16_f32 v244, v0, v1
	v_cvt_pk_f16_f32 v245, v2, v3
	s_waitcnt lgkmcnt(14)
	v_mfma_f32_32x32x16_f16 v[220:235], v[152:155], v[56:59], v[220:235]
	ds_read_b128 v[152:155], v239 offset:31744
	v_cvt_pk_f16_f32 v246, v4, v5
	v_cvt_pk_f16_f32 v247, v6, v7
	s_waitcnt lgkmcnt(14)
	v_mfma_f32_32x32x16_f16 v[220:235], v[156:159], v[60:63], v[220:235]
	ds_read_b128 v[156:159], v239 offset:32768
	v_cvt_pk_f16_f32 v248, v8, v9
	v_cvt_pk_f16_f32 v249, v10, v11
	s_waitcnt lgkmcnt(14)
	v_mfma_f32_32x32x16_f16 v[220:235], v[160:163], v[64:67], v[220:235]
	ds_read_b128 v[160:163], v239 offset:33792
	v_cvt_pk_f16_f32 v250, v12, v13
	v_cvt_pk_f16_f32 v251, v14, v15
	s_waitcnt lgkmcnt(14)
	v_mfma_f32_32x32x16_f16 v[220:235], v[164:167], v[68:71], v[220:235]
	ds_read_b128 v[164:167], v239 offset:34816
	global_store_dwordx4 v241, v[244:247], s[26:27] nt
	s_waitcnt lgkmcnt(14)
	v_mfma_f32_32x32x16_f16 v[220:235], v[168:171], v[72:75], v[220:235]
	ds_read_b128 v[168:171], v239 offset:35840
	global_store_dwordx4 v241, v[248:251], s[26:27] offset:1024 nt
	s_waitcnt lgkmcnt(14)
	v_mfma_f32_32x32x16_f16 v[220:235], v[172:175], v[76:79], v[220:235]
	ds_read_b128 v[172:175], v239 offset:36864
	s_waitcnt lgkmcnt(14)
	v_mfma_f32_32x32x16_f16 v[220:235], v[176:179], v[80:83], v[220:235]
	ds_read_b128 v[176:179], v239 offset:37888
	s_waitcnt lgkmcnt(14)
	v_mfma_f32_32x32x16_f16 v[220:235], v[180:183], v[84:87], v[220:235]
	ds_read_b128 v[180:183], v239 offset:38912
	s_waitcnt lgkmcnt(14)
	v_mfma_f32_32x32x16_f16 v[220:235], v[184:187], v[88:91], v[220:235]
	ds_read_b128 v[184:187], v239 offset:39936
	s_waitcnt lgkmcnt(14)
	v_mfma_f32_32x32x16_f16 v[220:235], v[188:191], v[92:95], v[220:235]
	ds_read_b128 v[188:191], v239 offset:40960
	s_waitcnt lgkmcnt(14)
	v_mfma_f32_32x32x16_f16 v[220:235], v[192:195], v[96:99], v[220:235]
	ds_read_b128 v[192:195], v239 offset:41984
	s_waitcnt lgkmcnt(14)
	v_mfma_f32_32x32x16_f16 v[220:235], v[196:199], v[100:103], v[220:235]
	ds_read_b128 v[196:199], v239 offset:43008
	s_waitcnt vmcnt(2)
	ds_write_b128 v236, v[16:19] offset:49152
	ds_write_b128 v237, v[20:23] offset:49152
	ds_write_b128 v238, v[24:27] offset:49152
	s_waitcnt lgkmcnt(14)
	v_mfma_f32_32x32x16_f16 v[220:235], v[200:203], v[104:107], v[220:235]
	ds_read_b128 v[200:203], v239 offset:44032
	s_waitcnt lgkmcnt(14)
	v_mfma_f32_32x32x16_f16 v[220:235], v[204:207], v[108:111], v[220:235]
	ds_read_b128 v[204:207], v239 offset:45056
	s_waitcnt lgkmcnt(14)
	v_mfma_f32_32x32x16_f16 v[220:235], v[208:211], v[112:115], v[220:235]
	ds_read_b128 v[208:211], v239 offset:46080
	s_waitcnt lgkmcnt(14)
	v_mfma_f32_32x32x16_f16 v[220:235], v[212:215], v[116:119], v[220:235]
	ds_read_b128 v[212:215], v239 offset:47104
	s_waitcnt lgkmcnt(14)
	v_mfma_f32_32x32x16_f16 v[220:235], v[216:219], v[120:123], v[220:235]
	ds_read_b128 v[216:219], v239 offset:48128
	s_waitcnt lgkmcnt(5)
	s_barrier
	s_add_u32 s24, s22, 147456
	s_addc_u32 s25, s23, 0
	s_waitcnt lgkmcnt(14)
	v_mfma_f32_32x32x16_f16 v[0:15], v[124:127], v[28:31], 0
	ds_read_b128 v[124:127], v240 offset:0
	global_load_dwordx4 v[16:19], v236, s[24:25]
	global_load_dwordx4 v[20:23], v237, s[24:25]
	global_load_dwordx4 v[24:27], v238, s[24:25]
	s_waitcnt lgkmcnt(14)
	v_mfma_f32_32x32x16_f16 v[0:15], v[128:131], v[32:35], v[0:15]
	ds_read_b128 v[128:131], v240 offset:1024
	s_add_i32 s20, s14, 3
	s_cmp_lt_u32 s20, 12
	s_cselect_b32 s26, s8, s10
	s_cselect_b32 s27, s9, s11
	s_waitcnt lgkmcnt(14)
	v_mfma_f32_32x32x16_f16 v[0:15], v[132:135], v[36:39], v[0:15]
	ds_read_b128 v[132:135], v240 offset:2048
	s_cselect_b32 s21, 0, 12
	s_cmp_lt_u32 s20, 24
	s_cselect_b32 s26, s26, s0
	s_cselect_b32 s27, s27, s1
	s_waitcnt lgkmcnt(14)
	v_mfma_f32_32x32x16_f16 v[0:15], v[136:139], v[40:43], v[0:15]
	ds_read_b128 v[136:139], v240 offset:3072
	s_cselect_b32 s21, s21, 24
	s_sub_i32 s20, s20, s21
	s_lshr_b32 s21, s20, 1
	s_and_b32 s20, s20, 1
	s_waitcnt lgkmcnt(14)
	v_mfma_f32_32x32x16_f16 v[0:15], v[140:143], v[44:47], v[0:15]
	ds_read_b128 v[140:143], v240 offset:4096
	s_add_i32 s21, s21, s15
	s_lshl_b32 s21, s21, 15
	s_lshl_b32 s20, s20, 11
	s_add_i32 s21, s21, s20
	s_waitcnt lgkmcnt(14)
	v_mfma_f32_32x32x16_f16 v[0:15], v[144:147], v[48:51], v[0:15]
	ds_read_b128 v[144:147], v240 offset:5120
	s_add_u32 s26, s26, s21
	s_addc_u32 s27, s27, 0
	s_waitcnt lgkmcnt(14)
	v_mfma_f32_32x32x16_f16 v[0:15], v[148:151], v[52:55], v[0:15]
	ds_read_b128 v[148:151], v240 offset:6144
	v_cvt_pk_f16_f32 v244, v220, v221
	v_cvt_pk_f16_f32 v245, v222, v223
	s_waitcnt lgkmcnt(14)
	v_mfma_f32_32x32x16_f16 v[0:15], v[152:155], v[56:59], v[0:15]
	ds_read_b128 v[152:155], v240 offset:7168
	v_cvt_pk_f16_f32 v246, v224, v225
	v_cvt_pk_f16_f32 v247, v226, v227
	s_waitcnt lgkmcnt(14)
	v_mfma_f32_32x32x16_f16 v[0:15], v[156:159], v[60:63], v[0:15]
	ds_read_b128 v[156:159], v240 offset:8192
	v_cvt_pk_f16_f32 v248, v228, v229
	v_cvt_pk_f16_f32 v249, v230, v231
	s_waitcnt lgkmcnt(14)
	v_mfma_f32_32x32x16_f16 v[0:15], v[160:163], v[64:67], v[0:15]
	ds_read_b128 v[160:163], v240 offset:9216
	v_cvt_pk_f16_f32 v250, v232, v233
	v_cvt_pk_f16_f32 v251, v234, v235
	s_waitcnt lgkmcnt(14)
	v_mfma_f32_32x32x16_f16 v[0:15], v[164:167], v[68:71], v[0:15]
	ds_read_b128 v[164:167], v240 offset:10240
	global_store_dwordx4 v241, v[244:247], s[26:27] nt
	s_waitcnt lgkmcnt(14)
	v_mfma_f32_32x32x16_f16 v[0:15], v[168:171], v[72:75], v[0:15]
	ds_read_b128 v[168:171], v240 offset:11264
	global_store_dwordx4 v241, v[248:251], s[26:27] offset:1024 nt
	s_waitcnt lgkmcnt(14)
	v_mfma_f32_32x32x16_f16 v[0:15], v[172:175], v[76:79], v[0:15]
	ds_read_b128 v[172:175], v240 offset:12288
	s_waitcnt lgkmcnt(14)
	v_mfma_f32_32x32x16_f16 v[0:15], v[176:179], v[80:83], v[0:15]
	ds_read_b128 v[176:179], v240 offset:13312
	s_waitcnt lgkmcnt(14)
	v_mfma_f32_32x32x16_f16 v[0:15], v[180:183], v[84:87], v[0:15]
	ds_read_b128 v[180:183], v240 offset:14336
	s_waitcnt lgkmcnt(14)
	v_mfma_f32_32x32x16_f16 v[0:15], v[184:187], v[88:91], v[0:15]
	ds_read_b128 v[184:187], v240 offset:15360
	s_waitcnt lgkmcnt(14)
	v_mfma_f32_32x32x16_f16 v[0:15], v[188:191], v[92:95], v[0:15]
	ds_read_b128 v[188:191], v240 offset:16384
	s_waitcnt lgkmcnt(14)
	v_mfma_f32_32x32x16_f16 v[0:15], v[192:195], v[96:99], v[0:15]
	ds_read_b128 v[192:195], v240 offset:17408
	s_waitcnt lgkmcnt(14)
	v_mfma_f32_32x32x16_f16 v[0:15], v[196:199], v[100:103], v[0:15]
	ds_read_b128 v[196:199], v240 offset:18432
	s_waitcnt vmcnt(2)
	ds_write_b128 v236, v[16:19] offset:0
	ds_write_b128 v237, v[20:23] offset:0
	ds_write_b128 v238, v[24:27] offset:0
	s_waitcnt lgkmcnt(14)
	v_mfma_f32_32x32x16_f16 v[0:15], v[200:203], v[104:107], v[0:15]
	ds_read_b128 v[200:203], v240 offset:19456
	s_waitcnt lgkmcnt(14)
	v_mfma_f32_32x32x16_f16 v[0:15], v[204:207], v[108:111], v[0:15]
	ds_read_b128 v[204:207], v240 offset:20480
	s_waitcnt lgkmcnt(14)
	v_mfma_f32_32x32x16_f16 v[0:15], v[208:211], v[112:115], v[0:15]
	ds_read_b128 v[208:211], v240 offset:21504
	s_waitcnt lgkmcnt(14)
	v_mfma_f32_32x32x16_f16 v[0:15], v[212:215], v[116:119], v[0:15]
	ds_read_b128 v[212:215], v240 offset:22528
	s_waitcnt lgkmcnt(14)
	v_mfma_f32_32x32x16_f16 v[0:15], v[216:219], v[120:123], v[0:15]
	ds_read_b128 v[216:219], v240 offset:23552
	s_waitcnt lgkmcnt(5)
	s_barrier
	s_add_u32 s24, s22, 172032
	s_addc_u32 s25, s23, 0
	s_waitcnt lgkmcnt(14)
	v_mfma_f32_32x32x16_f16 v[220:235], v[124:127], v[28:31], 0
	ds_read_b128 v[124:127], v239 offset:0
	global_load_dwordx4 v[16:19], v236, s[24:25]
	global_load_dwordx4 v[20:23], v237, s[24:25]
	global_load_dwordx4 v[24:27], v238, s[24:25]
	s_waitcnt lgkmcnt(14)
	v_mfma_f32_32x32x16_f16 v[220:235], v[128:131], v[32:35], v[220:235]
	ds_read_b128 v[128:131], v239 offset:1024
	s_add_i32 s20, s14, 4
	s_cmp_lt_u32 s20, 12
	s_cselect_b32 s26, s8, s10
	s_cselect_b32 s27, s9, s11
	s_waitcnt lgkmcnt(14)
	v_mfma_f32_32x32x16_f16 v[220:235], v[132:135], v[36:39], v[220:235]
	ds_read_b128 v[132:135], v239 offset:2048
	s_cselect_b32 s21, 0, 12
	s_cmp_lt_u32 s20, 24
	s_cselect_b32 s26, s26, s0
	s_cselect_b32 s27, s27, s1
	s_waitcnt lgkmcnt(14)
	v_mfma_f32_32x32x16_f16 v[220:235], v[136:139], v[40:43], v[220:235]
	ds_read_b128 v[136:139], v239 offset:3072
	s_cselect_b32 s21, s21, 24
	s_sub_i32 s20, s20, s21
	s_lshr_b32 s21, s20, 1
	s_and_b32 s20, s20, 1
	s_waitcnt lgkmcnt(14)
	v_mfma_f32_32x32x16_f16 v[220:235], v[140:143], v[44:47], v[220:235]
	ds_read_b128 v[140:143], v239 offset:4096
	s_add_i32 s21, s21, s15
	s_lshl_b32 s21, s21, 15
	s_lshl_b32 s20, s20, 11
	s_add_i32 s21, s21, s20
	s_waitcnt lgkmcnt(14)
	v_mfma_f32_32x32x16_f16 v[220:235], v[144:147], v[48:51], v[220:235]
	ds_read_b128 v[144:147], v239 offset:5120
	s_add_u32 s26, s26, s21
	s_addc_u32 s27, s27, 0
	s_waitcnt lgkmcnt(14)
	v_mfma_f32_32x32x16_f16 v[220:235], v[148:151], v[52:55], v[220:235]
	ds_read_b128 v[148:151], v239 offset:6144
	v_cvt_pk_f16_f32 v244, v0, v1
	v_cvt_pk_f16_f32 v245, v2, v3
	s_waitcnt lgkmcnt(14)
	v_mfma_f32_32x32x16_f16 v[220:235], v[152:155], v[56:59], v[220:235]
	ds_read_b128 v[152:155], v239 offset:7168
	v_cvt_pk_f16_f32 v246, v4, v5
	v_cvt_pk_f16_f32 v247, v6, v7
	s_waitcnt lgkmcnt(14)
	v_mfma_f32_32x32x16_f16 v[220:235], v[156:159], v[60:63], v[220:235]
	ds_read_b128 v[156:159], v239 offset:8192
	v_cvt_pk_f16_f32 v248, v8, v9
	v_cvt_pk_f16_f32 v249, v10, v11
	s_waitcnt lgkmcnt(14)
	v_mfma_f32_32x32x16_f16 v[220:235], v[160:163], v[64:67], v[220:235]
	ds_read_b128 v[160:163], v239 offset:9216
	v_cvt_pk_f16_f32 v250, v12, v13
	v_cvt_pk_f16_f32 v251, v14, v15
	s_waitcnt lgkmcnt(14)
	v_mfma_f32_32x32x16_f16 v[220:235], v[164:167], v[68:71], v[220:235]
	ds_read_b128 v[164:167], v239 offset:10240
	global_store_dwordx4 v241, v[244:247], s[26:27] nt
	s_waitcnt lgkmcnt(14)
	v_mfma_f32_32x32x16_f16 v[220:235], v[168:171], v[72:75], v[220:235]
	ds_read_b128 v[168:171], v239 offset:11264
	global_store_dwordx4 v241, v[248:251], s[26:27] offset:1024 nt
	s_waitcnt lgkmcnt(14)
	v_mfma_f32_32x32x16_f16 v[220:235], v[172:175], v[76:79], v[220:235]
	ds_read_b128 v[172:175], v239 offset:12288
	s_waitcnt lgkmcnt(14)
	v_mfma_f32_32x32x16_f16 v[220:235], v[176:179], v[80:83], v[220:235]
	ds_read_b128 v[176:179], v239 offset:13312
	s_waitcnt lgkmcnt(14)
	v_mfma_f32_32x32x16_f16 v[220:235], v[180:183], v[84:87], v[220:235]
	ds_read_b128 v[180:183], v239 offset:14336
	s_waitcnt lgkmcnt(14)
	v_mfma_f32_32x32x16_f16 v[220:235], v[184:187], v[88:91], v[220:235]
	ds_read_b128 v[184:187], v239 offset:15360
	s_waitcnt lgkmcnt(14)
	v_mfma_f32_32x32x16_f16 v[220:235], v[188:191], v[92:95], v[220:235]
	ds_read_b128 v[188:191], v239 offset:16384
	s_waitcnt lgkmcnt(14)
	v_mfma_f32_32x32x16_f16 v[220:235], v[192:195], v[96:99], v[220:235]
	ds_read_b128 v[192:195], v239 offset:17408
	s_waitcnt lgkmcnt(14)
	v_mfma_f32_32x32x16_f16 v[220:235], v[196:199], v[100:103], v[220:235]
	ds_read_b128 v[196:199], v239 offset:18432
	s_waitcnt vmcnt(2)
	ds_write_b128 v236, v[16:19] offset:24576
	ds_write_b128 v237, v[20:23] offset:24576
	ds_write_b128 v238, v[24:27] offset:24576
	s_waitcnt lgkmcnt(14)
	v_mfma_f32_32x32x16_f16 v[220:235], v[200:203], v[104:107], v[220:235]
	ds_read_b128 v[200:203], v239 offset:19456
	s_waitcnt lgkmcnt(14)
	v_mfma_f32_32x32x16_f16 v[220:235], v[204:207], v[108:111], v[220:235]
	ds_read_b128 v[204:207], v239 offset:20480
	s_waitcnt lgkmcnt(14)
	v_mfma_f32_32x32x16_f16 v[220:235], v[208:211], v[112:115], v[220:235]
	ds_read_b128 v[208:211], v239 offset:21504
	s_waitcnt lgkmcnt(14)
	v_mfma_f32_32x32x16_f16 v[220:235], v[212:215], v[116:119], v[220:235]
	ds_read_b128 v[212:215], v239 offset:22528
	s_waitcnt lgkmcnt(14)
	v_mfma_f32_32x32x16_f16 v[220:235], v[216:219], v[120:123], v[220:235]
	ds_read_b128 v[216:219], v239 offset:23552
	s_waitcnt lgkmcnt(5)
	s_barrier
	s_add_u32 s24, s22, 196608
	s_addc_u32 s25, s23, 0
	s_waitcnt lgkmcnt(14)
	v_mfma_f32_32x32x16_f16 v[0:15], v[124:127], v[28:31], 0
	ds_read_b128 v[124:127], v239 offset:24576
	global_load_dwordx4 v[16:19], v236, s[24:25]
	global_load_dwordx4 v[20:23], v237, s[24:25]
	global_load_dwordx4 v[24:27], v238, s[24:25]
	s_waitcnt lgkmcnt(14)
	v_mfma_f32_32x32x16_f16 v[0:15], v[128:131], v[32:35], v[0:15]
	ds_read_b128 v[128:131], v239 offset:25600
	s_add_i32 s20, s14, 5
	s_cmp_lt_u32 s20, 12
	s_cselect_b32 s26, s8, s10
	s_cselect_b32 s27, s9, s11
	s_waitcnt lgkmcnt(14)
	v_mfma_f32_32x32x16_f16 v[0:15], v[132:135], v[36:39], v[0:15]
	ds_read_b128 v[132:135], v239 offset:26624
	s_cselect_b32 s21, 0, 12
	s_cmp_lt_u32 s20, 24
	s_cselect_b32 s26, s26, s0
	s_cselect_b32 s27, s27, s1
	s_waitcnt lgkmcnt(14)
	v_mfma_f32_32x32x16_f16 v[0:15], v[136:139], v[40:43], v[0:15]
	ds_read_b128 v[136:139], v239 offset:27648
	s_cselect_b32 s21, s21, 24
	s_sub_i32 s20, s20, s21
	s_lshr_b32 s21, s20, 1
	s_and_b32 s20, s20, 1
	s_waitcnt lgkmcnt(14)
	v_mfma_f32_32x32x16_f16 v[0:15], v[140:143], v[44:47], v[0:15]
	ds_read_b128 v[140:143], v239 offset:28672
	s_add_i32 s21, s21, s15
	s_lshl_b32 s21, s21, 15
	s_lshl_b32 s20, s20, 11
	s_add_i32 s21, s21, s20
	s_waitcnt lgkmcnt(14)
	v_mfma_f32_32x32x16_f16 v[0:15], v[144:147], v[48:51], v[0:15]
	ds_read_b128 v[144:147], v239 offset:29696
	s_add_u32 s26, s26, s21
	s_addc_u32 s27, s27, 0
	s_waitcnt lgkmcnt(14)
	v_mfma_f32_32x32x16_f16 v[0:15], v[148:151], v[52:55], v[0:15]
	ds_read_b128 v[148:151], v239 offset:30720
	v_cvt_pk_f16_f32 v244, v220, v221
	v_cvt_pk_f16_f32 v245, v222, v223
	s_waitcnt lgkmcnt(14)
	v_mfma_f32_32x32x16_f16 v[0:15], v[152:155], v[56:59], v[0:15]
	ds_read_b128 v[152:155], v239 offset:31744
	v_cvt_pk_f16_f32 v246, v224, v225
	v_cvt_pk_f16_f32 v247, v226, v227
	s_waitcnt lgkmcnt(14)
	v_mfma_f32_32x32x16_f16 v[0:15], v[156:159], v[60:63], v[0:15]
	ds_read_b128 v[156:159], v239 offset:32768
	v_cvt_pk_f16_f32 v248, v228, v229
	v_cvt_pk_f16_f32 v249, v230, v231
	s_waitcnt lgkmcnt(14)
	v_mfma_f32_32x32x16_f16 v[0:15], v[160:163], v[64:67], v[0:15]
	ds_read_b128 v[160:163], v239 offset:33792
	v_cvt_pk_f16_f32 v250, v232, v233
	v_cvt_pk_f16_f32 v251, v234, v235
	s_waitcnt lgkmcnt(14)
	v_mfma_f32_32x32x16_f16 v[0:15], v[164:167], v[68:71], v[0:15]
	ds_read_b128 v[164:167], v239 offset:34816
	global_store_dwordx4 v241, v[244:247], s[26:27] nt
	s_waitcnt lgkmcnt(14)
	v_mfma_f32_32x32x16_f16 v[0:15], v[168:171], v[72:75], v[0:15]
	ds_read_b128 v[168:171], v239 offset:35840
	global_store_dwordx4 v241, v[248:251], s[26:27] offset:1024 nt
	s_waitcnt lgkmcnt(14)
	v_mfma_f32_32x32x16_f16 v[0:15], v[172:175], v[76:79], v[0:15]
	ds_read_b128 v[172:175], v239 offset:36864
	s_waitcnt lgkmcnt(14)
	v_mfma_f32_32x32x16_f16 v[0:15], v[176:179], v[80:83], v[0:15]
	ds_read_b128 v[176:179], v239 offset:37888
	s_waitcnt lgkmcnt(14)
	v_mfma_f32_32x32x16_f16 v[0:15], v[180:183], v[84:87], v[0:15]
	ds_read_b128 v[180:183], v239 offset:38912
	s_waitcnt lgkmcnt(14)
	v_mfma_f32_32x32x16_f16 v[0:15], v[184:187], v[88:91], v[0:15]
	ds_read_b128 v[184:187], v239 offset:39936
	s_waitcnt lgkmcnt(14)
	v_mfma_f32_32x32x16_f16 v[0:15], v[188:191], v[92:95], v[0:15]
	ds_read_b128 v[188:191], v239 offset:40960
	s_waitcnt lgkmcnt(14)
	v_mfma_f32_32x32x16_f16 v[0:15], v[192:195], v[96:99], v[0:15]
	ds_read_b128 v[192:195], v239 offset:41984
	s_waitcnt lgkmcnt(14)
	v_mfma_f32_32x32x16_f16 v[0:15], v[196:199], v[100:103], v[0:15]
	ds_read_b128 v[196:199], v239 offset:43008
	s_waitcnt vmcnt(2)
	ds_write_b128 v236, v[16:19] offset:49152
	ds_write_b128 v237, v[20:23] offset:49152
	ds_write_b128 v238, v[24:27] offset:49152
	s_waitcnt lgkmcnt(14)
	v_mfma_f32_32x32x16_f16 v[0:15], v[200:203], v[104:107], v[0:15]
	ds_read_b128 v[200:203], v239 offset:44032
	s_waitcnt lgkmcnt(14)
	v_mfma_f32_32x32x16_f16 v[0:15], v[204:207], v[108:111], v[0:15]
	ds_read_b128 v[204:207], v239 offset:45056
	s_waitcnt lgkmcnt(14)
	v_mfma_f32_32x32x16_f16 v[0:15], v[208:211], v[112:115], v[0:15]
	ds_read_b128 v[208:211], v239 offset:46080
	s_waitcnt lgkmcnt(14)
	v_mfma_f32_32x32x16_f16 v[0:15], v[212:215], v[116:119], v[0:15]
	ds_read_b128 v[212:215], v239 offset:47104
	s_waitcnt lgkmcnt(14)
	v_mfma_f32_32x32x16_f16 v[0:15], v[216:219], v[120:123], v[0:15]
	ds_read_b128 v[216:219], v239 offset:48128
	s_waitcnt lgkmcnt(5)
	s_barrier
	s_waitcnt lgkmcnt(14)
	v_mfma_f32_32x32x16_f16 v[220:235], v[124:127], v[28:31], 0
	ds_read_b128 v[124:127], v240 offset:0
	s_waitcnt lgkmcnt(14)
	v_mfma_f32_32x32x16_f16 v[220:235], v[128:131], v[32:35], v[220:235]
	ds_read_b128 v[128:131], v240 offset:1024
	s_add_i32 s20, s14, 6
	s_cmp_lt_u32 s20, 12
	s_cselect_b32 s26, s8, s10
	s_cselect_b32 s27, s9, s11
	s_waitcnt lgkmcnt(14)
	v_mfma_f32_32x32x16_f16 v[220:235], v[132:135], v[36:39], v[220:235]
	ds_read_b128 v[132:135], v240 offset:2048
	s_cselect_b32 s21, 0, 12
	s_cmp_lt_u32 s20, 24
	s_cselect_b32 s26, s26, s0
	s_cselect_b32 s27, s27, s1
	s_waitcnt lgkmcnt(14)
	v_mfma_f32_32x32x16_f16 v[220:235], v[136:139], v[40:43], v[220:235]
	ds_read_b128 v[136:139], v240 offset:3072
	s_cselect_b32 s21, s21, 24
	s_sub_i32 s20, s20, s21
	s_lshr_b32 s21, s20, 1
	s_and_b32 s20, s20, 1
	s_waitcnt lgkmcnt(14)
	v_mfma_f32_32x32x16_f16 v[220:235], v[140:143], v[44:47], v[220:235]
	ds_read_b128 v[140:143], v240 offset:4096
	s_add_i32 s21, s21, s15
	s_lshl_b32 s21, s21, 15
	s_lshl_b32 s20, s20, 11
	s_add_i32 s21, s21, s20
	s_waitcnt lgkmcnt(14)
	v_mfma_f32_32x32x16_f16 v[220:235], v[144:147], v[48:51], v[220:235]
	ds_read_b128 v[144:147], v240 offset:5120
	s_add_u32 s26, s26, s21
	s_addc_u32 s27, s27, 0
	s_waitcnt lgkmcnt(14)
	v_mfma_f32_32x32x16_f16 v[220:235], v[148:151], v[52:55], v[220:235]
	ds_read_b128 v[148:151], v240 offset:6144
	v_cvt_pk_f16_f32 v244, v0, v1
	v_cvt_pk_f16_f32 v245, v2, v3
	s_waitcnt lgkmcnt(14)
	v_mfma_f32_32x32x16_f16 v[220:235], v[152:155], v[56:59], v[220:235]
	ds_read_b128 v[152:155], v240 offset:7168
	v_cvt_pk_f16_f32 v246, v4, v5
	v_cvt_pk_f16_f32 v247, v6, v7
	s_waitcnt lgkmcnt(14)
	v_mfma_f32_32x32x16_f16 v[220:235], v[156:159], v[60:63], v[220:235]
	ds_read_b128 v[156:159], v240 offset:8192
	v_cvt_pk_f16_f32 v248, v8, v9
	v_cvt_pk_f16_f32 v249, v10, v11
	s_waitcnt lgkmcnt(14)
	v_mfma_f32_32x32x16_f16 v[220:235], v[160:163], v[64:67], v[220:235]
	ds_read_b128 v[160:163], v240 offset:9216
	v_cvt_pk_f16_f32 v250, v12, v13
	v_cvt_pk_f16_f32 v251, v14, v15
	s_waitcnt lgkmcnt(14)
	v_mfma_f32_32x32x16_f16 v[220:235], v[164:167], v[68:71], v[220:235]
	ds_read_b128 v[164:167], v240 offset:10240
	global_store_dwordx4 v241, v[244:247], s[26:27] nt
	s_waitcnt lgkmcnt(14)
	v_mfma_f32_32x32x16_f16 v[220:235], v[168:171], v[72:75], v[220:235]
	ds_read_b128 v[168:171], v240 offset:11264
	global_store_dwordx4 v241, v[248:251], s[26:27] offset:1024 nt
	s_waitcnt lgkmcnt(14)
	v_mfma_f32_32x32x16_f16 v[220:235], v[172:175], v[76:79], v[220:235]
	ds_read_b128 v[172:175], v240 offset:12288
	s_waitcnt lgkmcnt(14)
	v_mfma_f32_32x32x16_f16 v[220:235], v[176:179], v[80:83], v[220:235]
	ds_read_b128 v[176:179], v240 offset:13312
	s_waitcnt lgkmcnt(14)
	v_mfma_f32_32x32x16_f16 v[220:235], v[180:183], v[84:87], v[220:235]
	ds_read_b128 v[180:183], v240 offset:14336
	s_waitcnt lgkmcnt(14)
	v_mfma_f32_32x32x16_f16 v[220:235], v[184:187], v[88:91], v[220:235]
	ds_read_b128 v[184:187], v240 offset:15360
	s_waitcnt lgkmcnt(14)
	v_mfma_f32_32x32x16_f16 v[220:235], v[188:191], v[92:95], v[220:235]
	ds_read_b128 v[188:191], v240 offset:16384
	s_waitcnt lgkmcnt(14)
	v_mfma_f32_32x32x16_f16 v[220:235], v[192:195], v[96:99], v[220:235]
	ds_read_b128 v[192:195], v240 offset:17408
	s_waitcnt lgkmcnt(14)
	v_mfma_f32_32x32x16_f16 v[220:235], v[196:199], v[100:103], v[220:235]
	ds_read_b128 v[196:199], v240 offset:18432
	s_waitcnt lgkmcnt(14)
	v_mfma_f32_32x32x16_f16 v[220:235], v[200:203], v[104:107], v[220:235]
	ds_read_b128 v[200:203], v240 offset:19456
	s_waitcnt lgkmcnt(14)
	v_mfma_f32_32x32x16_f16 v[220:235], v[204:207], v[108:111], v[220:235]
	ds_read_b128 v[204:207], v240 offset:20480
	s_waitcnt lgkmcnt(14)
	v_mfma_f32_32x32x16_f16 v[220:235], v[208:211], v[112:115], v[220:235]
	ds_read_b128 v[208:211], v240 offset:21504
	s_waitcnt lgkmcnt(14)
	v_mfma_f32_32x32x16_f16 v[220:235], v[212:215], v[116:119], v[220:235]
	ds_read_b128 v[212:215], v240 offset:22528
	s_waitcnt lgkmcnt(14)
	v_mfma_f32_32x32x16_f16 v[220:235], v[216:219], v[120:123], v[220:235]
	ds_read_b128 v[216:219], v240 offset:23552
	s_waitcnt lgkmcnt(14)
	v_mfma_f32_32x32x16_f16 v[0:15], v[124:127], v[28:31], 0
	s_waitcnt lgkmcnt(14)
	v_mfma_f32_32x32x16_f16 v[0:15], v[128:131], v[32:35], v[0:15]
	s_add_i32 s20, s14, 7
	s_cmp_lt_u32 s20, 12
	s_cselect_b32 s26, s8, s10
	s_cselect_b32 s27, s9, s11
	s_waitcnt lgkmcnt(14)
	v_mfma_f32_32x32x16_f16 v[0:15], v[132:135], v[36:39], v[0:15]
	s_cselect_b32 s21, 0, 12
	s_cmp_lt_u32 s20, 24
	s_cselect_b32 s26, s26, s0
	s_cselect_b32 s27, s27, s1
	s_waitcnt lgkmcnt(14)
	v_mfma_f32_32x32x16_f16 v[0:15], v[136:139], v[40:43], v[0:15]
	s_cselect_b32 s21, s21, 24
	s_sub_i32 s20, s20, s21
	s_lshr_b32 s21, s20, 1
	s_and_b32 s20, s20, 1
	s_waitcnt lgkmcnt(14)
	v_mfma_f32_32x32x16_f16 v[0:15], v[140:143], v[44:47], v[0:15]
	s_add_i32 s21, s21, s15
	s_lshl_b32 s21, s21, 15
	s_lshl_b32 s20, s20, 11
	s_add_i32 s21, s21, s20
	s_waitcnt lgkmcnt(14)
	v_mfma_f32_32x32x16_f16 v[0:15], v[144:147], v[48:51], v[0:15]
	s_add_u32 s26, s26, s21
	s_addc_u32 s27, s27, 0
	s_waitcnt lgkmcnt(14)
	v_mfma_f32_32x32x16_f16 v[0:15], v[148:151], v[52:55], v[0:15]
	v_cvt_pk_f16_f32 v244, v220, v221
	v_cvt_pk_f16_f32 v245, v222, v223
	s_waitcnt lgkmcnt(14)
	v_mfma_f32_32x32x16_f16 v[0:15], v[152:155], v[56:59], v[0:15]
	v_cvt_pk_f16_f32 v246, v224, v225
	v_cvt_pk_f16_f32 v247, v226, v227
	s_waitcnt lgkmcnt(14)
	v_mfma_f32_32x32x16_f16 v[0:15], v[156:159], v[60:63], v[0:15]
	v_cvt_pk_f16_f32 v248, v228, v229
	v_cvt_pk_f16_f32 v249, v230, v231
	s_waitcnt lgkmcnt(14)
	v_mfma_f32_32x32x16_f16 v[0:15], v[160:163], v[64:67], v[0:15]
	v_cvt_pk_f16_f32 v250, v232, v233
	v_cvt_pk_f16_f32 v251, v234, v235
	s_waitcnt lgkmcnt(13)
	v_mfma_f32_32x32x16_f16 v[0:15], v[164:167], v[68:71], v[0:15]
	global_store_dwordx4 v241, v[244:247], s[26:27] nt
	s_waitcnt lgkmcnt(12)
	v_mfma_f32_32x32x16_f16 v[0:15], v[168:171], v[72:75], v[0:15]
	global_store_dwordx4 v241, v[248:251], s[26:27] offset:1024 nt
	s_waitcnt lgkmcnt(11)
	v_mfma_f32_32x32x16_f16 v[0:15], v[172:175], v[76:79], v[0:15]
	s_waitcnt lgkmcnt(10)
	v_mfma_f32_32x32x16_f16 v[0:15], v[176:179], v[80:83], v[0:15]
	s_waitcnt lgkmcnt(9)
	v_mfma_f32_32x32x16_f16 v[0:15], v[180:183], v[84:87], v[0:15]
	s_waitcnt lgkmcnt(8)
	v_mfma_f32_32x32x16_f16 v[0:15], v[184:187], v[88:91], v[0:15]
	s_waitcnt lgkmcnt(7)
	v_mfma_f32_32x32x16_f16 v[0:15], v[188:191], v[92:95], v[0:15]
	s_waitcnt lgkmcnt(6)
	v_mfma_f32_32x32x16_f16 v[0:15], v[192:195], v[96:99], v[0:15]
	s_waitcnt lgkmcnt(5)
	v_mfma_f32_32x32x16_f16 v[0:15], v[196:199], v[100:103], v[0:15]
	s_waitcnt lgkmcnt(4)
	v_mfma_f32_32x32x16_f16 v[0:15], v[200:203], v[104:107], v[0:15]
	s_waitcnt lgkmcnt(3)
	v_mfma_f32_32x32x16_f16 v[0:15], v[204:207], v[108:111], v[0:15]
	s_waitcnt lgkmcnt(2)
	v_mfma_f32_32x32x16_f16 v[0:15], v[208:211], v[112:115], v[0:15]
	s_waitcnt lgkmcnt(1)
	v_mfma_f32_32x32x16_f16 v[0:15], v[212:215], v[116:119], v[0:15]
	s_waitcnt lgkmcnt(0)
	v_mfma_f32_32x32x16_f16 v[0:15], v[216:219], v[120:123], v[0:15]
	s_add_i32 s20, s14, 8
	s_cmp_lt_u32 s20, 12
	s_cselect_b32 s26, s8, s10
	s_cselect_b32 s27, s9, s11
	s_cselect_b32 s21, 0, 12
	s_cmp_lt_u32 s20, 24
	s_cselect_b32 s26, s26, s0
	s_cselect_b32 s27, s27, s1
	s_cselect_b32 s21, s21, 24
	s_sub_i32 s20, s20, s21
	s_lshr_b32 s21, s20, 1
	s_and_b32 s20, s20, 1
	s_add_i32 s21, s21, s15
	s_lshl_b32 s21, s21, 15
	s_lshl_b32 s20, s20, 11
	s_add_i32 s21, s21, s20
	s_add_u32 s26, s26, s21
	s_addc_u32 s27, s27, 0
	s_nop 7
	v_cvt_pk_f16_f32 v244, v0, v1
	v_cvt_pk_f16_f32 v245, v2, v3
	v_cvt_pk_f16_f32 v246, v4, v5
	v_cvt_pk_f16_f32 v247, v6, v7
	v_cvt_pk_f16_f32 v248, v8, v9
	v_cvt_pk_f16_f32 v249, v10, v11
	v_cvt_pk_f16_f32 v250, v12, v13
	v_cvt_pk_f16_f32 v251, v14, v15
	global_store_dwordx4 v241, v[244:247], s[26:27] nt
	global_store_dwordx4 v241, v[248:251], s[26:27] offset:1024 nt
	s_endpgm
.Lqkv_bodyN:
	ds_read_b128 v[124:127], v239 offset:0
	ds_read_b128 v[128:131], v239 offset:1024
	ds_read_b128 v[132:135], v239 offset:2048
	ds_read_b128 v[136:139], v239 offset:3072
	ds_read_b128 v[140:143], v239 offset:4096
	ds_read_b128 v[144:147], v239 offset:5120
	ds_read_b128 v[148:151], v239 offset:6144
	ds_read_b128 v[152:155], v239 offset:7168
	ds_read_b128 v[156:159], v239 offset:8192
	ds_read_b128 v[160:163], v239 offset:9216
	ds_read_b128 v[164:167], v239 offset:10240
	ds_read_b128 v[168:171], v239 offset:11264
	ds_read_b128 v[172:175], v239 offset:12288
	ds_read_b128 v[176:179], v239 offset:13312
	ds_read_b128 v[180:183], v239 offset:14336
	ds_read_b128 v[184:187], v239 offset:15360
	ds_read_b128 v[188:191], v239 offset:16384
	ds_read_b128 v[192:195], v239 offset:17408
	ds_read_b128 v[196:199], v239 offset:18432
	ds_read_b128 v[200:203], v239 offset:19456
	ds_read_b128 v[204:207], v239 offset:20480
	ds_read_b128 v[208:211], v239 offset:21504
	ds_read_b128 v[212:215], v239 offset:22528
	ds_read_b128 v[216:219], v239 offset:23552
	s_add_u32 s24, s22, 49152
	s_addc_u32 s25, s23, 0
	s_waitcnt lgkmcnt(14)
	v_mfma_f32_32x32x16_f16 v[0:15], v[28:31], v[124:127], 0
	ds_read_b128 v[124:127], v239 offset:24576
	global_load_dwordx4 v[16:19], v236, s[24:25]
	global_load_dwordx4 v[20:23], v237, s[24:25]
	global_load_dwordx4 v[24:27], v238, s[24:25]
	s_waitcnt lgkmcnt(14)
	v_mfma_f32_32x32x16_f16 v[0:15], v[32:35], v[128:131], v[0:15]
	ds_read_b128 v[128:131], v239 offset:25600
	s_waitcnt lgkmcnt(14)
	v_mfma_f32_32x32x16_f16 v[0:15], v[36:39], v[132:135], v[0:15]
	ds_read_b128 v[132:135], v239 offset:26624
	s_waitcnt lgkmcnt(14)
	v_mfma_f32_32x32x16_f16 v[0:15], v[40:43], v[136:139], v[0:15]
	ds_read_b128 v[136:139], v239 offset:27648
	s_waitcnt lgkmcnt(14)
	v_mfma_f32_32x32x16_f16 v[0:15], v[44:47], v[140:143], v[0:15]
	ds_read_b128 v[140:143], v239 offset:28672
	s_waitcnt lgkmcnt(14)
	v_mfma_f32_32x32x16_f16 v[0:15], v[48:51], v[144:147], v[0:15]
	ds_read_b128 v[144:147], v239 offset:29696
	s_waitcnt lgkmcnt(14)
	v_mfma_f32_32x32x16_f16 v[0:15], v[52:55], v[148:151], v[0:15]
	ds_read_b128 v[148:151], v239 offset:30720
	s_waitcnt lgkmcnt(14)
	v_mfma_f32_32x32x16_f16 v[0:15], v[56:59], v[152:155], v[0:15]
	ds_read_b128 v[152:155], v239 offset:31744
	s_waitcnt lgkmcnt(14)
	v_mfma_f32_32x32x16_f16 v[0:15], v[60:63], v[156:159], v[0:15]
	ds_read_b128 v[156:159], v239 offset:32768
	s_waitcnt lgkmcnt(14)
	v_mfma_f32_32x32x16_f16 v[0:15], v[64:67], v[160:163], v[0:15]
	ds_read_b128 v[160:163], v239 offset:33792
	s_waitcnt lgkmcnt(14)
	v_mfma_f32_32x32x16_f16 v[0:15], v[68:71], v[164:167], v[0:15]
	ds_read_b128 v[164:167], v239 offset:34816
	s_waitcnt lgkmcnt(14)
	v_mfma_f32_32x32x16_f16 v[0:15], v[72:75], v[168:171], v[0:15]
	ds_read_b128 v[168:171], v239 offset:35840
	s_waitcnt lgkmcnt(14)
	v_mfma_f32_32x32x16_f16 v[0:15], v[76:79], v[172:175], v[0:15]
	ds_read_b128 v[172:175], v239 offset:36864
	s_waitcnt lgkmcnt(14)
	v_mfma_f32_32x32x16_f16 v[0:15], v[80:83], v[176:179], v[0:15]
	ds_read_b128 v[176:179], v239 offset:37888
	s_waitcnt lgkmcnt(14)
	v_mfma_f32_32x32x16_f16 v[0:15], v[84:87], v[180:183], v[0:15]
	ds_read_b128 v[180:183], v239 offset:38912
	s_waitcnt lgkmcnt(14)
	v_mfma_f32_32x32x16_f16 v[0:15], v[88:91], v[184:187], v[0:15]
	ds_read_b128 v[184:187], v239 offset:39936
	s_waitcnt lgkmcnt(14)
	v_mfma_f32_32x32x16_f16 v[0:15], v[92:95], v[188:191], v[0:15]
	ds_read_b128 v[188:191], v239 offset:40960
	s_waitcnt lgkmcnt(14)
	v_mfma_f32_32x32x16_f16 v[0:15], v[96:99], v[192:195], v[0:15]
	ds_read_b128 v[192:195], v239 offset:41984
	s_waitcnt lgkmcnt(14)
	v_mfma_f32_32x32x16_f16 v[0:15], v[100:103], v[196:199], v[0:15]
	ds_read_b128 v[196:199], v239 offset:43008
	s_waitcnt vmcnt(0)
	ds_write_b128 v236, v[16:19] offset:49152
	ds_write_b128 v237, v[20:23] offset:49152
	ds_write_b128 v238, v[24:27] offset:49152
	s_waitcnt lgkmcnt(14)
	v_mfma_f32_32x32x16_f16 v[0:15], v[104:107], v[200:203], v[0:15]
	ds_read_b128 v[200:203], v239 offset:44032
	s_waitcnt lgkmcnt(14)
	v_mfma_f32_32x32x16_f16 v[0:15], v[108:111], v[204:207], v[0:15]
	ds_read_b128 v[204:207], v239 offset:45056
	s_waitcnt lgkmcnt(14)
	v_mfma_f32_32x32x16_f16 v[0:15], v[112:115], v[208:211], v[0:15]
	ds_read_b128 v[208:211], v239 offset:46080
	s_waitcnt lgkmcnt(14)
	v_mfma_f32_32x32x16_f16 v[0:15], v[116:119], v[212:215], v[0:15]
	ds_read_b128 v[212:215], v239 offset:47104
	s_waitcnt lgkmcnt(14)
	v_mfma_f32_32x32x16_f16 v[0:15], v[120:123], v[216:219], v[0:15]
	ds_read_b128 v[216:219], v239 offset:48128
	s_waitcnt lgkmcnt(5)
	s_barrier
	s_add_u32 s24, s22, 73728
	s_addc_u32 s25, s23, 0
	s_waitcnt lgkmcnt(14)
	v_mfma_f32_32x32x16_f16 v[220:235], v[28:31], v[124:127], 0
	ds_read_b128 v[124:127], v240 offset:0
	global_load_dwordx4 v[16:19], v236, s[24:25]
	global_load_dwordx4 v[20:23], v237, s[24:25]
	global_load_dwordx4 v[24:27], v238, s[24:25]
	s_waitcnt lgkmcnt(14)
	v_mfma_f32_32x32x16_f16 v[220:235], v[32:35], v[128:131], v[220:235]
	ds_read_b128 v[128:131], v240 offset:1024
	s_add_i32 s20, s14, 0
	s_cmp_lt_u32 s20, 12
	s_cselect_b32 s26, s8, s10
	s_cselect_b32 s27, s9, s11
	s_waitcnt lgkmcnt(14)
	v_mfma_f32_32x32x16_f16 v[220:235], v[36:39], v[132:135], v[220:235]
	ds_read_b128 v[132:135], v240 offset:2048
	s_cselect_b32 s21, 0, 12
	s_cmp_lt_u32 s20, 24
	s_cselect_b32 s26, s26, s0
	s_cselect_b32 s27, s27, s1
	s_waitcnt lgkmcnt(14)
	v_mfma_f32_32x32x16_f16 v[220:235], v[40:43], v[136:139], v[220:235]
	ds_read_b128 v[136:139], v240 offset:3072
	s_cselect_b32 s21, s21, 24
	s_sub_i32 s20, s20, s21
	s_lshr_b32 s21, s20, 1
	s_and_b32 s20, s20, 1
	s_waitcnt lgkmcnt(14)
	v_mfma_f32_32x32x16_f16 v[220:235], v[44:47], v[140:143], v[220:235]
	ds_read_b128 v[140:143], v240 offset:4096
	s_add_i32 s21, s21, s15
	s_lshl_b32 s21, s21, 15
	s_lshl_b32 s20, s20, 11
	s_add_i32 s21, s21, s20
	s_waitcnt lgkmcnt(14)
	v_mfma_f32_32x32x16_f16 v[220:235], v[48:51], v[144:147], v[220:235]
	ds_read_b128 v[144:147], v240 offset:5120
	s_add_u32 s26, s26, s21
	s_addc_u32 s27, s27, 0
	s_waitcnt lgkmcnt(14)
	v_mfma_f32_32x32x16_f16 v[220:235], v[52:55], v[148:151], v[220:235]
	ds_read_b128 v[148:151], v240 offset:6144
	v_cvt_pk_f16_f32 v244, v0, v1
	v_cvt_pk_f16_f32 v245, v2, v3
	s_waitcnt lgkmcnt(14)
	v_mfma_f32_32x32x16_f16 v[220:235], v[56:59], v[152:155], v[220:235]
	ds_read_b128 v[152:155], v240 offset:7168
	v_cvt_pk_f16_f32 v246, v4, v5
	v_cvt_pk_f16_f32 v247, v6, v7
	s_waitcnt lgkmcnt(14)
	v_mfma_f32_32x32x16_f16 v[220:235], v[60:63], v[156:159], v[220:235]
	ds_read_b128 v[156:159], v240 offset:8192
	v_cvt_pk_f16_f32 v248, v8, v9
	v_cvt_pk_f16_f32 v249, v10, v11
	s_waitcnt lgkmcnt(14)
	v_mfma_f32_32x32x16_f16 v[220:235], v[64:67], v[160:163], v[220:235]
	ds_read_b128 v[160:163], v240 offset:9216
	v_cvt_pk_f16_f32 v250, v12, v13
	v_cvt_pk_f16_f32 v251, v14, v15
	s_waitcnt lgkmcnt(14)
	v_mfma_f32_32x32x16_f16 v[220:235], v[68:71], v[164:167], v[220:235]
	ds_read_b128 v[164:167], v240 offset:10240
	global_store_dwordx4 v241, v[244:247], s[26:27] nt
	s_waitcnt lgkmcnt(14)
	v_mfma_f32_32x32x16_f16 v[220:235], v[72:75], v[168:171], v[220:235]
	ds_read_b128 v[168:171], v240 offset:11264
	global_store_dwordx4 v241, v[248:251], s[26:27] offset:1024 nt
	s_waitcnt lgkmcnt(14)
	v_mfma_f32_32x32x16_f16 v[220:235], v[76:79], v[172:175], v[220:235]
	ds_read_b128 v[172:175], v240 offset:12288
	s_waitcnt lgkmcnt(14)
	v_mfma_f32_32x32x16_f16 v[220:235], v[80:83], v[176:179], v[220:235]
	ds_read_b128 v[176:179], v240 offset:13312
	s_waitcnt lgkmcnt(14)
	v_mfma_f32_32x32x16_f16 v[220:235], v[84:87], v[180:183], v[220:235]
	ds_read_b128 v[180:183], v240 offset:14336
	s_waitcnt lgkmcnt(14)
	v_mfma_f32_32x32x16_f16 v[220:235], v[88:91], v[184:187], v[220:235]
	ds_read_b128 v[184:187], v240 offset:15360
	s_waitcnt lgkmcnt(14)
	v_mfma_f32_32x32x16_f16 v[220:235], v[92:95], v[188:191], v[220:235]
	ds_read_b128 v[188:191], v240 offset:16384
	s_waitcnt lgkmcnt(14)
	v_mfma_f32_32x32x16_f16 v[220:235], v[96:99], v[192:195], v[220:235]
	ds_read_b128 v[192:195], v240 offset:17408
	s_waitcnt lgkmcnt(14)
	v_mfma_f32_32x32x16_f16 v[220:235], v[100:103], v[196:199], v[220:235]
	ds_read_b128 v[196:199], v240 offset:18432
	s_waitcnt vmcnt(2)
	ds_write_b128 v236, v[16:19] offset:0
	ds_write_b128 v237, v[20:23] offset:0
	ds_write_b128 v238, v[24:27] offset:0
	s_waitcnt lgkmcnt(14)
	v_mfma_f32_32x32x16_f16 v[220:235], v[104:107], v[200:203], v[220:235]
	ds_read_b128 v[200:203], v240 offset:19456
	s_waitcnt lgkmcnt(14)
	v_mfma_f32_32x32x16_f16 v[220:235], v[108:111], v[204:207], v[220:235]
	ds_read_b128 v[204:207], v240 offset:20480
	s_waitcnt lgkmcnt(14)
	v_mfma_f32_32x32x16_f16 v[220:235], v[112:115], v[208:211], v[220:235]
	ds_read_b128 v[208:211], v240 offset:21504
	s_waitcnt lgkmcnt(14)
	v_mfma_f32_32x32x16_f16 v[220:235], v[116:119], v[212:215], v[220:235]
	ds_read_b128 v[212:215], v240 offset:22528
	s_waitcnt lgkmcnt(14)
	v_mfma_f32_32x32x16_f16 v[220:235], v[120:123], v[216:219], v[220:235]
	ds_read_b128 v[216:219], v240 offset:23552
	s_waitcnt lgkmcnt(5)
	s_barrier
	s_add_u32 s24, s22, 98304
	s_addc_u32 s25, s23, 0
	s_waitcnt lgkmcnt(14)
	v_mfma_f32_32x32x16_f16 v[0:15], v[28:31], v[124:127], 0
	ds_read_b128 v[124:127], v239 offset:0
	global_load_dwordx4 v[16:19], v236, s[24:25]
	global_load_dwordx4 v[20:23], v237, s[24:25]
	global_load_dwordx4 v[24:27], v238, s[24:25]
	s_waitcnt lgkmcnt(14)
	v_mfma_f32_32x32x16_f16 v[0:15], v[32:35], v[128:131], v[0:15]
	ds_read_b128 v[128:131], v239 offset:1024
	s_add_i32 s20, s14, 1
	s_cmp_lt_u32 s20, 12
	s_cselect_b32 s26, s8, s10
	s_cselect_b32 s27, s9, s11
	s_waitcnt lgkmcnt(14)
	v_mfma_f32_32x32x16_f16 v[0:15], v[36:39], v[132:135], v[0:15]
	ds_read_b128 v[132:135], v239 offset:2048
	s_cselect_b32 s21, 0, 12
	s_cmp_lt_u32 s20, 24
	s_cselect_b32 s26, s26, s0
	s_cselect_b32 s27, s27, s1
	s_waitcnt lgkmcnt(14)
	v_mfma_f32_32x32x16_f16 v[0:15], v[40:43], v[136:139], v[0:15]
	ds_read_b128 v[136:139], v239 offset:3072
	s_cselect_b32 s21, s21, 24
	s_sub_i32 s20, s20, s21
	s_lshr_b32 s21, s20, 1
	s_and_b32 s20, s20, 1
	s_waitcnt lgkmcnt(14)
	v_mfma_f32_32x32x16_f16 v[0:15], v[44:47], v[140:143], v[0:15]
	ds_read_b128 v[140:143], v239 offset:4096
	s_add_i32 s21, s21, s15
	s_lshl_b32 s21, s21, 15
	s_lshl_b32 s20, s20, 11
	s_add_i32 s21, s21, s20
	s_waitcnt lgkmcnt(14)
	v_mfma_f32_32x32x16_f16 v[0:15], v[48:51], v[144:147], v[0:15]
	ds_read_b128 v[144:147], v239 offset:5120
	s_add_u32 s26, s26, s21
	s_addc_u32 s27, s27, 0
	s_waitcnt lgkmcnt(14)
	v_mfma_f32_32x32x16_f16 v[0:15], v[52:55], v[148:151], v[0:15]
	ds_read_b128 v[148:151], v239 offset:6144
	v_cvt_pk_f16_f32 v244, v220, v221
	v_cvt_pk_f16_f32 v245, v222, v223
	s_waitcnt lgkmcnt(14)
	v_mfma_f32_32x32x16_f16 v[0:15], v[56:59], v[152:155], v[0:15]
	ds_read_b128 v[152:155], v239 offset:7168
	v_cvt_pk_f16_f32 v246, v224, v225
	v_cvt_pk_f16_f32 v247, v226, v227
	s_waitcnt lgkmcnt(14)
	v_mfma_f32_32x32x16_f16 v[0:15], v[60:63], v[156:159], v[0:15]
	ds_read_b128 v[156:159], v239 offset:8192
	v_cvt_pk_f16_f32 v248, v228, v229
	v_cvt_pk_f16_f32 v249, v230, v231
	s_waitcnt lgkmcnt(14)
	v_mfma_f32_32x32x16_f16 v[0:15], v[64:67], v[160:163], v[0:15]
	ds_read_b128 v[160:163], v239 offset:9216
	v_cvt_pk_f16_f32 v250, v232, v233
	v_cvt_pk_f16_f32 v251, v234, v235
	s_waitcnt lgkmcnt(14)
	v_mfma_f32_32x32x16_f16 v[0:15], v[68:71], v[164:167], v[0:15]
	ds_read_b128 v[164:167], v239 offset:10240
	global_store_dwordx4 v241, v[244:247], s[26:27] nt
	s_waitcnt lgkmcnt(14)
	v_mfma_f32_32x32x16_f16 v[0:15], v[72:75], v[168:171], v[0:15]
	ds_read_b128 v[168:171], v239 offset:11264
	global_store_dwordx4 v241, v[248:251], s[26:27] offset:1024 nt
	s_waitcnt lgkmcnt(14)
	v_mfma_f32_32x32x16_f16 v[0:15], v[76:79], v[172:175], v[0:15]
	ds_read_b128 v[172:175], v239 offset:12288
	s_waitcnt lgkmcnt(14)
	v_mfma_f32_32x32x16_f16 v[0:15], v[80:83], v[176:179], v[0:15]
	ds_read_b128 v[176:179], v239 offset:13312
	s_waitcnt lgkmcnt(14)
	v_mfma_f32_32x32x16_f16 v[0:15], v[84:87], v[180:183], v[0:15]
	ds_read_b128 v[180:183], v239 offset:14336
	s_waitcnt lgkmcnt(14)
	v_mfma_f32_32x32x16_f16 v[0:15], v[88:91], v[184:187], v[0:15]
	ds_read_b128 v[184:187], v239 offset:15360
	s_waitcnt lgkmcnt(14)
	v_mfma_f32_32x32x16_f16 v[0:15], v[92:95], v[188:191], v[0:15]
	ds_read_b128 v[188:191], v239 offset:16384
	s_waitcnt lgkmcnt(14)
	v_mfma_f32_32x32x16_f16 v[0:15], v[96:99], v[192:195], v[0:15]
	ds_read_b128 v[192:195], v239 offset:17408
	s_waitcnt lgkmcnt(14)
	v_mfma_f32_32x32x16_f16 v[0:15], v[100:103], v[196:199], v[0:15]
	ds_read_b128 v[196:199], v239 offset:18432
	s_waitcnt vmcnt(2)
	ds_write_b128 v236, v[16:19] offset:24576
	ds_write_b128 v237, v[20:23] offset:24576
	ds_write_b128 v238, v[24:27] offset:24576
	s_waitcnt lgkmcnt(14)
	v_mfma_f32_32x32x16_f16 v[0:15], v[104:107], v[200:203], v[0:15]
	ds_read_b128 v[200:203], v239 offset:19456
	s_waitcnt lgkmcnt(14)
	v_mfma_f32_32x32x16_f16 v[0:15], v[108:111], v[204:207], v[0:15]
	ds_read_b128 v[204:207], v239 offset:20480
	s_waitcnt lgkmcnt(14)
	v_mfma_f32_32x32x16_f16 v[0:15], v[112:115], v[208:211], v[0:15]
	ds_read_b128 v[208:211], v239 offset:21504
	s_waitcnt lgkmcnt(14)
	v_mfma_f32_32x32x16_f16 v[0:15], v[116:119], v[212:215], v[0:15]
	ds_read_b128 v[212:215], v239 offset:22528
	s_waitcnt lgkmcnt(14)
	v_mfma_f32_32x32x16_f16 v[0:15], v[120:123], v[216:219], v[0:15]
	ds_read_b128 v[216:219], v239 offset:23552
	s_waitcnt lgkmcnt(5)
	s_barrier
	s_add_u32 s24, s22, 122880
	s_addc_u32 s25, s23, 0
	s_waitcnt lgkmcnt(14)
	v_mfma_f32_32x32x16_f16 v[220:235], v[28:31], v[124:127], 0
	ds_read_b128 v[124:127], v239 offset:24576
	global_load_dwordx4 v[16:19], v236, s[24:25]
	global_load_dwordx4 v[20:23], v237, s[24:25]
	global_load_dwordx4 v[24:27], v238, s[24:25]
	s_waitcnt lgkmcnt(14)
	v_mfma_f32_32x32x16_f16 v[220:235], v[32:35], v[128:131], v[220:235]
	ds_read_b128 v[128:131], v239 offset:25600
	s_add_i32 s20, s14, 2
	s_cmp_lt_u32 s20, 12
	s_cselect_b32 s26, s8, s10
	s_cselect_b32 s27, s9, s11
	s_waitcnt lgkmcnt(14)
	v_mfma_f32_32x32x16_f16 v[220:235], v[36:39], v[132:135], v[220:235]
	ds_read_b128 v[132:135], v239 offset:26624
	s_cselect_b32 s21, 0, 12
	s_cmp_lt_u32 s20, 24
	s_cselect_b32 s26, s26, s0
	s_cselect_b32 s27, s27, s1
	s_waitcnt lgkmcnt(14)
	v_mfma_f32_32x32x16_f16 v[220:235], v[40:43], v[136:139], v[220:235]
	ds_read_b128 v[136:139], v239 offset:27648
	s_cselect_b32 s21, s21, 24
	s_sub_i32 s20, s20, s21
	s_lshr_b32 s21, s20, 1
	s_and_b32 s20, s20, 1
	s_waitcnt lgkmcnt(14)
	v_mfma_f32_32x32x16_f16 v[220:235], v[44:47], v[140:143], v[220:235]
	ds_read_b128 v[140:143], v239 offset:28672
	s_add_i32 s21, s21, s15
	s_lshl_b32 s21, s21, 15
	s_lshl_b32 s20, s20, 11
	s_add_i32 s21, s21, s20
	s_waitcnt lgkmcnt(14)
	v_mfma_f32_32x32x16_f16 v[220:235], v[48:51], v[144:147], v[220:235]
	ds_read_b128 v[144:147], v239 offset:29696
	s_add_u32 s26, s26, s21
	s_addc_u32 s27, s27, 0
	s_waitcnt lgkmcnt(14)
	v_mfma_f32_32x32x16_f16 v[220:235], v[52:55], v[148:151], v[220:235]
	ds_read_b128 v[148:151], v239 offset:30720
	v_cvt_pk_f16_f32 v244, v0, v1
	v_cvt_pk_f16_f32 v245, v2, v3
	s_waitcnt lgkmcnt(14)
	v_mfma_f32_32x32x16_f16 v[220:235], v[56:59], v[152:155], v[220:235]
	ds_read_b128 v[152:155], v239 offset:31744
	v_cvt_pk_f16_f32 v246, v4, v5
	v_cvt_pk_f16_f32 v247, v6, v7
	s_waitcnt lgkmcnt(14)
	v_mfma_f32_32x32x16_f16 v[220:235], v[60:63], v[156:159], v[220:235]
	ds_read_b128 v[156:159], v239 offset:32768
	v_cvt_pk_f16_f32 v248, v8, v9
	v_cvt_pk_f16_f32 v249, v10, v11
	s_waitcnt lgkmcnt(14)
	v_mfma_f32_32x32x16_f16 v[220:235], v[64:67], v[160:163], v[220:235]
	ds_read_b128 v[160:163], v239 offset:33792
	v_cvt_pk_f16_f32 v250, v12, v13
	v_cvt_pk_f16_f32 v251, v14, v15
	s_waitcnt lgkmcnt(14)
	v_mfma_f32_32x32x16_f16 v[220:235], v[68:71], v[164:167], v[220:235]
	ds_read_b128 v[164:167], v239 offset:34816
	global_store_dwordx4 v241, v[244:247], s[26:27] nt
	s_waitcnt lgkmcnt(14)
	v_mfma_f32_32x32x16_f16 v[220:235], v[72:75], v[168:171], v[220:235]
	ds_read_b128 v[168:171], v239 offset:35840
	global_store_dwordx4 v241, v[248:251], s[26:27] offset:1024 nt
	s_waitcnt lgkmcnt(14)
	v_mfma_f32_32x32x16_f16 v[220:235], v[76:79], v[172:175], v[220:235]
	ds_read_b128 v[172:175], v239 offset:36864
	s_waitcnt lgkmcnt(14)
	v_mfma_f32_32x32x16_f16 v[220:235], v[80:83], v[176:179], v[220:235]
	ds_read_b128 v[176:179], v239 offset:37888
	s_waitcnt lgkmcnt(14)
	v_mfma_f32_32x32x16_f16 v[220:235], v[84:87], v[180:183], v[220:235]
	ds_read_b128 v[180:183], v239 offset:38912
	s_waitcnt lgkmcnt(14)
	v_mfma_f32_32x32x16_f16 v[220:235], v[88:91], v[184:187], v[220:235]
	ds_read_b128 v[184:187], v239 offset:39936
	s_waitcnt lgkmcnt(14)
	v_mfma_f32_32x32x16_f16 v[220:235], v[92:95], v[188:191], v[220:235]
	ds_read_b128 v[188:191], v239 offset:40960
	s_waitcnt lgkmcnt(14)
	v_mfma_f32_32x32x16_f16 v[220:235], v[96:99], v[192:195], v[220:235]
	ds_read_b128 v[192:195], v239 offset:41984
	s_waitcnt lgkmcnt(14)
	v_mfma_f32_32x32x16_f16 v[220:235], v[100:103], v[196:199], v[220:235]
	ds_read_b128 v[196:199], v239 offset:43008
	s_waitcnt vmcnt(2)
	ds_write_b128 v236, v[16:19] offset:49152
	ds_write_b128 v237, v[20:23] offset:49152
	ds_write_b128 v238, v[24:27] offset:49152
	s_waitcnt lgkmcnt(14)
	v_mfma_f32_32x32x16_f16 v[220:235], v[104:107], v[200:203], v[220:235]
	ds_read_b128 v[200:203], v239 offset:44032
	s_waitcnt lgkmcnt(14)
	v_mfma_f32_32x32x16_f16 v[220:235], v[108:111], v[204:207], v[220:235]
	ds_read_b128 v[204:207], v239 offset:45056
	s_waitcnt lgkmcnt(14)
	v_mfma_f32_32x32x16_f16 v[220:235], v[112:115], v[208:211], v[220:235]
	ds_read_b128 v[208:211], v239 offset:46080
	s_waitcnt lgkmcnt(14)
	v_mfma_f32_32x32x16_f16 v[220:235], v[116:119], v[212:215], v[220:235]
	ds_read_b128 v[212:215], v239 offset:47104
	s_waitcnt lgkmcnt(14)
	v_mfma_f32_32x32x16_f16 v[220:235], v[120:123], v[216:219], v[220:235]
	ds_read_b128 v[216:219], v239 offset:48128
	s_waitcnt lgkmcnt(5)
	s_barrier
	s_add_u32 s24, s22, 147456
	s_addc_u32 s25, s23, 0
	s_waitcnt lgkmcnt(14)
	v_mfma_f32_32x32x16_f16 v[0:15], v[28:31], v[124:127], 0
	ds_read_b128 v[124:127], v240 offset:0
	global_load_dwordx4 v[16:19], v236, s[24:25]
	global_load_dwordx4 v[20:23], v237, s[24:25]
	global_load_dwordx4 v[24:27], v238, s[24:25]
	s_waitcnt lgkmcnt(14)
	v_mfma_f32_32x32x16_f16 v[0:15], v[32:35], v[128:131], v[0:15]
	ds_read_b128 v[128:131], v240 offset:1024
	s_add_i32 s20, s14, 3
	s_cmp_lt_u32 s20, 12
	s_cselect_b32 s26, s8, s10
	s_cselect_b32 s27, s9, s11
	s_waitcnt lgkmcnt(14)
	v_mfma_f32_32x32x16_f16 v[0:15], v[36:39], v[132:135], v[0:15]
	ds_read_b128 v[132:135], v240 offset:2048
	s_cselect_b32 s21, 0, 12
	s_cmp_lt_u32 s20, 24
	s_cselect_b32 s26, s26, s0
	s_cselect_b32 s27, s27, s1
	s_waitcnt lgkmcnt(14)
	v_mfma_f32_32x32x16_f16 v[0:15], v[40:43], v[136:139], v[0:15]
	ds_read_b128 v[136:139], v240 offset:3072
	s_cselect_b32 s21, s21, 24
	s_sub_i32 s20, s20, s21
	s_lshr_b32 s21, s20, 1
	s_and_b32 s20, s20, 1
	s_waitcnt lgkmcnt(14)
	v_mfma_f32_32x32x16_f16 v[0:15], v[44:47], v[140:143], v[0:15]
	ds_read_b128 v[140:143], v240 offset:4096
	s_add_i32 s21, s21, s15
	s_lshl_b32 s21, s21, 15
	s_lshl_b32 s20, s20, 11
	s_add_i32 s21, s21, s20
	s_waitcnt lgkmcnt(14)
	v_mfma_f32_32x32x16_f16 v[0:15], v[48:51], v[144:147], v[0:15]
	ds_read_b128 v[144:147], v240 offset:5120
	s_add_u32 s26, s26, s21
	s_addc_u32 s27, s27, 0
	s_waitcnt lgkmcnt(14)
	v_mfma_f32_32x32x16_f16 v[0:15], v[52:55], v[148:151], v[0:15]
	ds_read_b128 v[148:151], v240 offset:6144
	v_cvt_pk_f16_f32 v244, v220, v221
	v_cvt_pk_f16_f32 v245, v222, v223
	s_waitcnt lgkmcnt(14)
	v_mfma_f32_32x32x16_f16 v[0:15], v[56:59], v[152:155], v[0:15]
	ds_read_b128 v[152:155], v240 offset:7168
	v_cvt_pk_f16_f32 v246, v224, v225
	v_cvt_pk_f16_f32 v247, v226, v227
	s_waitcnt lgkmcnt(14)
	v_mfma_f32_32x32x16_f16 v[0:15], v[60:63], v[156:159], v[0:15]
	ds_read_b128 v[156:159], v240 offset:8192
	v_cvt_pk_f16_f32 v248, v228, v229
	v_cvt_pk_f16_f32 v249, v230, v231
	s_waitcnt lgkmcnt(14)
	v_mfma_f32_32x32x16_f16 v[0:15], v[64:67], v[160:163], v[0:15]
	ds_read_b128 v[160:163], v240 offset:9216
	v_cvt_pk_f16_f32 v250, v232, v233
	v_cvt_pk_f16_f32 v251, v234, v235
	s_waitcnt lgkmcnt(14)
	v_mfma_f32_32x32x16_f16 v[0:15], v[68:71], v[164:167], v[0:15]
	ds_read_b128 v[164:167], v240 offset:10240
	global_store_dwordx4 v241, v[244:247], s[26:27] nt
	s_waitcnt lgkmcnt(14)
	v_mfma_f32_32x32x16_f16 v[0:15], v[72:75], v[168:171], v[0:15]
	ds_read_b128 v[168:171], v240 offset:11264
	global_store_dwordx4 v241, v[248:251], s[26:27] offset:1024 nt
	s_waitcnt lgkmcnt(14)
	v_mfma_f32_32x32x16_f16 v[0:15], v[76:79], v[172:175], v[0:15]
	ds_read_b128 v[172:175], v240 offset:12288
	s_waitcnt lgkmcnt(14)
	v_mfma_f32_32x32x16_f16 v[0:15], v[80:83], v[176:179], v[0:15]
	ds_read_b128 v[176:179], v240 offset:13312
	s_waitcnt lgkmcnt(14)
	v_mfma_f32_32x32x16_f16 v[0:15], v[84:87], v[180:183], v[0:15]
	ds_read_b128 v[180:183], v240 offset:14336
	s_waitcnt lgkmcnt(14)
	v_mfma_f32_32x32x16_f16 v[0:15], v[88:91], v[184:187], v[0:15]
	ds_read_b128 v[184:187], v240 offset:15360
	s_waitcnt lgkmcnt(14)
	v_mfma_f32_32x32x16_f16 v[0:15], v[92:95], v[188:191], v[0:15]
	ds_read_b128 v[188:191], v240 offset:16384
	s_waitcnt lgkmcnt(14)
	v_mfma_f32_32x32x16_f16 v[0:15], v[96:99], v[192:195], v[0:15]
	ds_read_b128 v[192:195], v240 offset:17408
	s_waitcnt lgkmcnt(14)
	v_mfma_f32_32x32x16_f16 v[0:15], v[100:103], v[196:199], v[0:15]
	ds_read_b128 v[196:199], v240 offset:18432
	s_waitcnt vmcnt(2)
	ds_write_b128 v236, v[16:19] offset:0
	ds_write_b128 v237, v[20:23] offset:0
	ds_write_b128 v238, v[24:27] offset:0
	s_waitcnt lgkmcnt(14)
	v_mfma_f32_32x32x16_f16 v[0:15], v[104:107], v[200:203], v[0:15]
	ds_read_b128 v[200:203], v240 offset:19456
	s_waitcnt lgkmcnt(14)
	v_mfma_f32_32x32x16_f16 v[0:15], v[108:111], v[204:207], v[0:15]
	ds_read_b128 v[204:207], v240 offset:20480
	s_waitcnt lgkmcnt(14)
	v_mfma_f32_32x32x16_f16 v[0:15], v[112:115], v[208:211], v[0:15]
	ds_read_b128 v[208:211], v240 offset:21504
	s_waitcnt lgkmcnt(14)
	v_mfma_f32_32x32x16_f16 v[0:15], v[116:119], v[212:215], v[0:15]
	ds_read_b128 v[212:215], v240 offset:22528
	s_waitcnt lgkmcnt(14)
	v_mfma_f32_32x32x16_f16 v[0:15], v[120:123], v[216:219], v[0:15]
	ds_read_b128 v[216:219], v240 offset:23552
	s_waitcnt lgkmcnt(5)
	s_barrier
	s_add_u32 s24, s22, 172032
	s_addc_u32 s25, s23, 0
	s_waitcnt lgkmcnt(14)
	v_mfma_f32_32x32x16_f16 v[220:235], v[28:31], v[124:127], 0
	ds_read_b128 v[124:127], v239 offset:0
	global_load_dwordx4 v[16:19], v236, s[24:25]
	global_load_dwordx4 v[20:23], v237, s[24:25]
	global_load_dwordx4 v[24:27], v238, s[24:25]
	s_waitcnt lgkmcnt(14)
	v_mfma_f32_32x32x16_f16 v[220:235], v[32:35], v[128:131], v[220:235]
	ds_read_b128 v[128:131], v239 offset:1024
	s_add_i32 s20, s14, 4
	s_cmp_lt_u32 s20, 12
	s_cselect_b32 s26, s8, s10
	s_cselect_b32 s27, s9, s11
	s_waitcnt lgkmcnt(14)
	v_mfma_f32_32x32x16_f16 v[220:235], v[36:39], v[132:135], v[220:235]
	ds_read_b128 v[132:135], v239 offset:2048
	s_cselect_b32 s21, 0, 12
	s_cmp_lt_u32 s20, 24
	s_cselect_b32 s26, s26, s0
	s_cselect_b32 s27, s27, s1
	s_waitcnt lgkmcnt(14)
	v_mfma_f32_32x32x16_f16 v[220:235], v[40:43], v[136:139], v[220:235]
	ds_read_b128 v[136:139], v239 offset:3072
	s_cselect_b32 s21, s21, 24
	s_sub_i32 s20, s20, s21
	s_lshr_b32 s21, s20, 1
	s_and_b32 s20, s20, 1
	s_waitcnt lgkmcnt(14)
	v_mfma_f32_32x32x16_f16 v[220:235], v[44:47], v[140:143], v[220:235]
	ds_read_b128 v[140:143], v239 offset:4096
	s_add_i32 s21, s21, s15
	s_lshl_b32 s21, s21, 15
	s_lshl_b32 s20, s20, 11
	s_add_i32 s21, s21, s20
	s_waitcnt lgkmcnt(14)
	v_mfma_f32_32x32x16_f16 v[220:235], v[48:51], v[144:147], v[220:235]
	ds_read_b128 v[144:147], v239 offset:5120
	s_add_u32 s26, s26, s21
	s_addc_u32 s27, s27, 0
	s_waitcnt lgkmcnt(14)
	v_mfma_f32_32x32x16_f16 v[220:235], v[52:55], v[148:151], v[220:235]
	ds_read_b128 v[148:151], v239 offset:6144
	v_cvt_pk_f16_f32 v244, v0, v1
	v_cvt_pk_f16_f32 v245, v2, v3
	s_waitcnt lgkmcnt(14)
	v_mfma_f32_32x32x16_f16 v[220:235], v[56:59], v[152:155], v[220:235]
	ds_read_b128 v[152:155], v239 offset:7168
	v_cvt_pk_f16_f32 v246, v4, v5
	v_cvt_pk_f16_f32 v247, v6, v7
	s_waitcnt lgkmcnt(14)
	v_mfma_f32_32x32x16_f16 v[220:235], v[60:63], v[156:159], v[220:235]
	ds_read_b128 v[156:159], v239 offset:8192
	v_cvt_pk_f16_f32 v248, v8, v9
	v_cvt_pk_f16_f32 v249, v10, v11
	s_waitcnt lgkmcnt(14)
	v_mfma_f32_32x32x16_f16 v[220:235], v[64:67], v[160:163], v[220:235]
	ds_read_b128 v[160:163], v239 offset:9216
	v_cvt_pk_f16_f32 v250, v12, v13
	v_cvt_pk_f16_f32 v251, v14, v15
	s_waitcnt lgkmcnt(14)
	v_mfma_f32_32x32x16_f16 v[220:235], v[68:71], v[164:167], v[220:235]
	ds_read_b128 v[164:167], v239 offset:10240
	global_store_dwordx4 v241, v[244:247], s[26:27] nt
	s_waitcnt lgkmcnt(14)
	v_mfma_f32_32x32x16_f16 v[220:235], v[72:75], v[168:171], v[220:235]
	ds_read_b128 v[168:171], v239 offset:11264
	global_store_dwordx4 v241, v[248:251], s[26:27] offset:1024 nt
	s_waitcnt lgkmcnt(14)
	v_mfma_f32_32x32x16_f16 v[220:235], v[76:79], v[172:175], v[220:235]
	ds_read_b128 v[172:175], v239 offset:12288
	s_waitcnt lgkmcnt(14)
	v_mfma_f32_32x32x16_f16 v[220:235], v[80:83], v[176:179], v[220:235]
	ds_read_b128 v[176:179], v239 offset:13312
	s_waitcnt lgkmcnt(14)
	v_mfma_f32_32x32x16_f16 v[220:235], v[84:87], v[180:183], v[220:235]
	ds_read_b128 v[180:183], v239 offset:14336
	s_waitcnt lgkmcnt(14)
	v_mfma_f32_32x32x16_f16 v[220:235], v[88:91], v[184:187], v[220:235]
	ds_read_b128 v[184:187], v239 offset:15360
	s_waitcnt lgkmcnt(14)
	v_mfma_f32_32x32x16_f16 v[220:235], v[92:95], v[188:191], v[220:235]
	ds_read_b128 v[188:191], v239 offset:16384
	s_waitcnt lgkmcnt(14)
	v_mfma_f32_32x32x16_f16 v[220:235], v[96:99], v[192:195], v[220:235]
	ds_read_b128 v[192:195], v239 offset:17408
	s_waitcnt lgkmcnt(14)
	v_mfma_f32_32x32x16_f16 v[220:235], v[100:103], v[196:199], v[220:235]
	ds_read_b128 v[196:199], v239 offset:18432
	s_waitcnt vmcnt(2)
	ds_write_b128 v236, v[16:19] offset:24576
	ds_write_b128 v237, v[20:23] offset:24576
	ds_write_b128 v238, v[24:27] offset:24576
	s_waitcnt lgkmcnt(14)
	v_mfma_f32_32x32x16_f16 v[220:235], v[104:107], v[200:203], v[220:235]
	ds_read_b128 v[200:203], v239 offset:19456
	s_waitcnt lgkmcnt(14)
	v_mfma_f32_32x32x16_f16 v[220:235], v[108:111], v[204:207], v[220:235]
	ds_read_b128 v[204:207], v239 offset:20480
	s_waitcnt lgkmcnt(14)
	v_mfma_f32_32x32x16_f16 v[220:235], v[112:115], v[208:211], v[220:235]
	ds_read_b128 v[208:211], v239 offset:21504
	s_waitcnt lgkmcnt(14)
	v_mfma_f32_32x32x16_f16 v[220:235], v[116:119], v[212:215], v[220:235]
	ds_read_b128 v[212:215], v239 offset:22528
	s_waitcnt lgkmcnt(14)
	v_mfma_f32_32x32x16_f16 v[220:235], v[120:123], v[216:219], v[220:235]
	ds_read_b128 v[216:219], v239 offset:23552
	s_waitcnt lgkmcnt(5)
	s_barrier
	s_add_u32 s24, s22, 196608
	s_addc_u32 s25, s23, 0
	s_waitcnt lgkmcnt(14)
	v_mfma_f32_32x32x16_f16 v[0:15], v[28:31], v[124:127], 0
	ds_read_b128 v[124:127], v239 offset:24576
	global_load_dwordx4 v[16:19], v236, s[24:25]
	global_load_dwordx4 v[20:23], v237, s[24:25]
	global_load_dwordx4 v[24:27], v238, s[24:25]
	s_waitcnt lgkmcnt(14)
	v_mfma_f32_32x32x16_f16 v[0:15], v[32:35], v[128:131], v[0:15]
	ds_read_b128 v[128:131], v239 offset:25600
	s_add_i32 s20, s14, 5
	s_cmp_lt_u32 s20, 12
	s_cselect_b32 s26, s8, s10
	s_cselect_b32 s27, s9, s11
	s_waitcnt lgkmcnt(14)
	v_mfma_f32_32x32x16_f16 v[0:15], v[36:39], v[132:135], v[0:15]
	ds_read_b128 v[132:135], v239 offset:26624
	s_cselect_b32 s21, 0, 12
	s_cmp_lt_u32 s20, 24
	s_cselect_b32 s26, s26, s0
	s_cselect_b32 s27, s27, s1
	s_waitcnt lgkmcnt(14)
	v_mfma_f32_32x32x16_f16 v[0:15], v[40:43], v[136:139], v[0:15]
	ds_read_b128 v[136:139], v239 offset:27648
	s_cselect_b32 s21, s21, 24
	s_sub_i32 s20, s20, s21
	s_lshr_b32 s21, s20, 1
	s_and_b32 s20, s20, 1
	s_waitcnt lgkmcnt(14)
	v_mfma_f32_32x32x16_f16 v[0:15], v[44:47], v[140:143], v[0:15]
	ds_read_b128 v[140:143], v239 offset:28672
	s_add_i32 s21, s21, s15
	s_lshl_b32 s21, s21, 15
	s_lshl_b32 s20, s20, 11
	s_add_i32 s21, s21, s20
	s_waitcnt lgkmcnt(14)
	v_mfma_f32_32x32x16_f16 v[0:15], v[48:51], v[144:147], v[0:15]
	ds_read_b128 v[144:147], v239 offset:29696
	s_add_u32 s26, s26, s21
	s_addc_u32 s27, s27, 0
	s_waitcnt lgkmcnt(14)
	v_mfma_f32_32x32x16_f16 v[0:15], v[52:55], v[148:151], v[0:15]
	ds_read_b128 v[148:151], v239 offset:30720
	v_cvt_pk_f16_f32 v244, v220, v221
	v_cvt_pk_f16_f32 v245, v222, v223
	s_waitcnt lgkmcnt(14)
	v_mfma_f32_32x32x16_f16 v[0:15], v[56:59], v[152:155], v[0:15]
	ds_read_b128 v[152:155], v239 offset:31744
	v_cvt_pk_f16_f32 v246, v224, v225
	v_cvt_pk_f16_f32 v247, v226, v227
	s_waitcnt lgkmcnt(14)
	v_mfma_f32_32x32x16_f16 v[0:15], v[60:63], v[156:159], v[0:15]
	ds_read_b128 v[156:159], v239 offset:32768
	v_cvt_pk_f16_f32 v248, v228, v229
	v_cvt_pk_f16_f32 v249, v230, v231
	s_waitcnt lgkmcnt(14)
	v_mfma_f32_32x32x16_f16 v[0:15], v[64:67], v[160:163], v[0:15]
	ds_read_b128 v[160:163], v239 offset:33792
	v_cvt_pk_f16_f32 v250, v232, v233
	v_cvt_pk_f16_f32 v251, v234, v235
	s_waitcnt lgkmcnt(14)
	v_mfma_f32_32x32x16_f16 v[0:15], v[68:71], v[164:167], v[0:15]
	ds_read_b128 v[164:167], v239 offset:34816
	global_store_dwordx4 v241, v[244:247], s[26:27] nt
	s_waitcnt lgkmcnt(14)
	v_mfma_f32_32x32x16_f16 v[0:15], v[72:75], v[168:171], v[0:15]
	ds_read_b128 v[168:171], v239 offset:35840
	global_store_dwordx4 v241, v[248:251], s[26:27] offset:1024 nt
	s_waitcnt lgkmcnt(14)
	v_mfma_f32_32x32x16_f16 v[0:15], v[76:79], v[172:175], v[0:15]
	ds_read_b128 v[172:175], v239 offset:36864
	s_waitcnt lgkmcnt(14)
	v_mfma_f32_32x32x16_f16 v[0:15], v[80:83], v[176:179], v[0:15]
	ds_read_b128 v[176:179], v239 offset:37888
	s_waitcnt lgkmcnt(14)
	v_mfma_f32_32x32x16_f16 v[0:15], v[84:87], v[180:183], v[0:15]
	ds_read_b128 v[180:183], v239 offset:38912
	s_waitcnt lgkmcnt(14)
	v_mfma_f32_32x32x16_f16 v[0:15], v[88:91], v[184:187], v[0:15]
	ds_read_b128 v[184:187], v239 offset:39936
	s_waitcnt lgkmcnt(14)
	v_mfma_f32_32x32x16_f16 v[0:15], v[92:95], v[188:191], v[0:15]
	ds_read_b128 v[188:191], v239 offset:40960
	s_waitcnt lgkmcnt(14)
	v_mfma_f32_32x32x16_f16 v[0:15], v[96:99], v[192:195], v[0:15]
	ds_read_b128 v[192:195], v239 offset:41984
	s_waitcnt lgkmcnt(14)
	v_mfma_f32_32x32x16_f16 v[0:15], v[100:103], v[196:199], v[0:15]
	ds_read_b128 v[196:199], v239 offset:43008
	s_waitcnt vmcnt(2)
	ds_write_b128 v236, v[16:19] offset:49152
	ds_write_b128 v237, v[20:23] offset:49152
	ds_write_b128 v238, v[24:27] offset:49152
	s_waitcnt lgkmcnt(14)
	v_mfma_f32_32x32x16_f16 v[0:15], v[104:107], v[200:203], v[0:15]
	ds_read_b128 v[200:203], v239 offset:44032
	s_waitcnt lgkmcnt(14)
	v_mfma_f32_32x32x16_f16 v[0:15], v[108:111], v[204:207], v[0:15]
	ds_read_b128 v[204:207], v239 offset:45056
	s_waitcnt lgkmcnt(14)
	v_mfma_f32_32x32x16_f16 v[0:15], v[112:115], v[208:211], v[0:15]
	ds_read_b128 v[208:211], v239 offset:46080
	s_waitcnt lgkmcnt(14)
	v_mfma_f32_32x32x16_f16 v[0:15], v[116:119], v[212:215], v[0:15]
	ds_read_b128 v[212:215], v239 offset:47104
	s_waitcnt lgkmcnt(14)
	v_mfma_f32_32x32x16_f16 v[0:15], v[120:123], v[216:219], v[0:15]
	ds_read_b128 v[216:219], v239 offset:48128
	s_waitcnt lgkmcnt(5)
	s_barrier
	s_waitcnt lgkmcnt(14)
	v_mfma_f32_32x32x16_f16 v[220:235], v[28:31], v[124:127], 0
	ds_read_b128 v[124:127], v240 offset:0
	s_waitcnt lgkmcnt(14)
	v_mfma_f32_32x32x16_f16 v[220:235], v[32:35], v[128:131], v[220:235]
	ds_read_b128 v[128:131], v240 offset:1024
	s_add_i32 s20, s14, 6
	s_cmp_lt_u32 s20, 12
	s_cselect_b32 s26, s8, s10
	s_cselect_b32 s27, s9, s11
	s_waitcnt lgkmcnt(14)
	v_mfma_f32_32x32x16_f16 v[220:235], v[36:39], v[132:135], v[220:235]
	ds_read_b128 v[132:135], v240 offset:2048
	s_cselect_b32 s21, 0, 12
	s_cmp_lt_u32 s20, 24
	s_cselect_b32 s26, s26, s0
	s_cselect_b32 s27, s27, s1
	s_waitcnt lgkmcnt(14)
	v_mfma_f32_32x32x16_f16 v[220:235], v[40:43], v[136:139], v[220:235]
	ds_read_b128 v[136:139], v240 offset:3072
	s_cselect_b32 s21, s21, 24
	s_sub_i32 s20, s20, s21
	s_lshr_b32 s21, s20, 1
	s_and_b32 s20, s20, 1
	s_waitcnt lgkmcnt(14)
	v_mfma_f32_32x32x16_f16 v[220:235], v[44:47], v[140:143], v[220:235]
	ds_read_b128 v[140:143], v240 offset:4096
	s_add_i32 s21, s21, s15
	s_lshl_b32 s21, s21, 15
	s_lshl_b32 s20, s20, 11
	s_add_i32 s21, s21, s20
	s_waitcnt lgkmcnt(14)
	v_mfma_f32_32x32x16_f16 v[220:235], v[48:51], v[144:147], v[220:235]
	ds_read_b128 v[144:147], v240 offset:5120
	s_add_u32 s26, s26, s21
	s_addc_u32 s27, s27, 0
	s_waitcnt lgkmcnt(14)
	v_mfma_f32_32x32x16_f16 v[220:235], v[52:55], v[148:151], v[220:235]
	ds_read_b128 v[148:151], v240 offset:6144
	v_cvt_pk_f16_f32 v244, v0, v1
	v_cvt_pk_f16_f32 v245, v2, v3
	s_waitcnt lgkmcnt(14)
	v_mfma_f32_32x32x16_f16 v[220:235], v[56:59], v[152:155], v[220:235]
	ds_read_b128 v[152:155], v240 offset:7168
	v_cvt_pk_f16_f32 v246, v4, v5
	v_cvt_pk_f16_f32 v247, v6, v7
	s_waitcnt lgkmcnt(14)
	v_mfma_f32_32x32x16_f16 v[220:235], v[60:63], v[156:159], v[220:235]
	ds_read_b128 v[156:159], v240 offset:8192
	v_cvt_pk_f16_f32 v248, v8, v9
	v_cvt_pk_f16_f32 v249, v10, v11
	s_waitcnt lgkmcnt(14)
	v_mfma_f32_32x32x16_f16 v[220:235], v[64:67], v[160:163], v[220:235]
	ds_read_b128 v[160:163], v240 offset:9216
	v_cvt_pk_f16_f32 v250, v12, v13
	v_cvt_pk_f16_f32 v251, v14, v15
	s_waitcnt lgkmcnt(14)
	v_mfma_f32_32x32x16_f16 v[220:235], v[68:71], v[164:167], v[220:235]
	ds_read_b128 v[164:167], v240 offset:10240
	global_store_dwordx4 v241, v[244:247], s[26:27] nt
	s_waitcnt lgkmcnt(14)
	v_mfma_f32_32x32x16_f16 v[220:235], v[72:75], v[168:171], v[220:235]
	ds_read_b128 v[168:171], v240 offset:11264
	global_store_dwordx4 v241, v[248:251], s[26:27] offset:1024 nt
	s_waitcnt lgkmcnt(14)
	v_mfma_f32_32x32x16_f16 v[220:235], v[76:79], v[172:175], v[220:235]
	ds_read_b128 v[172:175], v240 offset:12288
	s_waitcnt lgkmcnt(14)
	v_mfma_f32_32x32x16_f16 v[220:235], v[80:83], v[176:179], v[220:235]
	ds_read_b128 v[176:179], v240 offset:13312
	s_waitcnt lgkmcnt(14)
	v_mfma_f32_32x32x16_f16 v[220:235], v[84:87], v[180:183], v[220:235]
	ds_read_b128 v[180:183], v240 offset:14336
	s_waitcnt lgkmcnt(14)
	v_mfma_f32_32x32x16_f16 v[220:235], v[88:91], v[184:187], v[220:235]
	ds_read_b128 v[184:187], v240 offset:15360
	s_waitcnt lgkmcnt(14)
	v_mfma_f32_32x32x16_f16 v[220:235], v[92:95], v[188:191], v[220:235]
	ds_read_b128 v[188:191], v240 offset:16384
	s_waitcnt lgkmcnt(14)
	v_mfma_f32_32x32x16_f16 v[220:235], v[96:99], v[192:195], v[220:235]
	ds_read_b128 v[192:195], v240 offset:17408
	s_waitcnt lgkmcnt(14)
	v_mfma_f32_32x32x16_f16 v[220:235], v[100:103], v[196:199], v[220:235]
	ds_read_b128 v[196:199], v240 offset:18432
	s_waitcnt lgkmcnt(14)
	v_mfma_f32_32x32x16_f16 v[220:235], v[104:107], v[200:203], v[220:235]
	ds_read_b128 v[200:203], v240 offset:19456
	s_waitcnt lgkmcnt(14)
	v_mfma_f32_32x32x16_f16 v[220:235], v[108:111], v[204:207], v[220:235]
	ds_read_b128 v[204:207], v240 offset:20480
	s_waitcnt lgkmcnt(14)
	v_mfma_f32_32x32x16_f16 v[220:235], v[112:115], v[208:211], v[220:235]
	ds_read_b128 v[208:211], v240 offset:21504
	s_waitcnt lgkmcnt(14)
	v_mfma_f32_32x32x16_f16 v[220:235], v[116:119], v[212:215], v[220:235]
	ds_read_b128 v[212:215], v240 offset:22528
	s_waitcnt lgkmcnt(14)
	v_mfma_f32_32x32x16_f16 v[220:235], v[120:123], v[216:219], v[220:235]
	ds_read_b128 v[216:219], v240 offset:23552
	s_waitcnt lgkmcnt(14)
	v_mfma_f32_32x32x16_f16 v[0:15], v[28:31], v[124:127], 0
	s_waitcnt lgkmcnt(14)
	v_mfma_f32_32x32x16_f16 v[0:15], v[32:35], v[128:131], v[0:15]
	s_add_i32 s20, s14, 7
	s_cmp_lt_u32 s20, 12
	s_cselect_b32 s26, s8, s10
	s_cselect_b32 s27, s9, s11
	s_waitcnt lgkmcnt(14)
	v_mfma_f32_32x32x16_f16 v[0:15], v[36:39], v[132:135], v[0:15]
	s_cselect_b32 s21, 0, 12
	s_cmp_lt_u32 s20, 24
	s_cselect_b32 s26, s26, s0
	s_cselect_b32 s27, s27, s1
	s_waitcnt lgkmcnt(14)
	v_mfma_f32_32x32x16_f16 v[0:15], v[40:43], v[136:139], v[0:15]
	s_cselect_b32 s21, s21, 24
	s_sub_i32 s20, s20, s21
	s_lshr_b32 s21, s20, 1
	s_and_b32 s20, s20, 1
	s_waitcnt lgkmcnt(14)
	v_mfma_f32_32x32x16_f16 v[0:15], v[44:47], v[140:143], v[0:15]
	s_add_i32 s21, s21, s15
	s_lshl_b32 s21, s21, 15
	s_lshl_b32 s20, s20, 11
	s_add_i32 s21, s21, s20
	s_waitcnt lgkmcnt(14)
	v_mfma_f32_32x32x16_f16 v[0:15], v[48:51], v[144:147], v[0:15]
	s_add_u32 s26, s26, s21
	s_addc_u32 s27, s27, 0
	s_waitcnt lgkmcnt(14)
	v_mfma_f32_32x32x16_f16 v[0:15], v[52:55], v[148:151], v[0:15]
	v_cvt_pk_f16_f32 v244, v220, v221
	v_cvt_pk_f16_f32 v245, v222, v223
	s_waitcnt lgkmcnt(14)
	v_mfma_f32_32x32x16_f16 v[0:15], v[56:59], v[152:155], v[0:15]
	v_cvt_pk_f16_f32 v246, v224, v225
	v_cvt_pk_f16_f32 v247, v226, v227
	s_waitcnt lgkmcnt(14)
	v_mfma_f32_32x32x16_f16 v[0:15], v[60:63], v[156:159], v[0:15]
	v_cvt_pk_f16_f32 v248, v228, v229
	v_cvt_pk_f16_f32 v249, v230, v231
	s_waitcnt lgkmcnt(14)
	v_mfma_f32_32x32x16_f16 v[0:15], v[64:67], v[160:163], v[0:15]
	v_cvt_pk_f16_f32 v250, v232, v233
	v_cvt_pk_f16_f32 v251, v234, v235
	s_waitcnt lgkmcnt(13)
	v_mfma_f32_32x32x16_f16 v[0:15], v[68:71], v[164:167], v[0:15]
	global_store_dwordx4 v241, v[244:247], s[26:27] nt
	s_waitcnt lgkmcnt(12)
	v_mfma_f32_32x32x16_f16 v[0:15], v[72:75], v[168:171], v[0:15]
	global_store_dwordx4 v241, v[248:251], s[26:27] offset:1024 nt
	s_waitcnt lgkmcnt(11)
	v_mfma_f32_32x32x16_f16 v[0:15], v[76:79], v[172:175], v[0:15]
	s_waitcnt lgkmcnt(10)
	v_mfma_f32_32x32x16_f16 v[0:15], v[80:83], v[176:179], v[0:15]
	s_waitcnt lgkmcnt(9)
	v_mfma_f32_32x32x16_f16 v[0:15], v[84:87], v[180:183], v[0:15]
	s_waitcnt lgkmcnt(8)
	v_mfma_f32_32x32x16_f16 v[0:15], v[88:91], v[184:187], v[0:15]
	s_waitcnt lgkmcnt(7)
	v_mfma_f32_32x32x16_f16 v[0:15], v[92:95], v[188:191], v[0:15]
	s_waitcnt lgkmcnt(6)
	v_mfma_f32_32x32x16_f16 v[0:15], v[96:99], v[192:195], v[0:15]
	s_waitcnt lgkmcnt(5)
	v_mfma_f32_32x32x16_f16 v[0:15], v[100:103], v[196:199], v[0:15]
	s_waitcnt lgkmcnt(4)
	v_mfma_f32_32x32x16_f16 v[0:15], v[104:107], v[200:203], v[0:15]
	s_waitcnt lgkmcnt(3)
	v_mfma_f32_32x32x16_f16 v[0:15], v[108:111], v[204:207], v[0:15]
	s_waitcnt lgkmcnt(2)
	v_mfma_f32_32x32x16_f16 v[0:15], v[112:115], v[208:211], v[0:15]
	s_waitcnt lgkmcnt(1)
	v_mfma_f32_32x32x16_f16 v[0:15], v[116:119], v[212:215], v[0:15]
	s_waitcnt lgkmcnt(0)
	v_mfma_f32_32x32x16_f16 v[0:15], v[120:123], v[216:219], v[0:15]
	s_add_i32 s20, s14, 8
	s_cmp_lt_u32 s20, 12
	s_cselect_b32 s26, s8, s10
	s_cselect_b32 s27, s9, s11
	s_cselect_b32 s21, 0, 12
	s_cmp_lt_u32 s20, 24
	s_cselect_b32 s26, s26, s0
	s_cselect_b32 s27, s27, s1
	s_cselect_b32 s21, s21, 24
	s_sub_i32 s20, s20, s21
	s_lshr_b32 s21, s20, 1
	s_and_b32 s20, s20, 1
	s_add_i32 s21, s21, s15
	s_lshl_b32 s21, s21, 15
	s_lshl_b32 s20, s20, 11
	s_add_i32 s21, s21, s20
	s_add_u32 s26, s26, s21
	s_addc_u32 s27, s27, 0
	s_nop 7
	v_cvt_pk_f16_f32 v244, v0, v1
	v_cvt_pk_f16_f32 v245, v2, v3
	v_cvt_pk_f16_f32 v246, v4, v5
	v_cvt_pk_f16_f32 v247, v6, v7
	v_cvt_pk_f16_f32 v248, v8, v9
	v_cvt_pk_f16_f32 v249, v10, v11
	v_cvt_pk_f16_f32 v250, v12, v13
	v_cvt_pk_f16_f32 v251, v14, v15
	global_store_dwordx4 v241, v[244:247], s[26:27] nt
	global_store_dwordx4 v241, v[248:251], s[26:27] offset:1024 nt
	s_endpgm

	.amdhsa_kernel _Z10qkv_kernelPKfPK15HIP_vector_typeIjLj4EEPDv8_DF16_S6_S6_
		.amdhsa_group_segment_fixed_size 86016
		.amdhsa_private_segment_fixed_size 0
		.amdhsa_kernarg_size 40
		.amdhsa_user_sgpr_count 2
		.amdhsa_user_sgpr_dispatch_ptr 0
		.amdhsa_user_sgpr_queue_ptr 0
		.amdhsa_user_sgpr_kernarg_segment_ptr 1
		.amdhsa_user_sgpr_dispatch_id 0
		.amdhsa_user_sgpr_kernarg_preload_length 0
		.amdhsa_user_sgpr_kernarg_preload_offset 0
		.amdhsa_user_sgpr_private_segment_size 0
		.amdhsa_uses_dynamic_stack 0
		.amdhsa_enable_private_segment 0
		.amdhsa_system_sgpr_workgroup_id_x 1
		.amdhsa_system_sgpr_workgroup_id_y 0
		.amdhsa_system_sgpr_workgroup_id_z 0
		.amdhsa_system_sgpr_workgroup_info 0
		.amdhsa_system_vgpr_workitem_id 0
		.amdhsa_next_free_vgpr 252
		.amdhsa_next_free_sgpr 96
		.amdhsa_accum_offset 252
		.amdhsa_reserve_vcc 1
		.amdhsa_float_round_mode_32 0
		.amdhsa_float_round_mode_16_64 0
		.amdhsa_float_denorm_mode_32 3
		.amdhsa_float_denorm_mode_16_64 3
		.amdhsa_dx10_clamp 1
		.amdhsa_ieee_mode 1
		.amdhsa_fp16_overflow 0
		.amdhsa_tg_split 0
		.amdhsa_exception_fp_ieee_invalid_op 0
		.amdhsa_exception_fp_denorm_src 0
		.amdhsa_exception_fp_ieee_div_zero 0
		.amdhsa_exception_fp_ieee_overflow 0
		.amdhsa_exception_fp_ieee_underflow 0
		.amdhsa_exception_fp_ieee_inexact 0
		.amdhsa_exception_int_div_zero 0
	.end_amdhsa_kernel

amdhsa.kernels:
  - .agpr_count:     0
    .args:
      - .actual_access:  read_only
        .address_space:  global
        .offset:         0
        .size:           8
        .value_kind:     global_buffer
      - .actual_access:  read_only
        .address_space:  global
        .offset:         8
        .size:           8
        .value_kind:     global_buffer
      - .actual_access:  read_only
        .address_space:  global
        .offset:         16
        .size:           8
        .value_kind:     global_buffer
      - .actual_access:  read_only
        .address_space:  global
        .offset:         24
        .size:           8
        .value_kind:     global_buffer
      - .actual_access:  write_only
        .address_space:  global
        .offset:         32
        .size:           8
        .value_kind:     global_buffer
      - .actual_access:  write_only
        .address_space:  global
        .offset:         40
        .size:           8
        .value_kind:     global_buffer
    .group_segment_fixed_size: 0
    .kernarg_segment_align: 8
    .kernarg_segment_size: 48
    .language:       OpenCL C
    .language_version:
      - 2
      - 0
    .max_flat_workgroup_size: 64
    .name:           _Z11prep_kernelPKfS0_S0_S0_PDv8_DF16_S2_
    .private_segment_fixed_size: 0
    .sgpr_count:     19
    .sgpr_spill_count: 0
    .symbol:         _Z11prep_kernelPKfS0_S0_S0_PDv8_DF16_S2_.kd
    .uniform_work_group_size: 1
    .uses_dynamic_stack: false
    .vgpr_count:     26
    .vgpr_spill_count: 0
    .wavefront_size: 64
  - .agpr_count:     0
    .args:
      - .actual_access:  read_only
        .address_space:  global
        .offset:         0
        .size:           8
        .value_kind:     global_buffer
      - .actual_access:  read_only
        .address_space:  global
        .offset:         8
        .size:           8
        .value_kind:     global_buffer
      - .actual_access:  write_only
        .address_space:  global
        .offset:         16
        .size:           8
        .value_kind:     global_buffer
      - .actual_access:  write_only
        .address_space:  global
        .offset:         24
        .size:           8
        .value_kind:     global_buffer
      - .actual_access:  write_only
        .address_space:  global
        .offset:         32
        .size:           8
        .value_kind:     global_buffer
    .group_segment_fixed_size: 86016
    .kernarg_segment_align: 8
    .kernarg_segment_size: 40
    .language:       OpenCL C
    .language_version:
      - 2
      - 0
    .max_flat_workgroup_size: 512
    .name:           _Z10qkv_kernelPKfPK15HIP_vector_typeIjLj4EEPDv8_DF16_S6_S6_
    .private_segment_fixed_size: 0
    .sgpr_count:     28
    .sgpr_spill_count: 0
    .symbol:         _Z10qkv_kernelPKfPK15HIP_vector_typeIjLj4EEPDv8_DF16_S6_S6_.kd
    .uniform_work_group_size: 1
    .uses_dynamic_stack: false
    .vgpr_count:     252
    .vgpr_spill_count: 0
    .wavefront_size: 64
  - .agpr_count:     0
    .args:
      - .actual_access:  read_only
        .address_space:  global
        .offset:         0
        .size:           8
        .value_kind:     global_buffer
      - .actual_access:  read_only
        .address_space:  global
        .offset:         8
        .size:           8
        .value_kind:     global_buffer
      - .actual_access:  read_only
        .address_space:  global
        .offset:         16
        .size:           8
        .value_kind:     global_buffer
      - .actual_access:  read_only
        .address_space:  global
        .offset:         24
        .size:           8
        .value_kind:     global_buffer
      - .actual_access:  read_only
        .address_space:  global
        .offset:         32
        .size:           8
        .value_kind:     global_buffer
      - .actual_access:  write_only
        .address_space:  global
        .offset:         40
        .size:           8
        .value_kind:     global_buffer
    .group_segment_fixed_size: 101376
    .kernarg_segment_align: 8
    .kernarg_segment_size: 48
    .language:       OpenCL C
    .language_version:
      - 2
      - 0
    .max_flat_workgroup_size: 768
    .name:           _Z15attn_out_kernelPKDv8_DF16_S1_S1_S1_PKfPf
    .private_segment_fixed_size: 0
    .sgpr_count:     62
    .sgpr_spill_count: 0
    .symbol:         _Z15attn_out_kernelPKDv8_DF16_S1_S1_S1_PKfPf.kd
    .uniform_work_group_size: 1
    .uses_dynamic_stack: false
    .vgpr_count:     158
    .vgpr_spill_count: 0
    .wavefront_size: 64
